# v027 with every s_setprio around the K-loop MFMA blocks removed (all phases at priority 0)
# speedup vs baseline: 1.0360x; 1.0027x over previous
; #define PG8_STAGE(bufoff, gbase, voff) do { _Pragma("unroll") for (int _i = 0; _i < 2; ++_i) \
;         __builtin_amdgcn_global_load_lds((const unsigned*)((const char*)(gbase) + (voff)[_i]), (LAS unsigned*)(lds + (bufoff) + ldsw + _i * 8192), 16, 0, 0); } while (0)
; #define PG8_LDA(dst, b, h) do { _Pragma("unroll") for (int m = 0; m < 4; ++m) _Pragma("unroll") for (int k = 0; k < 2; ++k) dst[m][k] = *(const LAS bf16x8*)(lds + PG8_SA(b, h) + ((aoff ^ (k * 64)) + m * 2048)); } while (0)
; #define PG8_LDB(dst, b, h) do { _Pragma("unroll") for (int n = 0; n < 2; ++n) _Pragma("unroll") for (int k = 0; k < 2; ++k) dst[n][k] = *(const LAS bf16x8*)(lds + PG8_SB(b, h) + ((boff ^ (k * 64)) + n * 2048)); } while (0)
; #define PG8_MMA(ai, bj, At, Bt) do { __builtin_amdgcn_s_setprio(1); _Pragma("unroll") for (int m = 0; m < 4; ++m) _Pragma("unroll") for (int n = 0; n < 2; ++n) _Pragma("unroll") for (int k = 0; k < 2; ++k) \
;         acc[ai][bj][m][n] = __builtin_amdgcn_mfma_f32_16x16x32_bf16(Bt[n][k], At[m][k], acc[ai][bj][m][n], 0, 0, 0); __builtin_amdgcn_s_setprio(0); } while (0)
; #define PG8_WAIT_V(n) asm volatile("s_waitcnt vmcnt(" #n ")" ::: "memory")
; #define PG8_WAIT_L(n) asm volatile("s_waitcnt lgkmcnt(" #n ")" ::: "memory")
; #define PG8_BAR __builtin_amdgcn_s_barrier()
; #define PG8_SCHED __builtin_amdgcn_sched_barrier(0)
;     ...
;             PG8_LDB(B0, 0, 0); PG8_LDB(B1, 0, 1); PG8_SCHED; PG8_LDA(At, 0, 0); PG8_STAGE(PG8_SA(1, 1), a1, voffA[1]);
;             PG8_WAIT_V(8); PG8_WAIT_L(0); PG8_BAR; if (do0) { PG8_MMA(0, 0, At, B0); PG8_MMA(0, 1, At, B1); } PG8_BAR; PG8_SCHED;
;             PG8_LDA(At, 0, 1); PG8_STAGE(PG8_SB(0, 0), b2, voffB); PG8_STAGE(PG8_SB(0, 1), b2 + hstep, voffB); PG8_STAGE(PG8_SA(0, 0), a2, vs[0]);
;             PG8_WAIT_V(8); PG8_WAIT_L(0); PG8_BAR; if (do1) { PG8_MMA(1, 0, At, B0); PG8_MMA(1, 1, At, B1); } PG8_BAR; PG8_SCHED;
.LBB0_192:
	ds_read_b128 v[158:161], v166
	ds_read_b128 v[180:183], v167
	ds_read_b128 v[184:187], v168
	ds_read_b128 v[188:191], v169
	ds_read_b128 v[192:195], v170
	ds_read_b128 v[200:203], v171
	ds_read_b128 v[204:207], v172
	ds_read_b128 v[208:211], v173
	s_add_u32 s28, s4, 0x80
	s_addc_u32 s29, s5, 0
	s_cmp_eq_u32 s64, 12
	s_cselect_b32 s35, s17, s29
	s_cselect_b32 s34, s60, s28
	s_cselect_b32 s29, s19, s63
	s_cselect_b32 s28, s61, s62
	v_lshl_add_u64 v[162:163], s[4:5], 0, v[152:153]
	s_add_i32 m0, s25, 0xc000
	ds_read_b128 v[212:215], v174
	ds_read_b128 v[216:219], v174 offset:2048
	ds_read_b128 v[220:223], v175
	ds_read_b128 v[224:227], v175 offset:2048
	ds_read_b128 v[228:231], v174 offset:4096
	ds_read_b128 v[232:235], v174 offset:6144
	ds_read_b128 v[236:239], v175 offset:4096
	ds_read_b128 v[240:243], v175 offset:6144
	global_load_lds_dwordx4 v[162:163], off
	v_lshl_add_u64 v[162:163], s[4:5], 0, v[150:151]
	s_add_i32 m0, s25, 0xe000
	s_add_u32 s30, s28, 0x4000
	global_load_lds_dwordx4 v[162:163], off
	s_waitcnt vmcnt(8)
	s_waitcnt lgkmcnt(0)
	s_addc_u32 s31, s29, 0
	s_barrier
	s_waitcnt lgkmcnt(0)
	v_mfma_f32_16x16x32_bf16 v[126:129], v[158:161], v[212:215], v[126:129]
	v_mfma_f32_16x16x32_bf16 v[122:125], v[184:187], v[212:215], v[122:125]
	v_mfma_f32_16x16x32_bf16 v[110:113], v[158:161], v[216:219], v[110:113]
	v_mfma_f32_16x16x32_bf16 v[106:109], v[184:187], v[216:219], v[106:109]
	v_mfma_f32_16x16x32_bf16 v[94:97], v[158:161], v[228:231], v[94:97]
	v_mfma_f32_16x16x32_bf16 v[90:93], v[184:187], v[228:231], v[90:93]
	v_mfma_f32_16x16x32_bf16 v[78:81], v[158:161], v[232:235], v[78:81]
	v_mfma_f32_16x16x32_bf16 v[74:77], v[184:187], v[232:235], v[74:77]
	v_mfma_f32_16x16x32_bf16 v[126:129], v[180:183], v[220:223], v[126:129]
	v_mfma_f32_16x16x32_bf16 v[122:125], v[188:191], v[220:223], v[122:125]
	v_mfma_f32_16x16x32_bf16 v[110:113], v[180:183], v[224:227], v[110:113]
	v_mfma_f32_16x16x32_bf16 v[106:109], v[188:191], v[224:227], v[106:109]
	v_mfma_f32_16x16x32_bf16 v[94:97], v[180:183], v[236:239], v[94:97]
	v_mfma_f32_16x16x32_bf16 v[90:93], v[188:191], v[236:239], v[90:93]
	v_mfma_f32_16x16x32_bf16 v[78:81], v[180:183], v[240:243], v[78:81]
	v_mfma_f32_16x16x32_bf16 v[74:77], v[188:191], v[240:243], v[74:77]
	v_mfma_f32_16x16x32_bf16 v[118:121], v[192:195], v[212:215], v[118:121]
	v_mfma_f32_16x16x32_bf16 v[114:117], v[204:207], v[212:215], v[114:117]
	v_mfma_f32_16x16x32_bf16 v[102:105], v[192:195], v[216:219], v[102:105]
	v_mfma_f32_16x16x32_bf16 v[98:101], v[204:207], v[216:219], v[98:101]
	v_mfma_f32_16x16x32_bf16 v[86:89], v[192:195], v[228:231], v[86:89]
	v_mfma_f32_16x16x32_bf16 v[82:85], v[204:207], v[228:231], v[82:85]
	v_mfma_f32_16x16x32_bf16 v[70:73], v[192:195], v[232:235], v[70:73]
	v_mfma_f32_16x16x32_bf16 v[66:69], v[204:207], v[232:235], v[66:69]
	v_mfma_f32_16x16x32_bf16 v[118:121], v[200:203], v[220:223], v[118:121]
	v_mfma_f32_16x16x32_bf16 v[114:117], v[208:211], v[220:223], v[114:117]
	v_mfma_f32_16x16x32_bf16 v[102:105], v[200:203], v[224:227], v[102:105]
	v_mfma_f32_16x16x32_bf16 v[98:101], v[208:211], v[224:227], v[98:101]
	v_mfma_f32_16x16x32_bf16 v[86:89], v[200:203], v[236:239], v[86:89]
	v_mfma_f32_16x16x32_bf16 v[82:85], v[208:211], v[236:239], v[82:85]
	v_mfma_f32_16x16x32_bf16 v[70:73], v[200:203], v[240:243], v[70:73]
	v_mfma_f32_16x16x32_bf16 v[66:69], v[208:211], v[240:243], v[66:69]
	s_barrier
	s_add_i32 s65, s56, s37
	v_lshl_add_u64 v[162:163], s[28:29], 0, v[130:131]
	s_mov_b32 m0, s65
	ds_read_b128 v[212:215], v174 offset:16384
	ds_read_b128 v[216:219], v174 offset:18432
	ds_read_b128 v[220:223], v175 offset:16384
	ds_read_b128 v[224:227], v175 offset:18432
	ds_read_b128 v[228:231], v174 offset:20480
	ds_read_b128 v[232:235], v174 offset:22528
	ds_read_b128 v[236:239], v175 offset:20480
	ds_read_b128 v[240:243], v175 offset:22528
	global_load_lds_dwordx4 v[162:163], off
	s_add_i32 m0, s65, 0x2000
	s_add_u32 s66, s28, 0x40000
	v_lshl_add_u64 v[162:163], s[28:29], 0, v[132:133]
	s_addc_u32 s67, s29, 0
	s_add_i32 s65, s57, s37
	global_load_lds_dwordx4 v[162:163], off
	v_lshl_add_u64 v[162:163], s[66:67], 0, v[130:131]
	s_mov_b32 m0, s65
	v_lshl_add_u64 v[196:197], s[34:35], 0, v[136:137]
	global_load_lds_dwordx4 v[162:163], off
	v_lshl_add_u64 v[162:163], s[66:67], 0, v[132:133]
	s_add_i32 m0, s65, 0x2000
	s_nop 0
	global_load_lds_dwordx4 v[162:163], off
	v_lshl_add_u64 v[162:163], s[34:35], 0, v[134:135]
	s_mov_b32 m0, s25
	s_nop 0
	global_load_lds_dwordx4 v[162:163], off
	s_mov_b32 m0, s27
	s_nop 0
	global_load_lds_dwordx4 v[196:197], off
	s_waitcnt vmcnt(8)
	s_waitcnt lgkmcnt(0)
	s_barrier
; #define PG8_STAGE(bufoff, gbase, voff) do { _Pragma("unroll") for (int _i = 0; _i < 2; ++_i) \
;         __builtin_amdgcn_global_load_lds((const unsigned*)((const char*)(gbase) + (voff)[_i]), (LAS unsigned*)(lds + (bufoff) + ldsw + _i * 8192), 16, 0, 0); } while (0)
; #define PG8_LDA(dst, b, h) do { _Pragma("unroll") for (int m = 0; m < 4; ++m) _Pragma("unroll") for (int k = 0; k < 2; ++k) dst[m][k] = *(const LAS bf16x8*)(lds + PG8_SA(b, h) + ((aoff ^ (k * 64)) + m * 2048)); } while (0)
; #define PG8_LDB(dst, b, h) do { _Pragma("unroll") for (int n = 0; n < 2; ++n) _Pragma("unroll") for (int k = 0; k < 2; ++k) dst[n][k] = *(const LAS bf16x8*)(lds + PG8_SB(b, h) + ((boff ^ (k * 64)) + n * 2048)); } while (0)
; #define PG8_MMA(ai, bj, At, Bt) do { __builtin_amdgcn_s_setprio(1); _Pragma("unroll") for (int m = 0; m < 4; ++m) _Pragma("unroll") for (int n = 0; n < 2; ++n) _Pragma("unroll") for (int k = 0; k < 2; ++k) \
;         acc[ai][bj][m][n] = __builtin_amdgcn_mfma_f32_16x16x32_bf16(Bt[n][k], At[m][k], acc[ai][bj][m][n], 0, 0, 0); __builtin_amdgcn_s_setprio(0); } while (0)
; #define PG8_WAIT_V(n) asm volatile("s_waitcnt vmcnt(" #n ")" ::: "memory")
; #define PG8_WAIT_L(n) asm volatile("s_waitcnt lgkmcnt(" #n ")" ::: "memory")
; #define PG8_BAR __builtin_amdgcn_s_barrier()
; #define PG8_SCHED __builtin_amdgcn_sched_barrier(0)
;     ...
;             PG8_WAIT_V(8); PG8_WAIT_L(0); PG8_BAR; if (do1) { PG8_MMA(1, 0, At, B0); PG8_MMA(1, 1, At, B1); } PG8_BAR; PG8_SCHED;
;             PG8_LDB(B0, 1, 0); PG8_LDB(B1, 1, 1); PG8_SCHED; PG8_LDA(At, 1, 0); PG8_STAGE(PG8_SA(0, 1), a2, vs[1]);
;             PG8_WAIT_V(8); PG8_WAIT_L(0); PG8_BAR; if (do0) { PG8_MMA(0, 0, At, B0); PG8_MMA(0, 1, At, B1); } PG8_BAR; PG8_SCHED;
	s_waitcnt lgkmcnt(0)
	v_mfma_f32_16x16x32_bf16 v[62:65], v[158:161], v[212:215], v[62:65]
	v_mfma_f32_16x16x32_bf16 v[58:61], v[184:187], v[212:215], v[58:61]
	v_mfma_f32_16x16x32_bf16 v[46:49], v[158:161], v[216:219], v[46:49]
	v_mfma_f32_16x16x32_bf16 v[42:45], v[184:187], v[216:219], v[42:45]
	v_mfma_f32_16x16x32_bf16 v[30:33], v[158:161], v[228:231], v[30:33]
	v_mfma_f32_16x16x32_bf16 v[26:29], v[184:187], v[228:231], v[26:29]
	v_mfma_f32_16x16x32_bf16 v[14:17], v[158:161], v[232:235], v[14:17]
	v_mfma_f32_16x16x32_bf16 v[10:13], v[184:187], v[232:235], v[10:13]
	v_mfma_f32_16x16x32_bf16 v[62:65], v[180:183], v[220:223], v[62:65]
	v_mfma_f32_16x16x32_bf16 v[58:61], v[188:191], v[220:223], v[58:61]
	v_mfma_f32_16x16x32_bf16 v[46:49], v[180:183], v[224:227], v[46:49]
	v_mfma_f32_16x16x32_bf16 v[42:45], v[188:191], v[224:227], v[42:45]
	v_mfma_f32_16x16x32_bf16 v[30:33], v[180:183], v[236:239], v[30:33]
	v_mfma_f32_16x16x32_bf16 v[26:29], v[188:191], v[236:239], v[26:29]
	v_mfma_f32_16x16x32_bf16 v[14:17], v[180:183], v[240:243], v[14:17]
	v_mfma_f32_16x16x32_bf16 v[10:13], v[188:191], v[240:243], v[10:13]
	v_mfma_f32_16x16x32_bf16 v[54:57], v[192:195], v[212:215], v[54:57]
	v_mfma_f32_16x16x32_bf16 v[50:53], v[204:207], v[212:215], v[50:53]
	v_mfma_f32_16x16x32_bf16 v[38:41], v[192:195], v[216:219], v[38:41]
	v_mfma_f32_16x16x32_bf16 v[34:37], v[204:207], v[216:219], v[34:37]
	v_mfma_f32_16x16x32_bf16 v[22:25], v[192:195], v[228:231], v[22:25]
	v_mfma_f32_16x16x32_bf16 v[18:21], v[204:207], v[228:231], v[18:21]
	v_mfma_f32_16x16x32_bf16 v[6:9], v[192:195], v[232:235], v[6:9]
	v_mfma_f32_16x16x32_bf16 v[2:5], v[204:207], v[232:235], v[2:5]
	v_mfma_f32_16x16x32_bf16 v[54:57], v[200:203], v[220:223], v[54:57]
	v_mfma_f32_16x16x32_bf16 v[50:53], v[208:211], v[220:223], v[50:53]
	v_mfma_f32_16x16x32_bf16 v[38:41], v[200:203], v[224:227], v[38:41]
	v_mfma_f32_16x16x32_bf16 v[34:37], v[208:211], v[224:227], v[34:37]
	v_mfma_f32_16x16x32_bf16 v[22:25], v[200:203], v[236:239], v[22:25]
	v_mfma_f32_16x16x32_bf16 v[18:21], v[208:211], v[236:239], v[18:21]
	v_mfma_f32_16x16x32_bf16 v[6:9], v[200:203], v[240:243], v[6:9]
	v_mfma_f32_16x16x32_bf16 v[2:5], v[208:211], v[240:243], v[2:5]
	s_barrier
	s_add_i32 s65, 0, 0x18000
	v_add_u32_e32 v142, s65, v145
	v_add_u32_e32 v180, s65, v165
	s_add_i32 s66, 0, 0x1c000
	ds_read_b128 v[158:161], v142
	ds_read_b128 v[180:183], v180
	ds_read_b128 v[184:187], v176
	ds_read_b128 v[188:191], v177
	v_add_u32_e32 v142, s66, v145
	v_add_u32_e32 v199, s66, v165
	ds_read_b128 v[192:195], v142
	ds_read_b128 v[200:203], v199
	ds_read_b128 v[204:207], v178
	ds_read_b128 v[208:211], v179
	s_mov_b32 m0, s38
	v_lshl_add_u64 v[244:245], s[34:35], 0, v[138:139]
	ds_read_b128 v[212:215], v174 offset:32768
	ds_read_b128 v[216:219], v174 offset:34816
	ds_read_b128 v[220:223], v175 offset:32768
	ds_read_b128 v[224:227], v175 offset:34816
	ds_read_b128 v[228:231], v174 offset:36864
	ds_read_b128 v[232:235], v174 offset:38912
	ds_read_b128 v[236:239], v175 offset:36864
	ds_read_b128 v[240:243], v175 offset:38912
	global_load_lds_dwordx4 v[244:245], off
	v_lshl_add_u64 v[244:245], s[34:35], 0, v[140:141]
	s_mov_b32 m0, s39
	s_nop 0
	global_load_lds_dwordx4 v[244:245], off
	s_waitcnt vmcnt(8)
	s_waitcnt lgkmcnt(0)
	s_barrier
	s_waitcnt lgkmcnt(0)
	v_mfma_f32_16x16x32_bf16 v[126:129], v[158:161], v[212:215], v[126:129]
	v_mfma_f32_16x16x32_bf16 v[122:125], v[184:187], v[212:215], v[122:125]
	v_mfma_f32_16x16x32_bf16 v[110:113], v[158:161], v[216:219], v[110:113]
	v_mfma_f32_16x16x32_bf16 v[106:109], v[184:187], v[216:219], v[106:109]
	v_mfma_f32_16x16x32_bf16 v[94:97], v[158:161], v[228:231], v[94:97]
	v_mfma_f32_16x16x32_bf16 v[90:93], v[184:187], v[228:231], v[90:93]
	v_mfma_f32_16x16x32_bf16 v[78:81], v[158:161], v[232:235], v[78:81]
	v_mfma_f32_16x16x32_bf16 v[74:77], v[184:187], v[232:235], v[74:77]
	v_mfma_f32_16x16x32_bf16 v[126:129], v[180:183], v[220:223], v[126:129]
	v_mfma_f32_16x16x32_bf16 v[122:125], v[188:191], v[220:223], v[122:125]
	v_mfma_f32_16x16x32_bf16 v[110:113], v[180:183], v[224:227], v[110:113]
	v_mfma_f32_16x16x32_bf16 v[106:109], v[188:191], v[224:227], v[106:109]
	v_mfma_f32_16x16x32_bf16 v[94:97], v[180:183], v[236:239], v[94:97]
	v_mfma_f32_16x16x32_bf16 v[90:93], v[188:191], v[236:239], v[90:93]
	v_mfma_f32_16x16x32_bf16 v[78:81], v[180:183], v[240:243], v[78:81]
	v_mfma_f32_16x16x32_bf16 v[74:77], v[188:191], v[240:243], v[74:77]
	v_mfma_f32_16x16x32_bf16 v[118:121], v[192:195], v[212:215], v[118:121]
	v_mfma_f32_16x16x32_bf16 v[114:117], v[204:207], v[212:215], v[114:117]
	v_mfma_f32_16x16x32_bf16 v[102:105], v[192:195], v[216:219], v[102:105]
	v_mfma_f32_16x16x32_bf16 v[98:101], v[204:207], v[216:219], v[98:101]
	v_mfma_f32_16x16x32_bf16 v[86:89], v[192:195], v[228:231], v[86:89]
	v_mfma_f32_16x16x32_bf16 v[82:85], v[204:207], v[228:231], v[82:85]
	v_mfma_f32_16x16x32_bf16 v[70:73], v[192:195], v[232:235], v[70:73]
	v_mfma_f32_16x16x32_bf16 v[66:69], v[204:207], v[232:235], v[66:69]
	v_mfma_f32_16x16x32_bf16 v[118:121], v[200:203], v[220:223], v[118:121]
	v_mfma_f32_16x16x32_bf16 v[114:117], v[208:211], v[220:223], v[114:117]
	v_mfma_f32_16x16x32_bf16 v[102:105], v[200:203], v[224:227], v[102:105]
	v_mfma_f32_16x16x32_bf16 v[98:101], v[208:211], v[224:227], v[98:101]
	v_mfma_f32_16x16x32_bf16 v[86:89], v[200:203], v[236:239], v[86:89]
	v_mfma_f32_16x16x32_bf16 v[82:85], v[208:211], v[236:239], v[82:85]
	v_mfma_f32_16x16x32_bf16 v[70:73], v[200:203], v[240:243], v[70:73]
	v_mfma_f32_16x16x32_bf16 v[66:69], v[208:211], v[240:243], v[66:69]
	s_barrier
; #define PG8_STAGE(bufoff, gbase, voff) do { _Pragma("unroll") for (int _i = 0; _i < 2; ++_i) \
;         __builtin_amdgcn_global_load_lds((const unsigned*)((const char*)(gbase) + (voff)[_i]), (LAS unsigned*)(lds + (bufoff) + ldsw + _i * 8192), 16, 0, 0); } while (0)
; #define PG8_LDA(dst, b, h) do { _Pragma("unroll") for (int m = 0; m < 4; ++m) _Pragma("unroll") for (int k = 0; k < 2; ++k) dst[m][k] = *(const LAS bf16x8*)(lds + PG8_SA(b, h) + ((aoff ^ (k * 64)) + m * 2048)); } while (0)
; #define PG8_MMA(ai, bj, At, Bt) do { __builtin_amdgcn_s_setprio(1); _Pragma("unroll") for (int m = 0; m < 4; ++m) _Pragma("unroll") for (int n = 0; n < 2; ++n) _Pragma("unroll") for (int k = 0; k < 2; ++k) \
;         acc[ai][bj][m][n] = __builtin_amdgcn_mfma_f32_16x16x32_bf16(Bt[n][k], At[m][k], acc[ai][bj][m][n], 0, 0, 0); __builtin_amdgcn_s_setprio(0); } while (0)
; #define PG8_WAIT_V(n) asm volatile("s_waitcnt vmcnt(" #n ")" ::: "memory")
; #define PG8_WAIT_L(n) asm volatile("s_waitcnt lgkmcnt(" #n ")" ::: "memory")
; #define PG8_BAR __builtin_amdgcn_s_barrier()
; #define PG8_SCHED __builtin_amdgcn_sched_barrier(0)
;     ...
;             PG8_LDA(At, 1, 1); PG8_STAGE(PG8_SB(1, 0), b3, voffB); PG8_STAGE(PG8_SB(1, 1), b3 + hstep, voffB); PG8_STAGE(PG8_SA(1, 0), a3, vs[0]);
;             PG8_WAIT_V(8); PG8_WAIT_L(0); PG8_BAR; if (do1) { PG8_MMA(1, 0, At, B0); PG8_MMA(1, 1, At, B1); } PG8_BAR; PG8_SCHED;
;         }
;         if (wr == 0) PG8_BAR;
	s_add_i32 s34, s65, s37
	v_lshl_add_u64 v[244:245], s[30:31], 0, v[130:131]
	s_mov_b32 m0, s34
	ds_read_b128 v[212:215], v174 offset:49152
	ds_read_b128 v[216:219], v174 offset:51200
	ds_read_b128 v[220:223], v175 offset:49152
	ds_read_b128 v[224:227], v175 offset:51200
	ds_read_b128 v[228:231], v174 offset:53248
	ds_read_b128 v[232:235], v174 offset:55296
	ds_read_b128 v[236:239], v175 offset:53248
	ds_read_b128 v[240:243], v175 offset:55296
	global_load_lds_dwordx4 v[244:245], off
	s_add_i32 m0, s34, 0x2000
	s_add_u32 s28, s28, 0x44000
	v_lshl_add_u64 v[244:245], s[30:31], 0, v[132:133]
	s_addc_u32 s29, s29, 0
	s_add_i32 s30, s66, s37
	global_load_lds_dwordx4 v[244:245], off
	v_lshl_add_u64 v[244:245], s[28:29], 0, v[130:131]
	s_mov_b32 m0, s30
	v_lshl_add_u64 v[162:163], v[162:163], 0, s[8:9]
	global_load_lds_dwordx4 v[244:245], off
	v_lshl_add_u64 v[244:245], s[28:29], 0, v[132:133]
	s_add_i32 m0, s30, 0x2000
	s_nop 0
	global_load_lds_dwordx4 v[244:245], off
	s_mov_b32 m0, s51
	s_nop 0
	global_load_lds_dwordx4 v[162:163], off
	v_lshl_add_u64 v[162:163], v[196:197], 0, s[8:9]
	s_mov_b32 m0, s54
	s_nop 0
	global_load_lds_dwordx4 v[162:163], off
	s_waitcnt vmcnt(8)
	s_waitcnt lgkmcnt(0)
	s_barrier
	s_waitcnt lgkmcnt(0)
	v_mfma_f32_16x16x32_bf16 v[62:65], v[158:161], v[212:215], v[62:65]
	v_mfma_f32_16x16x32_bf16 v[58:61], v[184:187], v[212:215], v[58:61]
	v_mfma_f32_16x16x32_bf16 v[46:49], v[158:161], v[216:219], v[46:49]
	v_mfma_f32_16x16x32_bf16 v[42:45], v[184:187], v[216:219], v[42:45]
	v_mfma_f32_16x16x32_bf16 v[30:33], v[158:161], v[228:231], v[30:33]
	v_mfma_f32_16x16x32_bf16 v[26:29], v[184:187], v[228:231], v[26:29]
	v_mfma_f32_16x16x32_bf16 v[14:17], v[158:161], v[232:235], v[14:17]
	v_mfma_f32_16x16x32_bf16 v[10:13], v[184:187], v[232:235], v[10:13]
	v_mfma_f32_16x16x32_bf16 v[62:65], v[180:183], v[220:223], v[62:65]
	v_mfma_f32_16x16x32_bf16 v[58:61], v[188:191], v[220:223], v[58:61]
	v_mfma_f32_16x16x32_bf16 v[46:49], v[180:183], v[224:227], v[46:49]
	v_mfma_f32_16x16x32_bf16 v[42:45], v[188:191], v[224:227], v[42:45]
	v_mfma_f32_16x16x32_bf16 v[30:33], v[180:183], v[236:239], v[30:33]
	v_mfma_f32_16x16x32_bf16 v[26:29], v[188:191], v[236:239], v[26:29]
	v_mfma_f32_16x16x32_bf16 v[14:17], v[180:183], v[240:243], v[14:17]
	v_mfma_f32_16x16x32_bf16 v[10:13], v[188:191], v[240:243], v[10:13]
	v_mfma_f32_16x16x32_bf16 v[54:57], v[192:195], v[212:215], v[54:57]
	v_mfma_f32_16x16x32_bf16 v[50:53], v[204:207], v[212:215], v[50:53]
	v_mfma_f32_16x16x32_bf16 v[38:41], v[192:195], v[216:219], v[38:41]
	v_mfma_f32_16x16x32_bf16 v[34:37], v[204:207], v[216:219], v[34:37]
	v_mfma_f32_16x16x32_bf16 v[22:25], v[192:195], v[228:231], v[22:25]
	v_mfma_f32_16x16x32_bf16 v[18:21], v[204:207], v[228:231], v[18:21]
	v_mfma_f32_16x16x32_bf16 v[6:9], v[192:195], v[232:235], v[6:9]
	v_mfma_f32_16x16x32_bf16 v[2:5], v[204:207], v[232:235], v[2:5]
	v_mfma_f32_16x16x32_bf16 v[54:57], v[200:203], v[220:223], v[54:57]
	v_mfma_f32_16x16x32_bf16 v[50:53], v[208:211], v[220:223], v[50:53]
	v_mfma_f32_16x16x32_bf16 v[38:41], v[200:203], v[224:227], v[38:41]
	v_mfma_f32_16x16x32_bf16 v[34:37], v[208:211], v[224:227], v[34:37]
	v_mfma_f32_16x16x32_bf16 v[22:25], v[200:203], v[236:239], v[22:25]
	v_mfma_f32_16x16x32_bf16 v[18:21], v[208:211], v[236:239], v[18:21]
	v_mfma_f32_16x16x32_bf16 v[6:9], v[200:203], v[240:243], v[6:9]
	v_mfma_f32_16x16x32_bf16 v[2:5], v[208:211], v[240:243], v[2:5]
	s_barrier
	s_add_i32 s64, s64, 2
	s_add_u32 s62, s62, 0x8000
	s_addc_u32 s63, s63, 0
	s_add_u32 s4, s4, 0x100
	s_addc_u32 s5, s5, 0
	s_cmp_gt_u32 s64, 13
	s_cbranch_scc0 .LBB0_192
	s_and_b64 vcc, exec, s[12:13]
	s_cbranch_vccz .LBB0_195
	s_barrier

; #define PG8_STAGE(bufoff, gbase, voff) do { _Pragma("unroll") for (int _i = 0; _i < 2; ++_i) \
;         __builtin_amdgcn_global_load_lds((const unsigned*)((const char*)(gbase) + (voff)[_i]), (LAS unsigned*)(lds + (bufoff) + ldsw + _i * 8192), 16, 0, 0); } while (0)
; #define PG8_LDA(dst, b, h) do { _Pragma("unroll") for (int m = 0; m < 4; ++m) _Pragma("unroll") for (int k = 0; k < 2; ++k) dst[m][k] = *(const LAS bf16x8*)(lds + PG8_SA(b, h) + ((aoff ^ (k * 64)) + m * 2048)); } while (0)
; #define PG8_LDB(dst, b, h) do { _Pragma("unroll") for (int n = 0; n < 2; ++n) _Pragma("unroll") for (int k = 0; k < 2; ++k) dst[n][k] = *(const LAS bf16x8*)(lds + PG8_SB(b, h) + ((boff ^ (k * 64)) + n * 2048)); } while (0)
; #define PG8_MMA(ai, bj, At, Bt) do { __builtin_amdgcn_s_setprio(1); _Pragma("unroll") for (int m = 0; m < 4; ++m) _Pragma("unroll") for (int n = 0; n < 2; ++n) _Pragma("unroll") for (int k = 0; k < 2; ++k) \
;         acc[ai][bj][m][n] = __builtin_amdgcn_mfma_f32_16x16x32_bf16(Bt[n][k], At[m][k], acc[ai][bj][m][n], 0, 0, 0); __builtin_amdgcn_s_setprio(0); } while (0)
; #define PG8_WAIT_V(n) asm volatile("s_waitcnt vmcnt(" #n ")" ::: "memory")
; #define PG8_WAIT_L(n) asm volatile("s_waitcnt lgkmcnt(" #n ")" ::: "memory")
; #define PG8_BAR __builtin_amdgcn_s_barrier()
; #define PG8_SCHED __builtin_amdgcn_sched_barrier(0)
;     ...
;             PG8_LDB(B0, 0, 0); PG8_LDB(B1, 0, 1); PG8_SCHED; PG8_LDA(At, 0, 0); PG8_STAGE(PG8_SA(1, 1), a1, voffA[1]);
;             PG8_WAIT_V(8); PG8_WAIT_L(0); PG8_BAR; if (do0) { PG8_MMA(0, 0, At, B0); PG8_MMA(0, 1, At, B1); } PG8_BAR; PG8_SCHED;
;             PG8_LDA(At, 0, 1); PG8_STAGE(PG8_SB(0, 0), b2, voffB); PG8_STAGE(PG8_SB(0, 1), b2 + hstep, voffB); PG8_STAGE(PG8_SA(0, 0), a2, vs[0]);
;             PG8_WAIT_V(8); PG8_WAIT_L(0); PG8_BAR; if (do1) { PG8_MMA(1, 0, At, B0); PG8_MMA(1, 1, At, B1); } PG8_BAR; PG8_SCHED;
.LBB0_212:
	ds_read_b128 v[168:171], v153
	ds_read_b128 v[172:175], v154
	ds_read_b128 v[176:179], v155
	ds_read_b128 v[180:183], v156
	ds_read_b128 v[184:187], v157
	ds_read_b128 v[188:191], v158
	ds_read_b128 v[192:195], v159
	ds_read_b128 v[200:203], v160
	s_add_u32 s30, s4, 0x4000
	s_addc_u32 s31, s5, 0
	s_cmp_eq_u32 s64, 12
	s_cselect_b32 s36, s29, s30
	s_cselect_b32 s37, s17, s31
	s_cselect_b32 s34, s61, s62
	s_cselect_b32 s35, s19, s63
	s_add_u32 s30, s36, 0x4000
	s_addc_u32 s31, s37, 0
	v_lshl_add_u64 v[196:197], s[4:5], 0, v[148:149]
	s_add_i32 m0, s27, 0xc000
	ds_read_b128 v[204:207], v161
	ds_read_b128 v[208:211], v161 offset:2048
	ds_read_b128 v[212:215], v162
	ds_read_b128 v[216:219], v162 offset:2048
	ds_read_b128 v[220:223], v161 offset:4096
	ds_read_b128 v[224:227], v161 offset:6144
	ds_read_b128 v[228:231], v162 offset:4096
	ds_read_b128 v[232:235], v162 offset:6144
	global_load_lds_dwordx4 v[196:197], off
	v_lshl_add_u64 v[196:197], s[4:5], 0, v[150:151]
	s_add_i32 m0, s27, 0xe000
	s_nop 0
	global_load_lds_dwordx4 v[196:197], off
	s_waitcnt vmcnt(8)
	s_waitcnt lgkmcnt(0)
	s_barrier
	s_waitcnt lgkmcnt(0)
	v_mfma_f32_16x16x32_bf16 v[126:129], v[168:171], v[204:207], v[126:129]
	v_mfma_f32_16x16x32_bf16 v[122:125], v[176:179], v[204:207], v[122:125]
	v_mfma_f32_16x16x32_bf16 v[110:113], v[168:171], v[208:211], v[110:113]
	v_mfma_f32_16x16x32_bf16 v[106:109], v[176:179], v[208:211], v[106:109]
	v_mfma_f32_16x16x32_bf16 v[94:97], v[168:171], v[220:223], v[94:97]
	v_mfma_f32_16x16x32_bf16 v[90:93], v[176:179], v[220:223], v[90:93]
	v_mfma_f32_16x16x32_bf16 v[78:81], v[168:171], v[224:227], v[78:81]
	v_mfma_f32_16x16x32_bf16 v[74:77], v[176:179], v[224:227], v[74:77]
	v_mfma_f32_16x16x32_bf16 v[126:129], v[172:175], v[212:215], v[126:129]
	v_mfma_f32_16x16x32_bf16 v[122:125], v[180:183], v[212:215], v[122:125]
	v_mfma_f32_16x16x32_bf16 v[110:113], v[172:175], v[216:219], v[110:113]
	v_mfma_f32_16x16x32_bf16 v[106:109], v[180:183], v[216:219], v[106:109]
	v_mfma_f32_16x16x32_bf16 v[94:97], v[172:175], v[228:231], v[94:97]
	v_mfma_f32_16x16x32_bf16 v[90:93], v[180:183], v[228:231], v[90:93]
	v_mfma_f32_16x16x32_bf16 v[78:81], v[172:175], v[232:235], v[78:81]
	v_mfma_f32_16x16x32_bf16 v[74:77], v[180:183], v[232:235], v[74:77]
	v_mfma_f32_16x16x32_bf16 v[118:121], v[184:187], v[204:207], v[118:121]
	v_mfma_f32_16x16x32_bf16 v[114:117], v[192:195], v[204:207], v[114:117]
	v_mfma_f32_16x16x32_bf16 v[102:105], v[184:187], v[208:211], v[102:105]
	v_mfma_f32_16x16x32_bf16 v[98:101], v[192:195], v[208:211], v[98:101]
	v_mfma_f32_16x16x32_bf16 v[86:89], v[184:187], v[220:223], v[86:89]
	v_mfma_f32_16x16x32_bf16 v[82:85], v[192:195], v[220:223], v[82:85]
	v_mfma_f32_16x16x32_bf16 v[70:73], v[184:187], v[224:227], v[70:73]
	v_mfma_f32_16x16x32_bf16 v[66:69], v[192:195], v[224:227], v[66:69]
	v_mfma_f32_16x16x32_bf16 v[118:121], v[188:191], v[212:215], v[118:121]
	v_mfma_f32_16x16x32_bf16 v[114:117], v[200:203], v[212:215], v[114:117]
	v_mfma_f32_16x16x32_bf16 v[102:105], v[188:191], v[216:219], v[102:105]
	v_mfma_f32_16x16x32_bf16 v[98:101], v[200:203], v[216:219], v[98:101]
	v_mfma_f32_16x16x32_bf16 v[86:89], v[188:191], v[228:231], v[86:89]
	v_mfma_f32_16x16x32_bf16 v[82:85], v[200:203], v[228:231], v[82:85]
	v_mfma_f32_16x16x32_bf16 v[70:73], v[188:191], v[232:235], v[70:73]
	v_mfma_f32_16x16x32_bf16 v[66:69], v[200:203], v[232:235], v[66:69]
	s_barrier
	s_add_i32 s65, s58, s39
	v_lshl_add_u64 v[196:197], s[34:35], 0, v[132:133]
	s_mov_b32 m0, s65
	ds_read_b128 v[204:207], v161 offset:16384
	ds_read_b128 v[208:211], v161 offset:18432
	ds_read_b128 v[212:215], v162 offset:16384
	ds_read_b128 v[216:219], v162 offset:18432
	ds_read_b128 v[220:223], v161 offset:20480
	ds_read_b128 v[224:227], v161 offset:22528
	ds_read_b128 v[228:231], v162 offset:20480
	ds_read_b128 v[232:235], v162 offset:22528
	global_load_lds_dwordx4 v[196:197], off
	s_add_i32 m0, s65, 0x2000
	s_add_u32 s66, s34, 0x40000
	v_lshl_add_u64 v[236:237], s[34:35], 0, v[130:131]
	s_addc_u32 s67, s35, 0
	s_add_i32 s65, s59, s39
	global_load_lds_dwordx4 v[236:237], off
	v_lshl_add_u64 v[238:239], s[66:67], 0, v[132:133]
	s_mov_b32 m0, s65
	s_nop 0
	global_load_lds_dwordx4 v[238:239], off
	v_lshl_add_u64 v[238:239], s[66:67], 0, v[130:131]
	s_add_i32 m0, s65, 0x2000
	s_nop 0
	global_load_lds_dwordx4 v[238:239], off
	v_lshl_add_u64 v[238:239], s[36:37], 0, v[134:135]
	s_mov_b32 m0, s27
	s_nop 0
	global_load_lds_dwordx4 v[238:239], off
	v_lshl_add_u64 v[238:239], s[36:37], 0, v[136:137]
	s_mov_b32 m0, s48
	s_nop 0
	global_load_lds_dwordx4 v[238:239], off
	s_waitcnt vmcnt(8)
	s_waitcnt lgkmcnt(0)
	s_barrier
; #define PG8_STAGE(bufoff, gbase, voff) do { _Pragma("unroll") for (int _i = 0; _i < 2; ++_i) \
;         __builtin_amdgcn_global_load_lds((const unsigned*)((const char*)(gbase) + (voff)[_i]), (LAS unsigned*)(lds + (bufoff) + ldsw + _i * 8192), 16, 0, 0); } while (0)
; #define PG8_LDA(dst, b, h) do { _Pragma("unroll") for (int m = 0; m < 4; ++m) _Pragma("unroll") for (int k = 0; k < 2; ++k) dst[m][k] = *(const LAS bf16x8*)(lds + PG8_SA(b, h) + ((aoff ^ (k * 64)) + m * 2048)); } while (0)
; #define PG8_LDB(dst, b, h) do { _Pragma("unroll") for (int n = 0; n < 2; ++n) _Pragma("unroll") for (int k = 0; k < 2; ++k) dst[n][k] = *(const LAS bf16x8*)(lds + PG8_SB(b, h) + ((boff ^ (k * 64)) + n * 2048)); } while (0)
; #define PG8_MMA(ai, bj, At, Bt) do { __builtin_amdgcn_s_setprio(1); _Pragma("unroll") for (int m = 0; m < 4; ++m) _Pragma("unroll") for (int n = 0; n < 2; ++n) _Pragma("unroll") for (int k = 0; k < 2; ++k) \
;         acc[ai][bj][m][n] = __builtin_amdgcn_mfma_f32_16x16x32_bf16(Bt[n][k], At[m][k], acc[ai][bj][m][n], 0, 0, 0); __builtin_amdgcn_s_setprio(0); } while (0)
; #define PG8_WAIT_V(n) asm volatile("s_waitcnt vmcnt(" #n ")" ::: "memory")
; #define PG8_WAIT_L(n) asm volatile("s_waitcnt lgkmcnt(" #n ")" ::: "memory")
; #define PG8_BAR __builtin_amdgcn_s_barrier()
; #define PG8_SCHED __builtin_amdgcn_sched_barrier(0)
;     ...
;             PG8_WAIT_V(8); PG8_WAIT_L(0); PG8_BAR; if (do1) { PG8_MMA(1, 0, At, B0); PG8_MMA(1, 1, At, B1); } PG8_BAR; PG8_SCHED;
;             PG8_LDB(B0, 1, 0); PG8_LDB(B1, 1, 1); PG8_SCHED; PG8_LDA(At, 1, 0); PG8_STAGE(PG8_SA(0, 1), a2, vs[1]);
;             PG8_WAIT_V(8); PG8_WAIT_L(0); PG8_BAR; if (do0) { PG8_MMA(0, 0, At, B0); PG8_MMA(0, 1, At, B1); } PG8_BAR; PG8_SCHED;
	s_waitcnt lgkmcnt(0)
	v_mfma_f32_16x16x32_bf16 v[62:65], v[168:171], v[204:207], v[62:65]
	v_mfma_f32_16x16x32_bf16 v[58:61], v[176:179], v[204:207], v[58:61]
	v_mfma_f32_16x16x32_bf16 v[46:49], v[168:171], v[208:211], v[46:49]
	v_mfma_f32_16x16x32_bf16 v[42:45], v[176:179], v[208:211], v[42:45]
	v_mfma_f32_16x16x32_bf16 v[30:33], v[168:171], v[220:223], v[30:33]
	v_mfma_f32_16x16x32_bf16 v[26:29], v[176:179], v[220:223], v[26:29]
	v_mfma_f32_16x16x32_bf16 v[14:17], v[168:171], v[224:227], v[14:17]
	v_mfma_f32_16x16x32_bf16 v[10:13], v[176:179], v[224:227], v[10:13]
	v_mfma_f32_16x16x32_bf16 v[62:65], v[172:175], v[212:215], v[62:65]
	v_mfma_f32_16x16x32_bf16 v[58:61], v[180:183], v[212:215], v[58:61]
	v_mfma_f32_16x16x32_bf16 v[46:49], v[172:175], v[216:219], v[46:49]
	v_mfma_f32_16x16x32_bf16 v[42:45], v[180:183], v[216:219], v[42:45]
	v_mfma_f32_16x16x32_bf16 v[30:33], v[172:175], v[228:231], v[30:33]
	v_mfma_f32_16x16x32_bf16 v[26:29], v[180:183], v[228:231], v[26:29]
	v_mfma_f32_16x16x32_bf16 v[14:17], v[172:175], v[232:235], v[14:17]
	v_mfma_f32_16x16x32_bf16 v[10:13], v[180:183], v[232:235], v[10:13]
	v_mfma_f32_16x16x32_bf16 v[54:57], v[184:187], v[204:207], v[54:57]
	v_mfma_f32_16x16x32_bf16 v[50:53], v[192:195], v[204:207], v[50:53]
	v_mfma_f32_16x16x32_bf16 v[38:41], v[184:187], v[208:211], v[38:41]
	v_mfma_f32_16x16x32_bf16 v[34:37], v[192:195], v[208:211], v[34:37]
	v_mfma_f32_16x16x32_bf16 v[22:25], v[184:187], v[220:223], v[22:25]
	v_mfma_f32_16x16x32_bf16 v[18:21], v[192:195], v[220:223], v[18:21]
	v_mfma_f32_16x16x32_bf16 v[6:9], v[184:187], v[224:227], v[6:9]
	v_mfma_f32_16x16x32_bf16 v[2:5], v[192:195], v[224:227], v[2:5]
	v_mfma_f32_16x16x32_bf16 v[54:57], v[188:191], v[212:215], v[54:57]
	v_mfma_f32_16x16x32_bf16 v[50:53], v[200:203], v[212:215], v[50:53]
	v_mfma_f32_16x16x32_bf16 v[38:41], v[188:191], v[216:219], v[38:41]
	v_mfma_f32_16x16x32_bf16 v[34:37], v[200:203], v[216:219], v[34:37]
	v_mfma_f32_16x16x32_bf16 v[22:25], v[188:191], v[228:231], v[22:25]
	v_mfma_f32_16x16x32_bf16 v[18:21], v[200:203], v[228:231], v[18:21]
	v_mfma_f32_16x16x32_bf16 v[6:9], v[188:191], v[232:235], v[6:9]
	v_mfma_f32_16x16x32_bf16 v[2:5], v[200:203], v[232:235], v[2:5]
	s_barrier
	s_add_i32 s65, 0, 0x18000
	v_add_u32_e32 v167, s65, v143
	v_add_u32_e32 v172, s65, v152
	s_add_i32 s66, 0, 0x1c000
	ds_read_b128 v[168:171], v167
	ds_read_b128 v[172:175], v172
	ds_read_b128 v[176:179], v163
	ds_read_b128 v[180:183], v164
	v_add_u32_e32 v167, s66, v143
	v_add_u32_e32 v188, s66, v152
	ds_read_b128 v[184:187], v167
	ds_read_b128 v[188:191], v188
	ds_read_b128 v[192:195], v165
	ds_read_b128 v[200:203], v166
	s_mov_b32 m0, s49
	v_lshl_add_u64 v[238:239], s[36:37], 0, v[138:139]
	ds_read_b128 v[204:207], v161 offset:32768
	ds_read_b128 v[208:211], v161 offset:34816
	ds_read_b128 v[212:215], v162 offset:32768
	ds_read_b128 v[216:219], v162 offset:34816
	ds_read_b128 v[220:223], v161 offset:36864
	ds_read_b128 v[224:227], v161 offset:38912
	ds_read_b128 v[228:231], v162 offset:36864
	ds_read_b128 v[232:235], v162 offset:38912
	global_load_lds_dwordx4 v[238:239], off
	v_lshl_add_u64 v[238:239], s[36:37], 0, v[140:141]
	s_mov_b32 m0, s50
	s_nop 0
	global_load_lds_dwordx4 v[238:239], off
	s_waitcnt vmcnt(8)
	s_waitcnt lgkmcnt(0)
	s_barrier
	s_waitcnt lgkmcnt(0)
	v_mfma_f32_16x16x32_bf16 v[126:129], v[168:171], v[204:207], v[126:129]
	v_mfma_f32_16x16x32_bf16 v[122:125], v[176:179], v[204:207], v[122:125]
	v_mfma_f32_16x16x32_bf16 v[110:113], v[168:171], v[208:211], v[110:113]
	v_mfma_f32_16x16x32_bf16 v[106:109], v[176:179], v[208:211], v[106:109]
	v_mfma_f32_16x16x32_bf16 v[94:97], v[168:171], v[220:223], v[94:97]
	v_mfma_f32_16x16x32_bf16 v[90:93], v[176:179], v[220:223], v[90:93]
	v_mfma_f32_16x16x32_bf16 v[78:81], v[168:171], v[224:227], v[78:81]
	v_mfma_f32_16x16x32_bf16 v[74:77], v[176:179], v[224:227], v[74:77]
	v_mfma_f32_16x16x32_bf16 v[126:129], v[172:175], v[212:215], v[126:129]
	v_mfma_f32_16x16x32_bf16 v[122:125], v[180:183], v[212:215], v[122:125]
	v_mfma_f32_16x16x32_bf16 v[110:113], v[172:175], v[216:219], v[110:113]
	v_mfma_f32_16x16x32_bf16 v[106:109], v[180:183], v[216:219], v[106:109]
	v_mfma_f32_16x16x32_bf16 v[94:97], v[172:175], v[228:231], v[94:97]
	v_mfma_f32_16x16x32_bf16 v[90:93], v[180:183], v[228:231], v[90:93]
	v_mfma_f32_16x16x32_bf16 v[78:81], v[172:175], v[232:235], v[78:81]
	v_mfma_f32_16x16x32_bf16 v[74:77], v[180:183], v[232:235], v[74:77]
	v_mfma_f32_16x16x32_bf16 v[118:121], v[184:187], v[204:207], v[118:121]
	v_mfma_f32_16x16x32_bf16 v[114:117], v[192:195], v[204:207], v[114:117]
	v_mfma_f32_16x16x32_bf16 v[102:105], v[184:187], v[208:211], v[102:105]
	v_mfma_f32_16x16x32_bf16 v[98:101], v[192:195], v[208:211], v[98:101]
	v_mfma_f32_16x16x32_bf16 v[86:89], v[184:187], v[220:223], v[86:89]
	v_mfma_f32_16x16x32_bf16 v[82:85], v[192:195], v[220:223], v[82:85]
	v_mfma_f32_16x16x32_bf16 v[70:73], v[184:187], v[224:227], v[70:73]
	v_mfma_f32_16x16x32_bf16 v[66:69], v[192:195], v[224:227], v[66:69]
	v_mfma_f32_16x16x32_bf16 v[118:121], v[188:191], v[212:215], v[118:121]
	v_mfma_f32_16x16x32_bf16 v[114:117], v[200:203], v[212:215], v[114:117]
	v_mfma_f32_16x16x32_bf16 v[102:105], v[188:191], v[216:219], v[102:105]
	v_mfma_f32_16x16x32_bf16 v[98:101], v[200:203], v[216:219], v[98:101]
	v_mfma_f32_16x16x32_bf16 v[86:89], v[188:191], v[228:231], v[86:89]
	v_mfma_f32_16x16x32_bf16 v[82:85], v[200:203], v[228:231], v[82:85]
	v_mfma_f32_16x16x32_bf16 v[70:73], v[188:191], v[232:235], v[70:73]
	v_mfma_f32_16x16x32_bf16 v[66:69], v[200:203], v[232:235], v[66:69]
	s_barrier
; #define PG8_STAGE(bufoff, gbase, voff) do { _Pragma("unroll") for (int _i = 0; _i < 2; ++_i) \
;         __builtin_amdgcn_global_load_lds((const unsigned*)((const char*)(gbase) + (voff)[_i]), (LAS unsigned*)(lds + (bufoff) + ldsw + _i * 8192), 16, 0, 0); } while (0)
; #define PG8_LDA(dst, b, h) do { _Pragma("unroll") for (int m = 0; m < 4; ++m) _Pragma("unroll") for (int k = 0; k < 2; ++k) dst[m][k] = *(const LAS bf16x8*)(lds + PG8_SA(b, h) + ((aoff ^ (k * 64)) + m * 2048)); } while (0)
; #define PG8_MMA(ai, bj, At, Bt) do { __builtin_amdgcn_s_setprio(1); _Pragma("unroll") for (int m = 0; m < 4; ++m) _Pragma("unroll") for (int n = 0; n < 2; ++n) _Pragma("unroll") for (int k = 0; k < 2; ++k) \
;         acc[ai][bj][m][n] = __builtin_amdgcn_mfma_f32_16x16x32_bf16(Bt[n][k], At[m][k], acc[ai][bj][m][n], 0, 0, 0); __builtin_amdgcn_s_setprio(0); } while (0)
; #define PG8_WAIT_V(n) asm volatile("s_waitcnt vmcnt(" #n ")" ::: "memory")
; #define PG8_WAIT_L(n) asm volatile("s_waitcnt lgkmcnt(" #n ")" ::: "memory")
; #define PG8_BAR __builtin_amdgcn_s_barrier()
; #define PG8_SCHED __builtin_amdgcn_sched_barrier(0)
;     ...
;             PG8_LDA(At, 1, 1); PG8_STAGE(PG8_SB(1, 0), b3, voffB); PG8_STAGE(PG8_SB(1, 1), b3 + hstep, voffB); PG8_STAGE(PG8_SA(1, 0), a3, vs[0]);
;             PG8_WAIT_V(8); PG8_WAIT_L(0); PG8_BAR; if (do1) { PG8_MMA(1, 0, At, B0); PG8_MMA(1, 1, At, B1); } PG8_BAR; PG8_SCHED;
;         }
;         if (wr == 0) PG8_BAR;
	s_add_i32 s36, s65, s39
	v_lshl_add_u64 v[196:197], v[196:197], 0, s[12:13]
	s_mov_b32 m0, s36
	ds_read_b128 v[204:207], v161 offset:49152
	ds_read_b128 v[208:211], v161 offset:51200
	ds_read_b128 v[212:215], v162 offset:49152
	ds_read_b128 v[216:219], v162 offset:51200
	ds_read_b128 v[220:223], v161 offset:53248
	ds_read_b128 v[224:227], v161 offset:55296
	ds_read_b128 v[228:231], v162 offset:53248
	ds_read_b128 v[232:235], v162 offset:55296
	global_load_lds_dwordx4 v[196:197], off
	s_add_i32 m0, s36, 0x2000
	s_add_u32 s34, s34, 0x40080
	v_lshl_add_u64 v[196:197], v[236:237], 0, s[12:13]
	s_addc_u32 s35, s35, 0
	s_add_i32 s36, s66, s39
	global_load_lds_dwordx4 v[196:197], off
	v_lshl_add_u64 v[196:197], s[34:35], 0, v[132:133]
	s_mov_b32 m0, s36
	s_nop 0
	global_load_lds_dwordx4 v[196:197], off
	v_lshl_add_u64 v[196:197], s[34:35], 0, v[130:131]
	s_add_i32 m0, s36, 0x2000
	s_nop 0
	global_load_lds_dwordx4 v[196:197], off
	v_lshl_add_u64 v[196:197], s[30:31], 0, v[134:135]
	s_mov_b32 m0, s55
	s_nop 0
	global_load_lds_dwordx4 v[196:197], off
	v_lshl_add_u64 v[196:197], s[30:31], 0, v[136:137]
	s_mov_b32 m0, s56
	s_nop 0
	global_load_lds_dwordx4 v[196:197], off
	s_waitcnt vmcnt(8)
	s_waitcnt lgkmcnt(0)
	s_barrier
	s_waitcnt lgkmcnt(0)
	v_mfma_f32_16x16x32_bf16 v[62:65], v[168:171], v[204:207], v[62:65]
	v_mfma_f32_16x16x32_bf16 v[58:61], v[176:179], v[204:207], v[58:61]
	v_mfma_f32_16x16x32_bf16 v[46:49], v[168:171], v[208:211], v[46:49]
	v_mfma_f32_16x16x32_bf16 v[42:45], v[176:179], v[208:211], v[42:45]
	v_mfma_f32_16x16x32_bf16 v[30:33], v[168:171], v[220:223], v[30:33]
	v_mfma_f32_16x16x32_bf16 v[26:29], v[176:179], v[220:223], v[26:29]
	v_mfma_f32_16x16x32_bf16 v[14:17], v[168:171], v[224:227], v[14:17]
	v_mfma_f32_16x16x32_bf16 v[10:13], v[176:179], v[224:227], v[10:13]
	v_mfma_f32_16x16x32_bf16 v[62:65], v[172:175], v[212:215], v[62:65]
	v_mfma_f32_16x16x32_bf16 v[58:61], v[180:183], v[212:215], v[58:61]
	v_mfma_f32_16x16x32_bf16 v[46:49], v[172:175], v[216:219], v[46:49]
	v_mfma_f32_16x16x32_bf16 v[42:45], v[180:183], v[216:219], v[42:45]
	v_mfma_f32_16x16x32_bf16 v[30:33], v[172:175], v[228:231], v[30:33]
	v_mfma_f32_16x16x32_bf16 v[26:29], v[180:183], v[228:231], v[26:29]
	v_mfma_f32_16x16x32_bf16 v[14:17], v[172:175], v[232:235], v[14:17]
	v_mfma_f32_16x16x32_bf16 v[10:13], v[180:183], v[232:235], v[10:13]
	v_mfma_f32_16x16x32_bf16 v[54:57], v[184:187], v[204:207], v[54:57]
	v_mfma_f32_16x16x32_bf16 v[50:53], v[192:195], v[204:207], v[50:53]
	v_mfma_f32_16x16x32_bf16 v[38:41], v[184:187], v[208:211], v[38:41]
	v_mfma_f32_16x16x32_bf16 v[34:37], v[192:195], v[208:211], v[34:37]
	v_mfma_f32_16x16x32_bf16 v[22:25], v[184:187], v[220:223], v[22:25]
	v_mfma_f32_16x16x32_bf16 v[18:21], v[192:195], v[220:223], v[18:21]
	v_mfma_f32_16x16x32_bf16 v[6:9], v[184:187], v[224:227], v[6:9]
	v_mfma_f32_16x16x32_bf16 v[2:5], v[192:195], v[224:227], v[2:5]
	v_mfma_f32_16x16x32_bf16 v[54:57], v[188:191], v[212:215], v[54:57]
	v_mfma_f32_16x16x32_bf16 v[50:53], v[200:203], v[212:215], v[50:53]
	v_mfma_f32_16x16x32_bf16 v[38:41], v[188:191], v[216:219], v[38:41]
	v_mfma_f32_16x16x32_bf16 v[34:37], v[200:203], v[216:219], v[34:37]
	v_mfma_f32_16x16x32_bf16 v[22:25], v[188:191], v[228:231], v[22:25]
	v_mfma_f32_16x16x32_bf16 v[18:21], v[200:203], v[228:231], v[18:21]
	v_mfma_f32_16x16x32_bf16 v[6:9], v[188:191], v[232:235], v[6:9]
	v_mfma_f32_16x16x32_bf16 v[2:5], v[200:203], v[232:235], v[2:5]
	s_barrier
	s_add_i32 s64, s64, 2
	s_add_u32 s62, s62, 0x100
	s_addc_u32 s63, s63, 0
	s_add_u32 s4, s4, 0x8000
	s_addc_u32 s5, s5, 0
	s_cmp_gt_u32 s64, 13
	s_cbranch_scc0 .LBB0_212
	s_and_b64 vcc, exec, s[14:15]
	s_cbranch_vccz .LBB0_215
	s_barrier

; #define PG8_STAGE(bufoff, gbase, voff) do { _Pragma("unroll") for (int _i = 0; _i < 2; ++_i) \
;         __builtin_amdgcn_global_load_lds((const unsigned*)((const char*)(gbase) + (voff)[_i]), (LAS unsigned*)(lds + (bufoff) + ldsw + _i * 8192), 16, 0, 0); } while (0)
; #define PG8_LDA(dst, b, h) do { _Pragma("unroll") for (int m = 0; m < 4; ++m) _Pragma("unroll") for (int k = 0; k < 2; ++k) dst[m][k] = *(const LAS bf16x8*)(lds + PG8_SA(b, h) + ((aoff ^ (k * 64)) + m * 2048)); } while (0)
; #define PG8_LDB(dst, b, h) do { _Pragma("unroll") for (int n = 0; n < 2; ++n) _Pragma("unroll") for (int k = 0; k < 2; ++k) dst[n][k] = *(const LAS bf16x8*)(lds + PG8_SB(b, h) + ((boff ^ (k * 64)) + n * 2048)); } while (0)
; #define PG8_MMA(ai, bj, At, Bt) do { __builtin_amdgcn_s_setprio(1); _Pragma("unroll") for (int m = 0; m < 4; ++m) _Pragma("unroll") for (int n = 0; n < 2; ++n) _Pragma("unroll") for (int k = 0; k < 2; ++k) \
;         acc[ai][bj][m][n] = __builtin_amdgcn_mfma_f32_16x16x32_bf16(Bt[n][k], At[m][k], acc[ai][bj][m][n], 0, 0, 0); __builtin_amdgcn_s_setprio(0); } while (0)
; #define PG8_WAIT_V(n) asm volatile("s_waitcnt vmcnt(" #n ")" ::: "memory")
; #define PG8_WAIT_L(n) asm volatile("s_waitcnt lgkmcnt(" #n ")" ::: "memory")
; #define PG8_BAR __builtin_amdgcn_s_barrier()
; #define PG8_SCHED __builtin_amdgcn_sched_barrier(0)
;     ...
;             PG8_LDB(B0, 0, 0); PG8_LDB(B1, 0, 1); PG8_SCHED; PG8_LDA(At, 0, 0); PG8_STAGE(PG8_SA(1, 1), a1, voffA[1]);
;             PG8_WAIT_V(8); PG8_WAIT_L(0); PG8_BAR; if (do0) { PG8_MMA(0, 0, At, B0); PG8_MMA(0, 1, At, B1); } PG8_BAR; PG8_SCHED;
;             PG8_LDA(At, 0, 1); PG8_STAGE(PG8_SB(0, 0), b2, voffB); PG8_STAGE(PG8_SB(0, 1), b2 + hstep, voffB); PG8_STAGE(PG8_SA(0, 0), a2, vs[0]);
;             PG8_WAIT_V(8); PG8_WAIT_L(0); PG8_BAR; if (do1) { PG8_MMA(1, 0, At, B0); PG8_MMA(1, 1, At, B1); } PG8_BAR; PG8_SCHED;
.LBB0_460:
	ds_read_b128 v[130:133], v203
	ds_read_b128 v[134:137], v204
	ds_read_b128 v[138:141], v205
	ds_read_b128 v[142:145], v206
	ds_read_b128 v[168:171], v207
	ds_read_b128 v[172:175], v208
	ds_read_b128 v[176:179], v209
	ds_read_b128 v[180:183], v210
	s_add_u32 s4, s2, 0x80
	s_addc_u32 s5, s3, 0
	s_cmp_eq_u32 s41, 12
	s_cselect_b32 s39, s9, s5
	s_cselect_b32 s38, s12, s4
	s_cselect_b32 s5, s27, s40
	s_cselect_b32 s4, s29, s37
	v_lshl_add_u64 v[196:197], s[2:3], 0, v[162:163]
	s_add_i32 m0, s50, 0xc000
	ds_read_b128 v[184:187], v211
	ds_read_b128 v[188:191], v211 offset:2048
	ds_read_b128 v[192:195], v212
	ds_read_b128 v[220:223], v212 offset:2048
	ds_read_b128 v[224:227], v211 offset:4096
	ds_read_b128 v[228:231], v211 offset:6144
	ds_read_b128 v[232:235], v212 offset:4096
	ds_read_b128 v[236:239], v212 offset:6144
	global_load_lds_dwordx4 v[196:197], off
	v_lshl_add_u64 v[196:197], s[2:3], 0, v[160:161]
	s_add_i32 m0, s50, 0xe000
	s_add_u32 s6, s4, 0x4000
	global_load_lds_dwordx4 v[196:197], off
	s_waitcnt vmcnt(8)
	s_waitcnt lgkmcnt(0)
	s_addc_u32 s7, s5, 0
	s_barrier
	s_waitcnt lgkmcnt(0)
	v_mfma_f32_16x16x32_bf16 v[126:129], v[130:133], v[184:187], v[126:129]
	v_mfma_f32_16x16x32_bf16 v[58:61], v[138:141], v[184:187], v[58:61]
	v_mfma_f32_16x16x32_bf16 v[122:125], v[130:133], v[188:191], v[122:125]
	v_mfma_f32_16x16x32_bf16 v[118:121], v[138:141], v[188:191], v[118:121]
	v_mfma_f32_16x16x32_bf16 v[114:117], v[130:133], v[224:227], v[114:117]
	v_mfma_f32_16x16x32_bf16 v[110:113], v[138:141], v[224:227], v[110:113]
	v_mfma_f32_16x16x32_bf16 v[106:109], v[130:133], v[228:231], v[106:109]
	v_mfma_f32_16x16x32_bf16 v[102:105], v[138:141], v[228:231], v[102:105]
	v_mfma_f32_16x16x32_bf16 v[126:129], v[134:137], v[192:195], v[126:129]
	v_mfma_f32_16x16x32_bf16 v[58:61], v[142:145], v[192:195], v[58:61]
	v_mfma_f32_16x16x32_bf16 v[122:125], v[134:137], v[220:223], v[122:125]
	v_mfma_f32_16x16x32_bf16 v[118:121], v[142:145], v[220:223], v[118:121]
	v_mfma_f32_16x16x32_bf16 v[114:117], v[134:137], v[232:235], v[114:117]
	v_mfma_f32_16x16x32_bf16 v[110:113], v[142:145], v[232:235], v[110:113]
	v_mfma_f32_16x16x32_bf16 v[106:109], v[134:137], v[236:239], v[106:109]
	v_mfma_f32_16x16x32_bf16 v[102:105], v[142:145], v[236:239], v[102:105]
	v_mfma_f32_16x16x32_bf16 v[66:69], v[168:171], v[184:187], v[66:69]
	v_mfma_f32_16x16x32_bf16 v[50:53], v[176:179], v[184:187], v[50:53]
	v_mfma_f32_16x16x32_bf16 v[54:57], v[168:171], v[188:191], v[54:57]
	v_mfma_f32_16x16x32_bf16 v[42:45], v[176:179], v[188:191], v[42:45]
	v_mfma_f32_16x16x32_bf16 v[46:49], v[168:171], v[224:227], v[46:49]
	v_mfma_f32_16x16x32_bf16 v[34:37], v[176:179], v[224:227], v[34:37]
	v_mfma_f32_16x16x32_bf16 v[98:101], v[168:171], v[228:231], v[98:101]
	v_mfma_f32_16x16x32_bf16 v[38:41], v[176:179], v[228:231], v[38:41]
	v_mfma_f32_16x16x32_bf16 v[66:69], v[172:175], v[192:195], v[66:69]
	v_mfma_f32_16x16x32_bf16 v[50:53], v[180:183], v[192:195], v[50:53]
	v_mfma_f32_16x16x32_bf16 v[54:57], v[172:175], v[220:223], v[54:57]
	v_mfma_f32_16x16x32_bf16 v[42:45], v[180:183], v[220:223], v[42:45]
	v_mfma_f32_16x16x32_bf16 v[46:49], v[172:175], v[232:235], v[46:49]
	v_mfma_f32_16x16x32_bf16 v[34:37], v[180:183], v[232:235], v[34:37]
	v_mfma_f32_16x16x32_bf16 v[98:101], v[172:175], v[236:239], v[98:101]
	v_mfma_f32_16x16x32_bf16 v[38:41], v[180:183], v[236:239], v[38:41]
	s_barrier
	s_add_i32 s42, s65, s49
	v_lshl_add_u64 v[196:197], s[4:5], 0, v[146:147]
	s_mov_b32 m0, s42
	ds_read_b128 v[184:187], v211 offset:16384
	ds_read_b128 v[188:191], v211 offset:18432
	ds_read_b128 v[192:195], v212 offset:16384
	ds_read_b128 v[220:223], v212 offset:18432
	ds_read_b128 v[224:227], v211 offset:20480
	ds_read_b128 v[228:231], v211 offset:22528
	ds_read_b128 v[232:235], v212 offset:20480
	ds_read_b128 v[236:239], v212 offset:22528
	global_load_lds_dwordx4 v[196:197], off
	s_add_i32 m0, s42, 0x2000
	s_add_u32 s42, s4, 0x40000
	v_lshl_add_u64 v[196:197], s[4:5], 0, v[148:149]
	s_addc_u32 s43, s5, 0
	s_add_i32 s74, s66, s49
	global_load_lds_dwordx4 v[196:197], off
	v_lshl_add_u64 v[196:197], s[42:43], 0, v[146:147]
	s_mov_b32 m0, s74
	v_lshl_add_u64 v[240:241], s[38:39], 0, v[152:153]
	global_load_lds_dwordx4 v[196:197], off
	v_lshl_add_u64 v[196:197], s[42:43], 0, v[148:149]
	s_add_i32 m0, s74, 0x2000
	s_nop 0
	global_load_lds_dwordx4 v[196:197], off
	v_lshl_add_u64 v[196:197], s[38:39], 0, v[150:151]
	s_mov_b32 m0, s50
	s_nop 0
	global_load_lds_dwordx4 v[196:197], off
	s_mov_b32 m0, s51
	s_nop 0
	global_load_lds_dwordx4 v[240:241], off
	s_waitcnt vmcnt(8)
	s_waitcnt lgkmcnt(0)
	s_barrier
; #define PG8_STAGE(bufoff, gbase, voff) do { _Pragma("unroll") for (int _i = 0; _i < 2; ++_i) \
;         __builtin_amdgcn_global_load_lds((const unsigned*)((const char*)(gbase) + (voff)[_i]), (LAS unsigned*)(lds + (bufoff) + ldsw + _i * 8192), 16, 0, 0); } while (0)
; #define PG8_LDA(dst, b, h) do { _Pragma("unroll") for (int m = 0; m < 4; ++m) _Pragma("unroll") for (int k = 0; k < 2; ++k) dst[m][k] = *(const LAS bf16x8*)(lds + PG8_SA(b, h) + ((aoff ^ (k * 64)) + m * 2048)); } while (0)
; #define PG8_LDB(dst, b, h) do { _Pragma("unroll") for (int n = 0; n < 2; ++n) _Pragma("unroll") for (int k = 0; k < 2; ++k) dst[n][k] = *(const LAS bf16x8*)(lds + PG8_SB(b, h) + ((boff ^ (k * 64)) + n * 2048)); } while (0)
; #define PG8_MMA(ai, bj, At, Bt) do { __builtin_amdgcn_s_setprio(1); _Pragma("unroll") for (int m = 0; m < 4; ++m) _Pragma("unroll") for (int n = 0; n < 2; ++n) _Pragma("unroll") for (int k = 0; k < 2; ++k) \
;         acc[ai][bj][m][n] = __builtin_amdgcn_mfma_f32_16x16x32_bf16(Bt[n][k], At[m][k], acc[ai][bj][m][n], 0, 0, 0); __builtin_amdgcn_s_setprio(0); } while (0)
; #define PG8_WAIT_V(n) asm volatile("s_waitcnt vmcnt(" #n ")" ::: "memory")
; #define PG8_WAIT_L(n) asm volatile("s_waitcnt lgkmcnt(" #n ")" ::: "memory")
; #define PG8_BAR __builtin_amdgcn_s_barrier()
; #define PG8_SCHED __builtin_amdgcn_sched_barrier(0)
;     ...
;             PG8_WAIT_V(8); PG8_WAIT_L(0); PG8_BAR; if (do1) { PG8_MMA(1, 0, At, B0); PG8_MMA(1, 1, At, B1); } PG8_BAR; PG8_SCHED;
;             PG8_LDB(B0, 1, 0); PG8_LDB(B1, 1, 1); PG8_SCHED; PG8_LDA(At, 1, 0); PG8_STAGE(PG8_SA(0, 1), a2, vs[1]);
;             PG8_WAIT_V(8); PG8_WAIT_L(0); PG8_BAR; if (do0) { PG8_MMA(0, 0, At, B0); PG8_MMA(0, 1, At, B1); } PG8_BAR; PG8_SCHED;
	s_waitcnt lgkmcnt(0)
	v_mfma_f32_16x16x32_bf16 v[94:97], v[130:133], v[184:187], v[94:97]
	v_mfma_f32_16x16x32_bf16 v[26:29], v[138:141], v[184:187], v[26:29]
	v_mfma_f32_16x16x32_bf16 v[90:93], v[130:133], v[188:191], v[90:93]
	v_mfma_f32_16x16x32_bf16 v[86:89], v[138:141], v[188:191], v[86:89]
	v_mfma_f32_16x16x32_bf16 v[82:85], v[130:133], v[224:227], v[82:85]
	v_mfma_f32_16x16x32_bf16 v[78:81], v[138:141], v[224:227], v[78:81]
	v_mfma_f32_16x16x32_bf16 v[74:77], v[130:133], v[228:231], v[74:77]
	v_mfma_f32_16x16x32_bf16 v[70:73], v[138:141], v[228:231], v[70:73]
	v_mfma_f32_16x16x32_bf16 v[94:97], v[134:137], v[192:195], v[94:97]
	v_mfma_f32_16x16x32_bf16 v[26:29], v[142:145], v[192:195], v[26:29]
	v_mfma_f32_16x16x32_bf16 v[90:93], v[134:137], v[220:223], v[90:93]
	v_mfma_f32_16x16x32_bf16 v[86:89], v[142:145], v[220:223], v[86:89]
	v_mfma_f32_16x16x32_bf16 v[82:85], v[134:137], v[232:235], v[82:85]
	v_mfma_f32_16x16x32_bf16 v[78:81], v[142:145], v[232:235], v[78:81]
	v_mfma_f32_16x16x32_bf16 v[74:77], v[134:137], v[236:239], v[74:77]
	v_mfma_f32_16x16x32_bf16 v[70:73], v[142:145], v[236:239], v[70:73]
	v_mfma_f32_16x16x32_bf16 v[30:33], v[168:171], v[184:187], v[30:33]
	v_mfma_f32_16x16x32_bf16 v[18:21], v[176:179], v[184:187], v[18:21]
	v_mfma_f32_16x16x32_bf16 v[22:25], v[168:171], v[188:191], v[22:25]
	v_mfma_f32_16x16x32_bf16 v[10:13], v[176:179], v[188:191], v[10:13]
	v_mfma_f32_16x16x32_bf16 v[14:17], v[168:171], v[224:227], v[14:17]
	v_mfma_f32_16x16x32_bf16 v[2:5], v[176:179], v[224:227], v[2:5]
	v_mfma_f32_16x16x32_bf16 v[62:65], v[168:171], v[228:231], v[62:65]
	v_mfma_f32_16x16x32_bf16 v[6:9], v[176:179], v[228:231], v[6:9]
	v_mfma_f32_16x16x32_bf16 v[30:33], v[172:175], v[192:195], v[30:33]
	v_mfma_f32_16x16x32_bf16 v[18:21], v[180:183], v[192:195], v[18:21]
	v_mfma_f32_16x16x32_bf16 v[22:25], v[172:175], v[220:223], v[22:25]
	v_mfma_f32_16x16x32_bf16 v[10:13], v[180:183], v[220:223], v[10:13]
	v_mfma_f32_16x16x32_bf16 v[14:17], v[172:175], v[232:235], v[14:17]
	v_mfma_f32_16x16x32_bf16 v[2:5], v[180:183], v[232:235], v[2:5]
	v_mfma_f32_16x16x32_bf16 v[62:65], v[172:175], v[236:239], v[62:65]
	v_mfma_f32_16x16x32_bf16 v[6:9], v[180:183], v[236:239], v[6:9]
	s_barrier
	s_add_i32 s42, 0, 0x18000
	s_add_i32 s43, 0, 0x1c000
	v_add_u32_e32 v130, s42, v201
	v_add_u32_e32 v134, s42, v202
	v_add_u32_e32 v158, s43, v201
	v_add_u32_e32 v172, s43, v202
	ds_read_b128 v[130:133], v130
	ds_read_b128 v[134:137], v134
	ds_read_b128 v[138:141], v213
	ds_read_b128 v[142:145], v214
	ds_read_b128 v[168:171], v158
	ds_read_b128 v[172:175], v172
	ds_read_b128 v[176:179], v215
	ds_read_b128 v[180:183], v216
	s_mov_b32 m0, s52
	v_lshl_add_u64 v[242:243], s[38:39], 0, v[154:155]
	ds_read_b128 v[184:187], v211 offset:32768
	ds_read_b128 v[188:191], v211 offset:34816
	ds_read_b128 v[192:195], v212 offset:32768
	ds_read_b128 v[220:223], v212 offset:34816
	ds_read_b128 v[224:227], v211 offset:36864
	ds_read_b128 v[228:231], v211 offset:38912
	ds_read_b128 v[232:235], v212 offset:36864
	ds_read_b128 v[236:239], v212 offset:38912
	global_load_lds_dwordx4 v[242:243], off
	v_lshl_add_u64 v[242:243], s[38:39], 0, v[156:157]
	s_mov_b32 m0, s53
	s_nop 0
	global_load_lds_dwordx4 v[242:243], off
	s_waitcnt vmcnt(8)
	s_waitcnt lgkmcnt(0)
	s_barrier
	s_waitcnt lgkmcnt(0)
	v_mfma_f32_16x16x32_bf16 v[126:129], v[130:133], v[184:187], v[126:129]
	v_mfma_f32_16x16x32_bf16 v[58:61], v[138:141], v[184:187], v[58:61]
	v_mfma_f32_16x16x32_bf16 v[122:125], v[130:133], v[188:191], v[122:125]
	v_mfma_f32_16x16x32_bf16 v[118:121], v[138:141], v[188:191], v[118:121]
	v_mfma_f32_16x16x32_bf16 v[114:117], v[130:133], v[224:227], v[114:117]
	v_mfma_f32_16x16x32_bf16 v[110:113], v[138:141], v[224:227], v[110:113]
	v_mfma_f32_16x16x32_bf16 v[106:109], v[130:133], v[228:231], v[106:109]
	v_mfma_f32_16x16x32_bf16 v[102:105], v[138:141], v[228:231], v[102:105]
	v_mfma_f32_16x16x32_bf16 v[126:129], v[134:137], v[192:195], v[126:129]
	v_mfma_f32_16x16x32_bf16 v[58:61], v[142:145], v[192:195], v[58:61]
	v_mfma_f32_16x16x32_bf16 v[122:125], v[134:137], v[220:223], v[122:125]
	v_mfma_f32_16x16x32_bf16 v[118:121], v[142:145], v[220:223], v[118:121]
	v_mfma_f32_16x16x32_bf16 v[114:117], v[134:137], v[232:235], v[114:117]
	v_mfma_f32_16x16x32_bf16 v[110:113], v[142:145], v[232:235], v[110:113]
	v_mfma_f32_16x16x32_bf16 v[106:109], v[134:137], v[236:239], v[106:109]
	v_mfma_f32_16x16x32_bf16 v[102:105], v[142:145], v[236:239], v[102:105]
	v_mfma_f32_16x16x32_bf16 v[66:69], v[168:171], v[184:187], v[66:69]
	v_mfma_f32_16x16x32_bf16 v[50:53], v[176:179], v[184:187], v[50:53]
	v_mfma_f32_16x16x32_bf16 v[54:57], v[168:171], v[188:191], v[54:57]
	v_mfma_f32_16x16x32_bf16 v[42:45], v[176:179], v[188:191], v[42:45]
	v_mfma_f32_16x16x32_bf16 v[46:49], v[168:171], v[224:227], v[46:49]
	v_mfma_f32_16x16x32_bf16 v[34:37], v[176:179], v[224:227], v[34:37]
	v_mfma_f32_16x16x32_bf16 v[98:101], v[168:171], v[228:231], v[98:101]
	v_mfma_f32_16x16x32_bf16 v[38:41], v[176:179], v[228:231], v[38:41]
	v_mfma_f32_16x16x32_bf16 v[66:69], v[172:175], v[192:195], v[66:69]
	v_mfma_f32_16x16x32_bf16 v[50:53], v[180:183], v[192:195], v[50:53]
	v_mfma_f32_16x16x32_bf16 v[54:57], v[172:175], v[220:223], v[54:57]
	v_mfma_f32_16x16x32_bf16 v[42:45], v[180:183], v[220:223], v[42:45]
	v_mfma_f32_16x16x32_bf16 v[46:49], v[172:175], v[232:235], v[46:49]
	v_mfma_f32_16x16x32_bf16 v[34:37], v[180:183], v[232:235], v[34:37]
	v_mfma_f32_16x16x32_bf16 v[98:101], v[172:175], v[236:239], v[98:101]
	v_mfma_f32_16x16x32_bf16 v[38:41], v[180:183], v[236:239], v[38:41]
	s_barrier
; #define PG8_STAGE(bufoff, gbase, voff) do { _Pragma("unroll") for (int _i = 0; _i < 2; ++_i) \
;         __builtin_amdgcn_global_load_lds((const unsigned*)((const char*)(gbase) + (voff)[_i]), (LAS unsigned*)(lds + (bufoff) + ldsw + _i * 8192), 16, 0, 0); } while (0)
; #define PG8_LDA(dst, b, h) do { _Pragma("unroll") for (int m = 0; m < 4; ++m) _Pragma("unroll") for (int k = 0; k < 2; ++k) dst[m][k] = *(const LAS bf16x8*)(lds + PG8_SA(b, h) + ((aoff ^ (k * 64)) + m * 2048)); } while (0)
; #define PG8_MMA(ai, bj, At, Bt) do { __builtin_amdgcn_s_setprio(1); _Pragma("unroll") for (int m = 0; m < 4; ++m) _Pragma("unroll") for (int n = 0; n < 2; ++n) _Pragma("unroll") for (int k = 0; k < 2; ++k) \
;         acc[ai][bj][m][n] = __builtin_amdgcn_mfma_f32_16x16x32_bf16(Bt[n][k], At[m][k], acc[ai][bj][m][n], 0, 0, 0); __builtin_amdgcn_s_setprio(0); } while (0)
; #define PG8_WAIT_V(n) asm volatile("s_waitcnt vmcnt(" #n ")" ::: "memory")
; #define PG8_WAIT_L(n) asm volatile("s_waitcnt lgkmcnt(" #n ")" ::: "memory")
; #define PG8_BAR __builtin_amdgcn_s_barrier()
; #define PG8_SCHED __builtin_amdgcn_sched_barrier(0)
;     ...
;             PG8_LDA(At, 1, 1); PG8_STAGE(PG8_SB(1, 0), b3, voffB); PG8_STAGE(PG8_SB(1, 1), b3 + hstep, voffB); PG8_STAGE(PG8_SA(1, 0), a3, vs[0]);
;             PG8_WAIT_V(8); PG8_WAIT_L(0); PG8_BAR; if (do1) { PG8_MMA(1, 0, At, B0); PG8_MMA(1, 1, At, B1); } PG8_BAR; PG8_SCHED;
;         }
;         if (wr == 0) PG8_BAR;
	s_add_i32 s38, s42, s49
	v_lshl_add_u64 v[242:243], s[6:7], 0, v[146:147]
	s_mov_b32 m0, s38
	ds_read_b128 v[184:187], v211 offset:49152
	ds_read_b128 v[188:191], v211 offset:51200
	ds_read_b128 v[192:195], v212 offset:49152
	ds_read_b128 v[220:223], v212 offset:51200
	ds_read_b128 v[224:227], v211 offset:53248
	ds_read_b128 v[228:231], v211 offset:55296
	ds_read_b128 v[232:235], v212 offset:53248
	ds_read_b128 v[236:239], v212 offset:55296
	global_load_lds_dwordx4 v[242:243], off
	s_add_i32 m0, s38, 0x2000
	s_add_u32 s4, s4, 0x44000
	v_lshl_add_u64 v[242:243], s[6:7], 0, v[148:149]
	s_addc_u32 s5, s5, 0
	s_add_i32 s6, s43, s49
	global_load_lds_dwordx4 v[242:243], off
	v_lshl_add_u64 v[242:243], s[4:5], 0, v[146:147]
	s_mov_b32 m0, s6
	v_lshl_add_u64 v[196:197], v[196:197], 0, s[92:93]
	global_load_lds_dwordx4 v[242:243], off
	v_lshl_add_u64 v[242:243], s[4:5], 0, v[148:149]
	s_add_i32 m0, s6, 0x2000
	s_nop 0
	global_load_lds_dwordx4 v[242:243], off
	s_mov_b32 m0, s55
	s_nop 0
	global_load_lds_dwordx4 v[196:197], off
	v_lshl_add_u64 v[196:197], v[240:241], 0, s[92:93]
	s_mov_b32 m0, s56
	s_nop 0
	global_load_lds_dwordx4 v[196:197], off
	s_waitcnt vmcnt(8)
	s_waitcnt lgkmcnt(0)
	s_barrier
	s_waitcnt lgkmcnt(0)
	v_mfma_f32_16x16x32_bf16 v[94:97], v[130:133], v[184:187], v[94:97]
	v_mfma_f32_16x16x32_bf16 v[26:29], v[138:141], v[184:187], v[26:29]
	v_mfma_f32_16x16x32_bf16 v[90:93], v[130:133], v[188:191], v[90:93]
	v_mfma_f32_16x16x32_bf16 v[86:89], v[138:141], v[188:191], v[86:89]
	v_mfma_f32_16x16x32_bf16 v[82:85], v[130:133], v[224:227], v[82:85]
	v_mfma_f32_16x16x32_bf16 v[78:81], v[138:141], v[224:227], v[78:81]
	v_mfma_f32_16x16x32_bf16 v[74:77], v[130:133], v[228:231], v[74:77]
	v_mfma_f32_16x16x32_bf16 v[70:73], v[138:141], v[228:231], v[70:73]
	v_mfma_f32_16x16x32_bf16 v[94:97], v[134:137], v[192:195], v[94:97]
	v_mfma_f32_16x16x32_bf16 v[26:29], v[142:145], v[192:195], v[26:29]
	v_mfma_f32_16x16x32_bf16 v[90:93], v[134:137], v[220:223], v[90:93]
	v_mfma_f32_16x16x32_bf16 v[86:89], v[142:145], v[220:223], v[86:89]
	v_mfma_f32_16x16x32_bf16 v[82:85], v[134:137], v[232:235], v[82:85]
	v_mfma_f32_16x16x32_bf16 v[78:81], v[142:145], v[232:235], v[78:81]
	v_mfma_f32_16x16x32_bf16 v[74:77], v[134:137], v[236:239], v[74:77]
	v_mfma_f32_16x16x32_bf16 v[70:73], v[142:145], v[236:239], v[70:73]
	v_mfma_f32_16x16x32_bf16 v[30:33], v[168:171], v[184:187], v[30:33]
	v_mfma_f32_16x16x32_bf16 v[18:21], v[176:179], v[184:187], v[18:21]
	v_mfma_f32_16x16x32_bf16 v[22:25], v[168:171], v[188:191], v[22:25]
	v_mfma_f32_16x16x32_bf16 v[10:13], v[176:179], v[188:191], v[10:13]
	v_mfma_f32_16x16x32_bf16 v[14:17], v[168:171], v[224:227], v[14:17]
	v_mfma_f32_16x16x32_bf16 v[2:5], v[176:179], v[224:227], v[2:5]
	v_mfma_f32_16x16x32_bf16 v[62:65], v[168:171], v[228:231], v[62:65]
	v_mfma_f32_16x16x32_bf16 v[6:9], v[176:179], v[228:231], v[6:9]
	v_mfma_f32_16x16x32_bf16 v[30:33], v[172:175], v[192:195], v[30:33]
	v_mfma_f32_16x16x32_bf16 v[18:21], v[180:183], v[192:195], v[18:21]
	v_mfma_f32_16x16x32_bf16 v[22:25], v[172:175], v[220:223], v[22:25]
	v_mfma_f32_16x16x32_bf16 v[10:13], v[180:183], v[220:223], v[10:13]
	v_mfma_f32_16x16x32_bf16 v[14:17], v[172:175], v[232:235], v[14:17]
	v_mfma_f32_16x16x32_bf16 v[2:5], v[180:183], v[232:235], v[2:5]
	v_mfma_f32_16x16x32_bf16 v[62:65], v[172:175], v[236:239], v[62:65]
	v_mfma_f32_16x16x32_bf16 v[6:9], v[180:183], v[236:239], v[6:9]
	s_barrier
	s_add_i32 s41, s41, 2
	s_add_u32 s37, s37, 0x8000
	s_addc_u32 s40, s40, 0
	s_add_u32 s2, s2, 0x100
	s_addc_u32 s3, s3, 0
	s_cmp_gt_u32 s41, 13
	s_cbranch_scc0 .LBB0_460
	s_and_b64 vcc, exec, s[24:25]
	s_cbranch_vccz .LBB0_463
	s_barrier

; #define PG8_STAGE(bufoff, gbase, voff) do { _Pragma("unroll") for (int _i = 0; _i < 2; ++_i) \
;         __builtin_amdgcn_global_load_lds((const unsigned*)((const char*)(gbase) + (voff)[_i]), (LAS unsigned*)(lds + (bufoff) + ldsw + _i * 8192), 16, 0, 0); } while (0)
; #define PG8_LDA(dst, b, h) do { _Pragma("unroll") for (int m = 0; m < 4; ++m) _Pragma("unroll") for (int k = 0; k < 2; ++k) dst[m][k] = *(const LAS bf16x8*)(lds + PG8_SA(b, h) + ((aoff ^ (k * 64)) + m * 2048)); } while (0)
; #define PG8_LDB(dst, b, h) do { _Pragma("unroll") for (int n = 0; n < 2; ++n) _Pragma("unroll") for (int k = 0; k < 2; ++k) dst[n][k] = *(const LAS bf16x8*)(lds + PG8_SB(b, h) + ((boff ^ (k * 64)) + n * 2048)); } while (0)
; #define PG8_MMA(ai, bj, At, Bt) do { __builtin_amdgcn_s_setprio(1); _Pragma("unroll") for (int m = 0; m < 4; ++m) _Pragma("unroll") for (int n = 0; n < 2; ++n) _Pragma("unroll") for (int k = 0; k < 2; ++k) \
;         acc[ai][bj][m][n] = __builtin_amdgcn_mfma_f32_16x16x32_bf16(Bt[n][k], At[m][k], acc[ai][bj][m][n], 0, 0, 0); __builtin_amdgcn_s_setprio(0); } while (0)
; #define PG8_WAIT_V(n) asm volatile("s_waitcnt vmcnt(" #n ")" ::: "memory")
; #define PG8_WAIT_L(n) asm volatile("s_waitcnt lgkmcnt(" #n ")" ::: "memory")
; #define PG8_BAR __builtin_amdgcn_s_barrier()
; #define PG8_SCHED __builtin_amdgcn_sched_barrier(0)
;     ...
;             PG8_LDB(B0, 0, 0); PG8_LDB(B1, 0, 1); PG8_SCHED; PG8_LDA(At, 0, 0); PG8_STAGE(PG8_SA(1, 1), a1, voffA[1]);
;             PG8_WAIT_V(8); PG8_WAIT_L(0); PG8_BAR; if (do0) { PG8_MMA(0, 0, At, B0); PG8_MMA(0, 1, At, B1); } PG8_BAR; PG8_SCHED;
;             PG8_LDA(At, 0, 1); PG8_STAGE(PG8_SB(0, 0), b2, voffB); PG8_STAGE(PG8_SB(0, 1), b2 + hstep, voffB); PG8_STAGE(PG8_SA(0, 0), a2, vs[0]);
;             PG8_WAIT_V(8); PG8_WAIT_L(0); PG8_BAR; if (do1) { PG8_MMA(1, 0, At, B0); PG8_MMA(1, 1, At, B1); } PG8_BAR; PG8_SCHED;
.LBB0_557:
	ds_read_b128 v[130:133], v199
	ds_read_b128 v[134:137], v200
	ds_read_b128 v[138:141], v201
	ds_read_b128 v[142:145], v202
	ds_read_b128 v[164:167], v203
	ds_read_b128 v[168:171], v204
	ds_read_b128 v[172:175], v205
	ds_read_b128 v[176:179], v206
	s_add_u32 s2, s0, 0x80
	s_addc_u32 s3, s1, 0
	s_cmp_eq_u32 s41, 12
	s_cselect_b32 s39, s7, s3
	s_cselect_b32 s38, s8, s2
	s_cselect_b32 s3, s25, s40
	s_cselect_b32 s2, s27, s37
	v_lshl_add_u64 v[192:193], s[0:1], 0, v[162:163]
	s_add_i32 m0, s50, 0xc000
	ds_read_b128 v[180:183], v207
	ds_read_b128 v[184:187], v207 offset:2048
	ds_read_b128 v[188:191], v208
	ds_read_b128 v[216:219], v208 offset:2048
	ds_read_b128 v[220:223], v207 offset:4096
	ds_read_b128 v[224:227], v207 offset:6144
	ds_read_b128 v[228:231], v208 offset:4096
	ds_read_b128 v[232:235], v208 offset:6144
	global_load_lds_dwordx4 v[192:193], off
	v_lshl_add_u64 v[192:193], s[0:1], 0, v[160:161]
	s_add_i32 m0, s50, 0xe000
	s_add_u32 s4, s2, 0x4000
	global_load_lds_dwordx4 v[192:193], off
	s_waitcnt vmcnt(8)
	s_waitcnt lgkmcnt(0)
	s_addc_u32 s5, s3, 0
	s_barrier
	s_waitcnt lgkmcnt(0)
	v_mfma_f32_16x16x32_bf16 v[126:129], v[130:133], v[180:183], v[126:129]
	v_mfma_f32_16x16x32_bf16 v[58:61], v[138:141], v[180:183], v[58:61]
	v_mfma_f32_16x16x32_bf16 v[122:125], v[130:133], v[184:187], v[122:125]
	v_mfma_f32_16x16x32_bf16 v[118:121], v[138:141], v[184:187], v[118:121]
	v_mfma_f32_16x16x32_bf16 v[114:117], v[130:133], v[220:223], v[114:117]
	v_mfma_f32_16x16x32_bf16 v[110:113], v[138:141], v[220:223], v[110:113]
	v_mfma_f32_16x16x32_bf16 v[106:109], v[130:133], v[224:227], v[106:109]
	v_mfma_f32_16x16x32_bf16 v[102:105], v[138:141], v[224:227], v[102:105]
	v_mfma_f32_16x16x32_bf16 v[126:129], v[134:137], v[188:191], v[126:129]
	v_mfma_f32_16x16x32_bf16 v[58:61], v[142:145], v[188:191], v[58:61]
	v_mfma_f32_16x16x32_bf16 v[122:125], v[134:137], v[216:219], v[122:125]
	v_mfma_f32_16x16x32_bf16 v[118:121], v[142:145], v[216:219], v[118:121]
	v_mfma_f32_16x16x32_bf16 v[114:117], v[134:137], v[228:231], v[114:117]
	v_mfma_f32_16x16x32_bf16 v[110:113], v[142:145], v[228:231], v[110:113]
	v_mfma_f32_16x16x32_bf16 v[106:109], v[134:137], v[232:235], v[106:109]
	v_mfma_f32_16x16x32_bf16 v[102:105], v[142:145], v[232:235], v[102:105]
	v_mfma_f32_16x16x32_bf16 v[66:69], v[164:167], v[180:183], v[66:69]
	v_mfma_f32_16x16x32_bf16 v[50:53], v[172:175], v[180:183], v[50:53]
	v_mfma_f32_16x16x32_bf16 v[54:57], v[164:167], v[184:187], v[54:57]
	v_mfma_f32_16x16x32_bf16 v[42:45], v[172:175], v[184:187], v[42:45]
	v_mfma_f32_16x16x32_bf16 v[46:49], v[164:167], v[220:223], v[46:49]
	v_mfma_f32_16x16x32_bf16 v[34:37], v[172:175], v[220:223], v[34:37]
	v_mfma_f32_16x16x32_bf16 v[98:101], v[164:167], v[224:227], v[98:101]
	v_mfma_f32_16x16x32_bf16 v[38:41], v[172:175], v[224:227], v[38:41]
	v_mfma_f32_16x16x32_bf16 v[66:69], v[168:171], v[188:191], v[66:69]
	v_mfma_f32_16x16x32_bf16 v[50:53], v[176:179], v[188:191], v[50:53]
	v_mfma_f32_16x16x32_bf16 v[54:57], v[168:171], v[216:219], v[54:57]
	v_mfma_f32_16x16x32_bf16 v[42:45], v[176:179], v[216:219], v[42:45]
	v_mfma_f32_16x16x32_bf16 v[46:49], v[168:171], v[228:231], v[46:49]
	v_mfma_f32_16x16x32_bf16 v[34:37], v[176:179], v[228:231], v[34:37]
	v_mfma_f32_16x16x32_bf16 v[98:101], v[168:171], v[232:235], v[98:101]
	v_mfma_f32_16x16x32_bf16 v[38:41], v[176:179], v[232:235], v[38:41]
	s_barrier
	s_add_i32 s42, s63, s49
	v_lshl_add_u64 v[192:193], s[2:3], 0, v[146:147]
	s_mov_b32 m0, s42
	ds_read_b128 v[180:183], v207 offset:16384
	ds_read_b128 v[184:187], v207 offset:18432
	ds_read_b128 v[188:191], v208 offset:16384
	ds_read_b128 v[216:219], v208 offset:18432
	ds_read_b128 v[220:223], v207 offset:20480
	ds_read_b128 v[224:227], v207 offset:22528
	ds_read_b128 v[228:231], v208 offset:20480
	ds_read_b128 v[232:235], v208 offset:22528
	global_load_lds_dwordx4 v[192:193], off
	s_add_i32 m0, s42, 0x2000
	s_add_u32 s42, s2, 0x40000
	v_lshl_add_u64 v[192:193], s[2:3], 0, v[148:149]
	s_addc_u32 s43, s3, 0
	s_add_i32 s73, s64, s49
	global_load_lds_dwordx4 v[192:193], off
	v_lshl_add_u64 v[192:193], s[42:43], 0, v[146:147]
	s_mov_b32 m0, s73
	v_lshl_add_u64 v[236:237], s[38:39], 0, v[152:153]
	global_load_lds_dwordx4 v[192:193], off
	v_lshl_add_u64 v[192:193], s[42:43], 0, v[148:149]
	s_add_i32 m0, s73, 0x2000
	s_nop 0
	global_load_lds_dwordx4 v[192:193], off
	v_lshl_add_u64 v[192:193], s[38:39], 0, v[150:151]
	s_mov_b32 m0, s50
	s_nop 0
	global_load_lds_dwordx4 v[192:193], off
	s_mov_b32 m0, s51
	s_nop 0
	global_load_lds_dwordx4 v[236:237], off
	s_waitcnt vmcnt(8)
	s_waitcnt lgkmcnt(0)
	s_barrier
; #define PG8_STAGE(bufoff, gbase, voff) do { _Pragma("unroll") for (int _i = 0; _i < 2; ++_i) \
;         __builtin_amdgcn_global_load_lds((const unsigned*)((const char*)(gbase) + (voff)[_i]), (LAS unsigned*)(lds + (bufoff) + ldsw + _i * 8192), 16, 0, 0); } while (0)
; #define PG8_LDA(dst, b, h) do { _Pragma("unroll") for (int m = 0; m < 4; ++m) _Pragma("unroll") for (int k = 0; k < 2; ++k) dst[m][k] = *(const LAS bf16x8*)(lds + PG8_SA(b, h) + ((aoff ^ (k * 64)) + m * 2048)); } while (0)
; #define PG8_LDB(dst, b, h) do { _Pragma("unroll") for (int n = 0; n < 2; ++n) _Pragma("unroll") for (int k = 0; k < 2; ++k) dst[n][k] = *(const LAS bf16x8*)(lds + PG8_SB(b, h) + ((boff ^ (k * 64)) + n * 2048)); } while (0)
; #define PG8_MMA(ai, bj, At, Bt) do { __builtin_amdgcn_s_setprio(1); _Pragma("unroll") for (int m = 0; m < 4; ++m) _Pragma("unroll") for (int n = 0; n < 2; ++n) _Pragma("unroll") for (int k = 0; k < 2; ++k) \
;         acc[ai][bj][m][n] = __builtin_amdgcn_mfma_f32_16x16x32_bf16(Bt[n][k], At[m][k], acc[ai][bj][m][n], 0, 0, 0); __builtin_amdgcn_s_setprio(0); } while (0)
; #define PG8_WAIT_V(n) asm volatile("s_waitcnt vmcnt(" #n ")" ::: "memory")
; #define PG8_WAIT_L(n) asm volatile("s_waitcnt lgkmcnt(" #n ")" ::: "memory")
; #define PG8_BAR __builtin_amdgcn_s_barrier()
; #define PG8_SCHED __builtin_amdgcn_sched_barrier(0)
;     ...
;             PG8_WAIT_V(8); PG8_WAIT_L(0); PG8_BAR; if (do1) { PG8_MMA(1, 0, At, B0); PG8_MMA(1, 1, At, B1); } PG8_BAR; PG8_SCHED;
;             PG8_LDB(B0, 1, 0); PG8_LDB(B1, 1, 1); PG8_SCHED; PG8_LDA(At, 1, 0); PG8_STAGE(PG8_SA(0, 1), a2, vs[1]);
;             PG8_WAIT_V(8); PG8_WAIT_L(0); PG8_BAR; if (do0) { PG8_MMA(0, 0, At, B0); PG8_MMA(0, 1, At, B1); } PG8_BAR; PG8_SCHED;
	s_waitcnt lgkmcnt(0)
	v_mfma_f32_16x16x32_bf16 v[94:97], v[130:133], v[180:183], v[94:97]
	v_mfma_f32_16x16x32_bf16 v[26:29], v[138:141], v[180:183], v[26:29]
	v_mfma_f32_16x16x32_bf16 v[90:93], v[130:133], v[184:187], v[90:93]
	v_mfma_f32_16x16x32_bf16 v[86:89], v[138:141], v[184:187], v[86:89]
	v_mfma_f32_16x16x32_bf16 v[82:85], v[130:133], v[220:223], v[82:85]
	v_mfma_f32_16x16x32_bf16 v[78:81], v[138:141], v[220:223], v[78:81]
	v_mfma_f32_16x16x32_bf16 v[74:77], v[130:133], v[224:227], v[74:77]
	v_mfma_f32_16x16x32_bf16 v[70:73], v[138:141], v[224:227], v[70:73]
	v_mfma_f32_16x16x32_bf16 v[94:97], v[134:137], v[188:191], v[94:97]
	v_mfma_f32_16x16x32_bf16 v[26:29], v[142:145], v[188:191], v[26:29]
	v_mfma_f32_16x16x32_bf16 v[90:93], v[134:137], v[216:219], v[90:93]
	v_mfma_f32_16x16x32_bf16 v[86:89], v[142:145], v[216:219], v[86:89]
	v_mfma_f32_16x16x32_bf16 v[82:85], v[134:137], v[228:231], v[82:85]
	v_mfma_f32_16x16x32_bf16 v[78:81], v[142:145], v[228:231], v[78:81]
	v_mfma_f32_16x16x32_bf16 v[74:77], v[134:137], v[232:235], v[74:77]
	v_mfma_f32_16x16x32_bf16 v[70:73], v[142:145], v[232:235], v[70:73]
	v_mfma_f32_16x16x32_bf16 v[30:33], v[164:167], v[180:183], v[30:33]
	v_mfma_f32_16x16x32_bf16 v[18:21], v[172:175], v[180:183], v[18:21]
	v_mfma_f32_16x16x32_bf16 v[22:25], v[164:167], v[184:187], v[22:25]
	v_mfma_f32_16x16x32_bf16 v[10:13], v[172:175], v[184:187], v[10:13]
	v_mfma_f32_16x16x32_bf16 v[14:17], v[164:167], v[220:223], v[14:17]
	v_mfma_f32_16x16x32_bf16 v[2:5], v[172:175], v[220:223], v[2:5]
	v_mfma_f32_16x16x32_bf16 v[62:65], v[164:167], v[224:227], v[62:65]
	v_mfma_f32_16x16x32_bf16 v[6:9], v[172:175], v[224:227], v[6:9]
	v_mfma_f32_16x16x32_bf16 v[30:33], v[168:171], v[188:191], v[30:33]
	v_mfma_f32_16x16x32_bf16 v[18:21], v[176:179], v[188:191], v[18:21]
	v_mfma_f32_16x16x32_bf16 v[22:25], v[168:171], v[216:219], v[22:25]
	v_mfma_f32_16x16x32_bf16 v[10:13], v[176:179], v[216:219], v[10:13]
	v_mfma_f32_16x16x32_bf16 v[14:17], v[168:171], v[228:231], v[14:17]
	v_mfma_f32_16x16x32_bf16 v[2:5], v[176:179], v[228:231], v[2:5]
	v_mfma_f32_16x16x32_bf16 v[62:65], v[168:171], v[232:235], v[62:65]
	v_mfma_f32_16x16x32_bf16 v[6:9], v[176:179], v[232:235], v[6:9]
	s_barrier
	s_add_i32 s42, 0, 0x18000
	s_add_i32 s43, 0, 0x1c000
	v_add_u32_e32 v130, s42, v196
	v_add_u32_e32 v134, s42, v197
	v_add_u32_e32 v158, s43, v196
	v_add_u32_e32 v168, s43, v197
	ds_read_b128 v[130:133], v130
	ds_read_b128 v[134:137], v134
	ds_read_b128 v[138:141], v209
	ds_read_b128 v[142:145], v210
	ds_read_b128 v[164:167], v158
	ds_read_b128 v[168:171], v168
	ds_read_b128 v[172:175], v211
	ds_read_b128 v[176:179], v212
	s_mov_b32 m0, s52
	v_lshl_add_u64 v[238:239], s[38:39], 0, v[154:155]
	ds_read_b128 v[180:183], v207 offset:32768
	ds_read_b128 v[184:187], v207 offset:34816
	ds_read_b128 v[188:191], v208 offset:32768
	ds_read_b128 v[216:219], v208 offset:34816
	ds_read_b128 v[220:223], v207 offset:36864
	ds_read_b128 v[224:227], v207 offset:38912
	ds_read_b128 v[228:231], v208 offset:36864
	ds_read_b128 v[232:235], v208 offset:38912
	global_load_lds_dwordx4 v[238:239], off
	v_lshl_add_u64 v[238:239], s[38:39], 0, v[156:157]
	s_mov_b32 m0, s53
	s_nop 0
	global_load_lds_dwordx4 v[238:239], off
	s_waitcnt vmcnt(8)
	s_waitcnt lgkmcnt(0)
	s_barrier
	s_waitcnt lgkmcnt(0)
	v_mfma_f32_16x16x32_bf16 v[126:129], v[130:133], v[180:183], v[126:129]
	v_mfma_f32_16x16x32_bf16 v[58:61], v[138:141], v[180:183], v[58:61]
	v_mfma_f32_16x16x32_bf16 v[122:125], v[130:133], v[184:187], v[122:125]
	v_mfma_f32_16x16x32_bf16 v[118:121], v[138:141], v[184:187], v[118:121]
	v_mfma_f32_16x16x32_bf16 v[114:117], v[130:133], v[220:223], v[114:117]
	v_mfma_f32_16x16x32_bf16 v[110:113], v[138:141], v[220:223], v[110:113]
	v_mfma_f32_16x16x32_bf16 v[106:109], v[130:133], v[224:227], v[106:109]
	v_mfma_f32_16x16x32_bf16 v[102:105], v[138:141], v[224:227], v[102:105]
	v_mfma_f32_16x16x32_bf16 v[126:129], v[134:137], v[188:191], v[126:129]
	v_mfma_f32_16x16x32_bf16 v[58:61], v[142:145], v[188:191], v[58:61]
	v_mfma_f32_16x16x32_bf16 v[122:125], v[134:137], v[216:219], v[122:125]
	v_mfma_f32_16x16x32_bf16 v[118:121], v[142:145], v[216:219], v[118:121]
	v_mfma_f32_16x16x32_bf16 v[114:117], v[134:137], v[228:231], v[114:117]
	v_mfma_f32_16x16x32_bf16 v[110:113], v[142:145], v[228:231], v[110:113]
	v_mfma_f32_16x16x32_bf16 v[106:109], v[134:137], v[232:235], v[106:109]
	v_mfma_f32_16x16x32_bf16 v[102:105], v[142:145], v[232:235], v[102:105]
	v_mfma_f32_16x16x32_bf16 v[66:69], v[164:167], v[180:183], v[66:69]
	v_mfma_f32_16x16x32_bf16 v[50:53], v[172:175], v[180:183], v[50:53]
	v_mfma_f32_16x16x32_bf16 v[54:57], v[164:167], v[184:187], v[54:57]
	v_mfma_f32_16x16x32_bf16 v[42:45], v[172:175], v[184:187], v[42:45]
	v_mfma_f32_16x16x32_bf16 v[46:49], v[164:167], v[220:223], v[46:49]
	v_mfma_f32_16x16x32_bf16 v[34:37], v[172:175], v[220:223], v[34:37]
	v_mfma_f32_16x16x32_bf16 v[98:101], v[164:167], v[224:227], v[98:101]
	v_mfma_f32_16x16x32_bf16 v[38:41], v[172:175], v[224:227], v[38:41]
	v_mfma_f32_16x16x32_bf16 v[66:69], v[168:171], v[188:191], v[66:69]
	v_mfma_f32_16x16x32_bf16 v[50:53], v[176:179], v[188:191], v[50:53]
	v_mfma_f32_16x16x32_bf16 v[54:57], v[168:171], v[216:219], v[54:57]
	v_mfma_f32_16x16x32_bf16 v[42:45], v[176:179], v[216:219], v[42:45]
	v_mfma_f32_16x16x32_bf16 v[46:49], v[168:171], v[228:231], v[46:49]
	v_mfma_f32_16x16x32_bf16 v[34:37], v[176:179], v[228:231], v[34:37]
	v_mfma_f32_16x16x32_bf16 v[98:101], v[168:171], v[232:235], v[98:101]
	v_mfma_f32_16x16x32_bf16 v[38:41], v[176:179], v[232:235], v[38:41]
	s_barrier
; #define PG8_STAGE(bufoff, gbase, voff) do { _Pragma("unroll") for (int _i = 0; _i < 2; ++_i) \
;         __builtin_amdgcn_global_load_lds((const unsigned*)((const char*)(gbase) + (voff)[_i]), (LAS unsigned*)(lds + (bufoff) + ldsw + _i * 8192), 16, 0, 0); } while (0)
; #define PG8_LDA(dst, b, h) do { _Pragma("unroll") for (int m = 0; m < 4; ++m) _Pragma("unroll") for (int k = 0; k < 2; ++k) dst[m][k] = *(const LAS bf16x8*)(lds + PG8_SA(b, h) + ((aoff ^ (k * 64)) + m * 2048)); } while (0)
; #define PG8_MMA(ai, bj, At, Bt) do { __builtin_amdgcn_s_setprio(1); _Pragma("unroll") for (int m = 0; m < 4; ++m) _Pragma("unroll") for (int n = 0; n < 2; ++n) _Pragma("unroll") for (int k = 0; k < 2; ++k) \
;         acc[ai][bj][m][n] = __builtin_amdgcn_mfma_f32_16x16x32_bf16(Bt[n][k], At[m][k], acc[ai][bj][m][n], 0, 0, 0); __builtin_amdgcn_s_setprio(0); } while (0)
; #define PG8_WAIT_V(n) asm volatile("s_waitcnt vmcnt(" #n ")" ::: "memory")
; #define PG8_WAIT_L(n) asm volatile("s_waitcnt lgkmcnt(" #n ")" ::: "memory")
; #define PG8_BAR __builtin_amdgcn_s_barrier()
; #define PG8_SCHED __builtin_amdgcn_sched_barrier(0)
;     ...
;             PG8_LDA(At, 1, 1); PG8_STAGE(PG8_SB(1, 0), b3, voffB); PG8_STAGE(PG8_SB(1, 1), b3 + hstep, voffB); PG8_STAGE(PG8_SA(1, 0), a3, vs[0]);
;             PG8_WAIT_V(8); PG8_WAIT_L(0); PG8_BAR; if (do1) { PG8_MMA(1, 0, At, B0); PG8_MMA(1, 1, At, B1); } PG8_BAR; PG8_SCHED;
;         }
;         if (wr == 0) PG8_BAR;
	s_add_i32 s38, s42, s49
	v_lshl_add_u64 v[238:239], s[4:5], 0, v[146:147]
	s_mov_b32 m0, s38
	ds_read_b128 v[180:183], v207 offset:49152
	ds_read_b128 v[184:187], v207 offset:51200
	ds_read_b128 v[188:191], v208 offset:49152
	ds_read_b128 v[216:219], v208 offset:51200
	ds_read_b128 v[220:223], v207 offset:53248
	ds_read_b128 v[224:227], v207 offset:55296
	ds_read_b128 v[228:231], v208 offset:53248
	ds_read_b128 v[232:235], v208 offset:55296
	global_load_lds_dwordx4 v[238:239], off
	s_add_i32 m0, s38, 0x2000
	s_add_u32 s2, s2, 0x44000
	v_lshl_add_u64 v[238:239], s[4:5], 0, v[148:149]
	s_addc_u32 s3, s3, 0
	s_add_i32 s4, s43, s49
	global_load_lds_dwordx4 v[238:239], off
	v_lshl_add_u64 v[238:239], s[2:3], 0, v[146:147]
	s_mov_b32 m0, s4
	v_lshl_add_u64 v[192:193], v[192:193], 0, s[92:93]
	global_load_lds_dwordx4 v[238:239], off
	v_lshl_add_u64 v[238:239], s[2:3], 0, v[148:149]
	s_add_i32 m0, s4, 0x2000
	s_nop 0
	global_load_lds_dwordx4 v[238:239], off
	s_mov_b32 m0, s55
	s_nop 0
	global_load_lds_dwordx4 v[192:193], off
	v_lshl_add_u64 v[192:193], v[236:237], 0, s[92:93]
	s_mov_b32 m0, s56
	s_nop 0
	global_load_lds_dwordx4 v[192:193], off
	s_waitcnt vmcnt(8)
	s_waitcnt lgkmcnt(0)
	s_barrier
	s_waitcnt lgkmcnt(0)
	v_mfma_f32_16x16x32_bf16 v[94:97], v[130:133], v[180:183], v[94:97]
	v_mfma_f32_16x16x32_bf16 v[26:29], v[138:141], v[180:183], v[26:29]
	v_mfma_f32_16x16x32_bf16 v[90:93], v[130:133], v[184:187], v[90:93]
	v_mfma_f32_16x16x32_bf16 v[86:89], v[138:141], v[184:187], v[86:89]
	v_mfma_f32_16x16x32_bf16 v[82:85], v[130:133], v[220:223], v[82:85]
	v_mfma_f32_16x16x32_bf16 v[78:81], v[138:141], v[220:223], v[78:81]
	v_mfma_f32_16x16x32_bf16 v[74:77], v[130:133], v[224:227], v[74:77]
	v_mfma_f32_16x16x32_bf16 v[70:73], v[138:141], v[224:227], v[70:73]
	v_mfma_f32_16x16x32_bf16 v[94:97], v[134:137], v[188:191], v[94:97]
	v_mfma_f32_16x16x32_bf16 v[26:29], v[142:145], v[188:191], v[26:29]
	v_mfma_f32_16x16x32_bf16 v[90:93], v[134:137], v[216:219], v[90:93]
	v_mfma_f32_16x16x32_bf16 v[86:89], v[142:145], v[216:219], v[86:89]
	v_mfma_f32_16x16x32_bf16 v[82:85], v[134:137], v[228:231], v[82:85]
	v_mfma_f32_16x16x32_bf16 v[78:81], v[142:145], v[228:231], v[78:81]
	v_mfma_f32_16x16x32_bf16 v[74:77], v[134:137], v[232:235], v[74:77]
	v_mfma_f32_16x16x32_bf16 v[70:73], v[142:145], v[232:235], v[70:73]
	v_mfma_f32_16x16x32_bf16 v[30:33], v[164:167], v[180:183], v[30:33]
	v_mfma_f32_16x16x32_bf16 v[18:21], v[172:175], v[180:183], v[18:21]
	v_mfma_f32_16x16x32_bf16 v[22:25], v[164:167], v[184:187], v[22:25]
	v_mfma_f32_16x16x32_bf16 v[10:13], v[172:175], v[184:187], v[10:13]
	v_mfma_f32_16x16x32_bf16 v[14:17], v[164:167], v[220:223], v[14:17]
	v_mfma_f32_16x16x32_bf16 v[2:5], v[172:175], v[220:223], v[2:5]
	v_mfma_f32_16x16x32_bf16 v[62:65], v[164:167], v[224:227], v[62:65]
	v_mfma_f32_16x16x32_bf16 v[6:9], v[172:175], v[224:227], v[6:9]
	v_mfma_f32_16x16x32_bf16 v[30:33], v[168:171], v[188:191], v[30:33]
	v_mfma_f32_16x16x32_bf16 v[18:21], v[176:179], v[188:191], v[18:21]
	v_mfma_f32_16x16x32_bf16 v[22:25], v[168:171], v[216:219], v[22:25]
	v_mfma_f32_16x16x32_bf16 v[10:13], v[176:179], v[216:219], v[10:13]
	v_mfma_f32_16x16x32_bf16 v[14:17], v[168:171], v[228:231], v[14:17]
	v_mfma_f32_16x16x32_bf16 v[2:5], v[176:179], v[228:231], v[2:5]
	v_mfma_f32_16x16x32_bf16 v[62:65], v[168:171], v[232:235], v[62:65]
	v_mfma_f32_16x16x32_bf16 v[6:9], v[176:179], v[232:235], v[6:9]
	s_barrier
	s_add_i32 s41, s41, 2
	s_add_u32 s37, s37, 0x8000
	s_addc_u32 s40, s40, 0
	s_add_u32 s0, s0, 0x100
	s_addc_u32 s1, s1, 0
	s_cmp_gt_u32 s41, 13
	s_cbranch_scc0 .LBB0_557
	s_and_b64 vcc, exec, s[80:81]
	s_cbranch_vccz .LBB0_560
	s_barrier

; #define PG8_STAGE(bufoff, gbase, voff) do { _Pragma("unroll") for (int _i = 0; _i < 2; ++_i) \
;         __builtin_amdgcn_global_load_lds((const unsigned*)((const char*)(gbase) + (voff)[_i]), (LAS unsigned*)(lds + (bufoff) + ldsw + _i * 8192), 16, 0, 0); } while (0)
; #define PG8_LDA(dst, b, h) do { _Pragma("unroll") for (int m = 0; m < 4; ++m) _Pragma("unroll") for (int k = 0; k < 2; ++k) dst[m][k] = *(const LAS bf16x8*)(lds + PG8_SA(b, h) + ((aoff ^ (k * 64)) + m * 2048)); } while (0)
; #define PG8_LDB(dst, b, h) do { _Pragma("unroll") for (int n = 0; n < 2; ++n) _Pragma("unroll") for (int k = 0; k < 2; ++k) dst[n][k] = *(const LAS bf16x8*)(lds + PG8_SB(b, h) + ((boff ^ (k * 64)) + n * 2048)); } while (0)
; #define PG8_MMA(ai, bj, At, Bt) do { __builtin_amdgcn_s_setprio(1); _Pragma("unroll") for (int m = 0; m < 4; ++m) _Pragma("unroll") for (int n = 0; n < 2; ++n) _Pragma("unroll") for (int k = 0; k < 2; ++k) \
;         acc[ai][bj][m][n] = __builtin_amdgcn_mfma_f32_16x16x32_bf16(Bt[n][k], At[m][k], acc[ai][bj][m][n], 0, 0, 0); __builtin_amdgcn_s_setprio(0); } while (0)
; #define PG8_WAIT_V(n) asm volatile("s_waitcnt vmcnt(" #n ")" ::: "memory")
; #define PG8_WAIT_L(n) asm volatile("s_waitcnt lgkmcnt(" #n ")" ::: "memory")
; #define PG8_BAR __builtin_amdgcn_s_barrier()
; #define PG8_SCHED __builtin_amdgcn_sched_barrier(0)
;     ...
;         const int nt = (SPLITK && cur.kq >= 0) ? (cur.kq < 2 ? 12 : 10) : ntf;
;         const bool shortu = cur.pm >= SHORT_PM, do0 = (HALFM && cur.kq >= 0) ? cur.kq == 0 : (!shortu || wr == 0), do1 = (HALFM && cur.kq >= 0) ? cur.kq == 1 : !shortu;
;     ...
;             PG8_LDB(B0, 0, 0); PG8_LDB(B1, 0, 1); PG8_SCHED; PG8_LDA(At, 0, 0); PG8_STAGE(PG8_SA(1, 1), a1, voffA[1]);
;             PG8_WAIT_V(8); PG8_WAIT_L(0); PG8_BAR; if (do0) { PG8_MMA(0, 0, At, B0); PG8_MMA(0, 1, At, B1); } PG8_BAR; PG8_SCHED;
;             PG8_LDA(At, 0, 1); PG8_STAGE(PG8_SB(0, 0), b2, voffB); PG8_STAGE(PG8_SB(0, 1), b2 + hstep, voffB); PG8_STAGE(PG8_SA(0, 0), a2, vs[0]);
;             PG8_WAIT_V(8); PG8_WAIT_L(0); PG8_BAR; if (do1) { PG8_MMA(1, 0, At, B0); PG8_MMA(1, 1, At, B1); } PG8_BAR; PG8_SCHED;
.LBB0_1008:
	v_add_u32_e32 v2, s54, v226
	v_add_u32_e32 v134, s54, v227
	ds_read_b128 v[150:153], v2
	ds_read_b128 v[154:157], v134
	v_add_u32_e32 v2, s55, v226
	v_add_u32_e32 v134, s55, v227
	ds_read_b128 v[158:161], v2
	ds_read_b128 v[162:165], v134
	v_add_u32_e32 v2, s56, v226
	v_add_u32_e32 v138, s56, v227
	ds_read_b128 v[134:137], v2
	ds_read_b128 v[138:141], v138
	v_add_u32_e32 v2, s57, v226
	v_add_u32_e32 v146, s57, v227
	ds_read_b128 v[142:145], v2
	ds_read_b128 v[146:149], v146
	v_lshl_add_u64 v[224:225], v[222:223], 0, s[28:29]
	s_add_i32 m0, s23, 0xc000
	s_waitcnt lgkmcnt(0)
	ds_read_b128 v[190:193], v228
	ds_read_b128 v[178:181], v228 offset:2048
	ds_read_b128 v[194:197], v229
	ds_read_b128 v[182:185], v229 offset:2048
	ds_read_b128 v[174:177], v228 offset:4096
	ds_read_b128 v[166:169], v228 offset:6144
	ds_read_b128 v[186:189], v229 offset:4096
	ds_read_b128 v[170:173], v229 offset:6144
	global_load_lds_dwordx4 v[224:225], off
	v_lshl_add_u64 v[224:225], v[220:221], 0, s[28:29]
	s_add_i32 m0, s23, 0xe000
	v_cndmask_b32_e64 v2, 0, 1, s[26:27]
	global_load_lds_dwordx4 v[224:225], off
	s_waitcnt vmcnt(8)
	s_waitcnt lgkmcnt(0)
	v_cmp_ne_u32_e64 s[8:9], 1, v2
	s_andn2_b64 vcc, exec, s[26:27]
	s_barrier
	s_cbranch_vccnz .LBB0_1010
	s_waitcnt lgkmcnt(0)
	v_mfma_f32_16x16x32_bf16 v[130:133], v[150:153], v[190:193], v[130:133]
	v_mfma_f32_16x16x32_bf16 v[126:129], v[158:161], v[190:193], v[126:129]
	v_mfma_f32_16x16x32_bf16 v[114:117], v[150:153], v[178:181], v[114:117]
	v_mfma_f32_16x16x32_bf16 v[110:113], v[158:161], v[178:181], v[110:113]
	v_mfma_f32_16x16x32_bf16 v[98:101], v[150:153], v[174:177], v[98:101]
	v_mfma_f32_16x16x32_bf16 v[94:97], v[158:161], v[174:177], v[94:97]
	v_mfma_f32_16x16x32_bf16 v[82:85], v[150:153], v[166:169], v[82:85]
	v_mfma_f32_16x16x32_bf16 v[78:81], v[158:161], v[166:169], v[78:81]
	v_mfma_f32_16x16x32_bf16 v[130:133], v[154:157], v[194:197], v[130:133]
	v_mfma_f32_16x16x32_bf16 v[126:129], v[162:165], v[194:197], v[126:129]
	v_mfma_f32_16x16x32_bf16 v[114:117], v[154:157], v[182:185], v[114:117]
	v_mfma_f32_16x16x32_bf16 v[110:113], v[162:165], v[182:185], v[110:113]
	v_mfma_f32_16x16x32_bf16 v[98:101], v[154:157], v[186:189], v[98:101]
	v_mfma_f32_16x16x32_bf16 v[94:97], v[162:165], v[186:189], v[94:97]
	v_mfma_f32_16x16x32_bf16 v[82:85], v[154:157], v[170:173], v[82:85]
	v_mfma_f32_16x16x32_bf16 v[78:81], v[162:165], v[170:173], v[78:81]
	v_mfma_f32_16x16x32_bf16 v[122:125], v[134:137], v[190:193], v[122:125]
	v_mfma_f32_16x16x32_bf16 v[118:121], v[142:145], v[190:193], v[118:121]
	v_mfma_f32_16x16x32_bf16 v[106:109], v[134:137], v[178:181], v[106:109]
	v_mfma_f32_16x16x32_bf16 v[102:105], v[142:145], v[178:181], v[102:105]
	v_mfma_f32_16x16x32_bf16 v[90:93], v[134:137], v[174:177], v[90:93]
	v_mfma_f32_16x16x32_bf16 v[86:89], v[142:145], v[174:177], v[86:89]
	v_mfma_f32_16x16x32_bf16 v[74:77], v[134:137], v[166:169], v[74:77]
	v_mfma_f32_16x16x32_bf16 v[70:73], v[142:145], v[166:169], v[70:73]
	v_mfma_f32_16x16x32_bf16 v[122:125], v[138:141], v[194:197], v[122:125]
	v_mfma_f32_16x16x32_bf16 v[118:121], v[146:149], v[194:197], v[118:121]
	v_mfma_f32_16x16x32_bf16 v[106:109], v[138:141], v[182:185], v[106:109]
	v_mfma_f32_16x16x32_bf16 v[102:105], v[146:149], v[182:185], v[102:105]
	v_mfma_f32_16x16x32_bf16 v[90:93], v[138:141], v[186:189], v[90:93]
	v_mfma_f32_16x16x32_bf16 v[86:89], v[146:149], v[186:189], v[86:89]
	v_mfma_f32_16x16x32_bf16 v[74:77], v[138:141], v[170:173], v[74:77]
	v_mfma_f32_16x16x32_bf16 v[70:73], v[146:149], v[170:173], v[70:73]
.LBB0_1010:
	s_add_u32 s10, s90, s28
	s_addc_u32 s11, s91, s29
	s_add_u32 s30, s10, 0x4213700
	s_addc_u32 s31, s11, 0
	s_and_b64 s[10:11], s[6:7], exec
	v_cndmask_b32_e64 v2, v218, v4, s[6:7]
	v_cndmask_b32_e64 v224, v219, v5, s[6:7]
	s_cselect_b32 s35, s83, s31
	s_cselect_b32 s34, s82, s30
	s_cselect_b32 s31, s21, s64
	s_cselect_b32 s30, s20, s19
	s_barrier
	s_mov_b32 m0, s37
	v_lshl_add_u64 v[232:233], s[30:31], 0, v[202:203]
	s_add_u32 s10, s30, 0x40000
	s_waitcnt lgkmcnt(0)
	ds_read_b128 v[190:193], v228 offset:16384
	ds_read_b128 v[178:181], v228 offset:18432
	ds_read_b128 v[194:197], v229 offset:16384
	ds_read_b128 v[182:185], v229 offset:18432
	ds_read_b128 v[174:177], v228 offset:20480
	ds_read_b128 v[166:169], v228 offset:22528
	ds_read_b128 v[186:189], v229 offset:20480
	ds_read_b128 v[170:173], v229 offset:22528
	global_load_lds_dwordx4 v[232:233], off
	v_lshl_add_u64 v[232:233], s[30:31], 0, v[204:205]
	s_mov_b32 m0, s38
	s_addc_u32 s11, s31, 0
	global_load_lds_dwordx4 v[232:233], off
	v_lshl_add_u64 v[232:233], s[10:11], 0, v[202:203]
	s_mov_b32 m0, s39
	v_cndmask_b32_e64 v213, 0, 1, s[24:25]
	global_load_lds_dwordx4 v[232:233], off
	v_lshl_add_u64 v[232:233], s[10:11], 0, v[204:205]
	s_mov_b32 m0, s40
	v_cmp_ne_u32_e64 s[10:11], 1, v213
	global_load_lds_dwordx4 v[232:233], off
	s_mov_b32 m0, s23
	s_andn2_b64 vcc, exec, s[24:25]
	global_load_lds_dwordx4 v2, s[34:35]
	s_mov_b32 m0, s41
	s_nop 0
	global_load_lds_dwordx4 v224, s[34:35]
	s_waitcnt vmcnt(8)
	s_waitcnt lgkmcnt(0)
	s_barrier
	s_cbranch_vccnz .LBB0_1012
; #define PG8_STAGE(bufoff, gbase, voff) do { _Pragma("unroll") for (int _i = 0; _i < 2; ++_i) \
;         __builtin_amdgcn_global_load_lds((const unsigned*)((const char*)(gbase) + (voff)[_i]), (LAS unsigned*)(lds + (bufoff) + ldsw + _i * 8192), 16, 0, 0); } while (0)
; #define PG8_LDA(dst, b, h) do { _Pragma("unroll") for (int m = 0; m < 4; ++m) _Pragma("unroll") for (int k = 0; k < 2; ++k) dst[m][k] = *(const LAS bf16x8*)(lds + PG8_SA(b, h) + ((aoff ^ (k * 64)) + m * 2048)); } while (0)
; #define PG8_LDB(dst, b, h) do { _Pragma("unroll") for (int n = 0; n < 2; ++n) _Pragma("unroll") for (int k = 0; k < 2; ++k) dst[n][k] = *(const LAS bf16x8*)(lds + PG8_SB(b, h) + ((boff ^ (k * 64)) + n * 2048)); } while (0)
; #define PG8_MMA(ai, bj, At, Bt) do { __builtin_amdgcn_s_setprio(1); _Pragma("unroll") for (int m = 0; m < 4; ++m) _Pragma("unroll") for (int n = 0; n < 2; ++n) _Pragma("unroll") for (int k = 0; k < 2; ++k) \
;         acc[ai][bj][m][n] = __builtin_amdgcn_mfma_f32_16x16x32_bf16(Bt[n][k], At[m][k], acc[ai][bj][m][n], 0, 0, 0); __builtin_amdgcn_s_setprio(0); } while (0)
; #define PG8_WAIT_V(n) asm volatile("s_waitcnt vmcnt(" #n ")" ::: "memory")
; #define PG8_WAIT_L(n) asm volatile("s_waitcnt lgkmcnt(" #n ")" ::: "memory")
; #define PG8_BAR __builtin_amdgcn_s_barrier()
; #define PG8_SCHED __builtin_amdgcn_sched_barrier(0)
;     ...
;             PG8_LDA(At, 0, 1); PG8_STAGE(PG8_SB(0, 0), b2, voffB); PG8_STAGE(PG8_SB(0, 1), b2 + hstep, voffB); PG8_STAGE(PG8_SA(0, 0), a2, vs[0]);
;             PG8_WAIT_V(8); PG8_WAIT_L(0); PG8_BAR; if (do1) { PG8_MMA(1, 0, At, B0); PG8_MMA(1, 1, At, B1); } PG8_BAR; PG8_SCHED;
;             PG8_LDB(B0, 1, 0); PG8_LDB(B1, 1, 1); PG8_SCHED; PG8_LDA(At, 1, 0); PG8_STAGE(PG8_SA(0, 1), a2, vs[1]);
;             PG8_WAIT_V(8); PG8_WAIT_L(0); PG8_BAR; if (do0) { PG8_MMA(0, 0, At, B0); PG8_MMA(0, 1, At, B1); } PG8_BAR; PG8_SCHED;
	s_waitcnt lgkmcnt(0)
	v_mfma_f32_16x16x32_bf16 v[66:69], v[150:153], v[190:193], v[66:69]
	v_mfma_f32_16x16x32_bf16 v[62:65], v[158:161], v[190:193], v[62:65]
	v_mfma_f32_16x16x32_bf16 v[50:53], v[150:153], v[178:181], v[50:53]
	v_mfma_f32_16x16x32_bf16 v[46:49], v[158:161], v[178:181], v[46:49]
	v_mfma_f32_16x16x32_bf16 v[34:37], v[150:153], v[174:177], v[34:37]
	v_mfma_f32_16x16x32_bf16 v[30:33], v[158:161], v[174:177], v[30:33]
	v_mfma_f32_16x16x32_bf16 v[18:21], v[150:153], v[166:169], v[18:21]
	v_mfma_f32_16x16x32_bf16 v[14:17], v[158:161], v[166:169], v[14:17]
	v_mfma_f32_16x16x32_bf16 v[66:69], v[154:157], v[194:197], v[66:69]
	v_mfma_f32_16x16x32_bf16 v[62:65], v[162:165], v[194:197], v[62:65]
	v_mfma_f32_16x16x32_bf16 v[50:53], v[154:157], v[182:185], v[50:53]
	v_mfma_f32_16x16x32_bf16 v[46:49], v[162:165], v[182:185], v[46:49]
	v_mfma_f32_16x16x32_bf16 v[34:37], v[154:157], v[186:189], v[34:37]
	v_mfma_f32_16x16x32_bf16 v[30:33], v[162:165], v[186:189], v[30:33]
	v_mfma_f32_16x16x32_bf16 v[18:21], v[154:157], v[170:173], v[18:21]
	v_mfma_f32_16x16x32_bf16 v[14:17], v[162:165], v[170:173], v[14:17]
	v_mfma_f32_16x16x32_bf16 v[58:61], v[134:137], v[190:193], v[58:61]
	v_mfma_f32_16x16x32_bf16 v[54:57], v[142:145], v[190:193], v[54:57]
	v_mfma_f32_16x16x32_bf16 v[42:45], v[134:137], v[178:181], v[42:45]
	v_mfma_f32_16x16x32_bf16 v[38:41], v[142:145], v[178:181], v[38:41]
	v_mfma_f32_16x16x32_bf16 v[26:29], v[134:137], v[174:177], v[26:29]
	v_mfma_f32_16x16x32_bf16 v[22:25], v[142:145], v[174:177], v[22:25]
	v_mfma_f32_16x16x32_bf16 v[10:13], v[134:137], v[166:169], v[10:13]
	v_mfma_f32_16x16x32_bf16 v[6:9], v[142:145], v[166:169], v[6:9]
	v_mfma_f32_16x16x32_bf16 v[58:61], v[138:141], v[194:197], v[58:61]
	v_mfma_f32_16x16x32_bf16 v[54:57], v[146:149], v[194:197], v[54:57]
	v_mfma_f32_16x16x32_bf16 v[42:45], v[138:141], v[182:185], v[42:45]
	v_mfma_f32_16x16x32_bf16 v[38:41], v[146:149], v[182:185], v[38:41]
	v_mfma_f32_16x16x32_bf16 v[26:29], v[138:141], v[186:189], v[26:29]
	v_mfma_f32_16x16x32_bf16 v[22:25], v[146:149], v[186:189], v[22:25]
	v_mfma_f32_16x16x32_bf16 v[10:13], v[138:141], v[170:173], v[10:13]
	v_mfma_f32_16x16x32_bf16 v[6:9], v[146:149], v[170:173], v[6:9]
.LBB0_1012:
	v_cndmask_b32_e64 v213, v214, v215, s[6:7]
	v_cndmask_b32_e64 v225, v216, v217, s[6:7]
	s_barrier
	s_add_i32 s6, 0, 0x18000
	v_add_u32_e32 v134, s6, v226
	v_add_u32_e32 v135, s6, v227
	ds_read_b128 v[150:153], v134
	ds_read_b128 v[154:157], v135
	v_add_u32_e32 v134, s58, v226
	s_add_i32 s6, 0, 0x1c000
	v_add_u32_e32 v135, s58, v227
	ds_read_b128 v[158:161], v134
	ds_read_b128 v[162:165], v135
	v_add_u32_e32 v134, s6, v226
	v_add_u32_e32 v138, s6, v227
	v_add_u32_e32 v142, s59, v226
	v_add_u32_e32 v146, s59, v227
	ds_read_b128 v[134:137], v134
	ds_read_b128 v[138:141], v138
	ds_read_b128 v[142:145], v142
	ds_read_b128 v[146:149], v146
	s_mov_b32 m0, s42
	s_waitcnt lgkmcnt(0)
	ds_read_b128 v[190:193], v228 offset:32768
	ds_read_b128 v[178:181], v228 offset:34816
	ds_read_b128 v[194:197], v229 offset:32768
	ds_read_b128 v[182:185], v229 offset:34816
	ds_read_b128 v[174:177], v228 offset:36864
	ds_read_b128 v[166:169], v228 offset:38912
	ds_read_b128 v[186:189], v229 offset:36864
	ds_read_b128 v[170:173], v229 offset:38912
	global_load_lds_dwordx4 v213, s[34:35]
	s_mov_b32 m0, s43
	s_and_b64 vcc, exec, s[8:9]
	global_load_lds_dwordx4 v225, s[34:35]
	s_waitcnt vmcnt(8)
	s_waitcnt lgkmcnt(0)
	s_barrier
	s_cbranch_vccnz .LBB0_1014
	s_waitcnt lgkmcnt(0)
	v_mfma_f32_16x16x32_bf16 v[130:133], v[150:153], v[190:193], v[130:133]
	v_mfma_f32_16x16x32_bf16 v[126:129], v[158:161], v[190:193], v[126:129]
	v_mfma_f32_16x16x32_bf16 v[114:117], v[150:153], v[178:181], v[114:117]
	v_mfma_f32_16x16x32_bf16 v[110:113], v[158:161], v[178:181], v[110:113]
	v_mfma_f32_16x16x32_bf16 v[98:101], v[150:153], v[174:177], v[98:101]
	v_mfma_f32_16x16x32_bf16 v[94:97], v[158:161], v[174:177], v[94:97]
	v_mfma_f32_16x16x32_bf16 v[82:85], v[150:153], v[166:169], v[82:85]
	v_mfma_f32_16x16x32_bf16 v[78:81], v[158:161], v[166:169], v[78:81]
	v_mfma_f32_16x16x32_bf16 v[130:133], v[154:157], v[194:197], v[130:133]
	v_mfma_f32_16x16x32_bf16 v[126:129], v[162:165], v[194:197], v[126:129]
	v_mfma_f32_16x16x32_bf16 v[114:117], v[154:157], v[182:185], v[114:117]
	v_mfma_f32_16x16x32_bf16 v[110:113], v[162:165], v[182:185], v[110:113]
	v_mfma_f32_16x16x32_bf16 v[98:101], v[154:157], v[186:189], v[98:101]
	v_mfma_f32_16x16x32_bf16 v[94:97], v[162:165], v[186:189], v[94:97]
	v_mfma_f32_16x16x32_bf16 v[82:85], v[154:157], v[170:173], v[82:85]
	v_mfma_f32_16x16x32_bf16 v[78:81], v[162:165], v[170:173], v[78:81]
	v_mfma_f32_16x16x32_bf16 v[122:125], v[134:137], v[190:193], v[122:125]
	v_mfma_f32_16x16x32_bf16 v[118:121], v[142:145], v[190:193], v[118:121]
	v_mfma_f32_16x16x32_bf16 v[106:109], v[134:137], v[178:181], v[106:109]
	v_mfma_f32_16x16x32_bf16 v[102:105], v[142:145], v[178:181], v[102:105]
	v_mfma_f32_16x16x32_bf16 v[90:93], v[134:137], v[174:177], v[90:93]
	v_mfma_f32_16x16x32_bf16 v[86:89], v[142:145], v[174:177], v[86:89]
	v_mfma_f32_16x16x32_bf16 v[74:77], v[134:137], v[166:169], v[74:77]
	v_mfma_f32_16x16x32_bf16 v[70:73], v[142:145], v[166:169], v[70:73]
	v_mfma_f32_16x16x32_bf16 v[122:125], v[138:141], v[194:197], v[122:125]
	v_mfma_f32_16x16x32_bf16 v[118:121], v[146:149], v[194:197], v[118:121]
	v_mfma_f32_16x16x32_bf16 v[106:109], v[138:141], v[182:185], v[106:109]
	v_mfma_f32_16x16x32_bf16 v[102:105], v[146:149], v[182:185], v[102:105]
	v_mfma_f32_16x16x32_bf16 v[90:93], v[138:141], v[186:189], v[90:93]
	v_mfma_f32_16x16x32_bf16 v[86:89], v[146:149], v[186:189], v[86:89]
	v_mfma_f32_16x16x32_bf16 v[74:77], v[138:141], v[170:173], v[74:77]
	v_mfma_f32_16x16x32_bf16 v[70:73], v[146:149], v[170:173], v[70:73]
; #define PG8_STAGE(bufoff, gbase, voff) do { _Pragma("unroll") for (int _i = 0; _i < 2; ++_i) \
;         __builtin_amdgcn_global_load_lds((const unsigned*)((const char*)(gbase) + (voff)[_i]), (LAS unsigned*)(lds + (bufoff) + ldsw + _i * 8192), 16, 0, 0); } while (0)
; #define PG8_LDA(dst, b, h) do { _Pragma("unroll") for (int m = 0; m < 4; ++m) _Pragma("unroll") for (int k = 0; k < 2; ++k) dst[m][k] = *(const LAS bf16x8*)(lds + PG8_SA(b, h) + ((aoff ^ (k * 64)) + m * 2048)); } while (0)
; #define PG8_MMA(ai, bj, At, Bt) do { __builtin_amdgcn_s_setprio(1); _Pragma("unroll") for (int m = 0; m < 4; ++m) _Pragma("unroll") for (int n = 0; n < 2; ++n) _Pragma("unroll") for (int k = 0; k < 2; ++k) \
;         acc[ai][bj][m][n] = __builtin_amdgcn_mfma_f32_16x16x32_bf16(Bt[n][k], At[m][k], acc[ai][bj][m][n], 0, 0, 0); __builtin_amdgcn_s_setprio(0); } while (0)
; #define PG8_WAIT_V(n) asm volatile("s_waitcnt vmcnt(" #n ")" ::: "memory")
; #define PG8_WAIT_L(n) asm volatile("s_waitcnt lgkmcnt(" #n ")" ::: "memory")
; #define PG8_BAR __builtin_amdgcn_s_barrier()
; #define PG8_SCHED __builtin_amdgcn_sched_barrier(0)
;     ...
;             PG8_LDA(At, 1, 1); PG8_STAGE(PG8_SB(1, 0), b3, voffB); PG8_STAGE(PG8_SB(1, 1), b3 + hstep, voffB); PG8_STAGE(PG8_SA(1, 0), a3, vs[0]);
;             PG8_WAIT_V(8); PG8_WAIT_L(0); PG8_BAR; if (do1) { PG8_MMA(1, 0, At, B0); PG8_MMA(1, 1, At, B1); } PG8_BAR; PG8_SCHED;
;         }
.LBB0_1014:
	v_mov_b32_e32 v225, v3
	s_add_u32 s6, s30, 0x4000
	v_lshl_add_u64 v[232:233], s[34:35], 0, v[2:3]
	v_lshl_add_u64 v[224:225], s[34:35], 0, v[224:225]
	s_addc_u32 s7, s31, 0
	s_barrier
	s_mov_b32 m0, s47
	v_lshl_add_u64 v[234:235], s[6:7], 0, v[202:203]
	s_waitcnt lgkmcnt(0)
	ds_read_b128 v[190:193], v228 offset:49152
	ds_read_b128 v[178:181], v228 offset:51200
	ds_read_b128 v[194:197], v229 offset:49152
	ds_read_b128 v[182:185], v229 offset:51200
	ds_read_b128 v[174:177], v228 offset:53248
	ds_read_b128 v[166:169], v228 offset:55296
	ds_read_b128 v[186:189], v229 offset:53248
	ds_read_b128 v[170:173], v229 offset:55296
	global_load_lds_dwordx4 v[234:235], off
	v_lshl_add_u64 v[234:235], s[6:7], 0, v[204:205]
	s_add_u32 s6, s30, 0x44000
	s_mov_b32 m0, s48
	s_addc_u32 s7, s31, 0
	global_load_lds_dwordx4 v[234:235], off
	v_lshl_add_u64 v[234:235], s[6:7], 0, v[202:203]
	s_mov_b32 m0, s51
	v_lshl_add_u64 v[232:233], v[232:233], 0, s[16:17]
	global_load_lds_dwordx4 v[234:235], off
	v_lshl_add_u64 v[234:235], s[6:7], 0, v[204:205]
	s_mov_b32 m0, s52
	v_lshl_add_u64 v[224:225], v[224:225], 0, s[16:17]
	global_load_lds_dwordx4 v[234:235], off
	s_mov_b32 m0, s49
	s_and_b64 vcc, exec, s[10:11]
	global_load_lds_dwordx4 v[232:233], off
	s_mov_b32 m0, s50
	s_nop 0
	global_load_lds_dwordx4 v[224:225], off
	s_waitcnt vmcnt(8)
	s_waitcnt lgkmcnt(0)
	s_barrier
	s_cbranch_vccnz .LBB0_1005
	s_waitcnt lgkmcnt(0)
	v_mfma_f32_16x16x32_bf16 v[66:69], v[150:153], v[190:193], v[66:69]
	v_mfma_f32_16x16x32_bf16 v[62:65], v[158:161], v[190:193], v[62:65]
	v_mfma_f32_16x16x32_bf16 v[50:53], v[150:153], v[178:181], v[50:53]
	v_mfma_f32_16x16x32_bf16 v[46:49], v[158:161], v[178:181], v[46:49]
	v_mfma_f32_16x16x32_bf16 v[34:37], v[150:153], v[174:177], v[34:37]
	v_mfma_f32_16x16x32_bf16 v[30:33], v[158:161], v[174:177], v[30:33]
	v_mfma_f32_16x16x32_bf16 v[18:21], v[150:153], v[166:169], v[18:21]
	v_mfma_f32_16x16x32_bf16 v[14:17], v[158:161], v[166:169], v[14:17]
	v_mfma_f32_16x16x32_bf16 v[66:69], v[154:157], v[194:197], v[66:69]
	v_mfma_f32_16x16x32_bf16 v[62:65], v[162:165], v[194:197], v[62:65]
	v_mfma_f32_16x16x32_bf16 v[50:53], v[154:157], v[182:185], v[50:53]
	v_mfma_f32_16x16x32_bf16 v[46:49], v[162:165], v[182:185], v[46:49]
	v_mfma_f32_16x16x32_bf16 v[34:37], v[154:157], v[186:189], v[34:37]
	v_mfma_f32_16x16x32_bf16 v[30:33], v[162:165], v[186:189], v[30:33]
	v_mfma_f32_16x16x32_bf16 v[18:21], v[154:157], v[170:173], v[18:21]
	v_mfma_f32_16x16x32_bf16 v[14:17], v[162:165], v[170:173], v[14:17]
	v_mfma_f32_16x16x32_bf16 v[58:61], v[134:137], v[190:193], v[58:61]
	v_mfma_f32_16x16x32_bf16 v[54:57], v[142:145], v[190:193], v[54:57]
	v_mfma_f32_16x16x32_bf16 v[42:45], v[134:137], v[178:181], v[42:45]
	v_mfma_f32_16x16x32_bf16 v[38:41], v[142:145], v[178:181], v[38:41]
	v_mfma_f32_16x16x32_bf16 v[26:29], v[134:137], v[174:177], v[26:29]
	v_mfma_f32_16x16x32_bf16 v[22:25], v[142:145], v[174:177], v[22:25]
	v_mfma_f32_16x16x32_bf16 v[10:13], v[134:137], v[166:169], v[10:13]
	v_mfma_f32_16x16x32_bf16 v[6:9], v[142:145], v[166:169], v[6:9]
	v_mfma_f32_16x16x32_bf16 v[58:61], v[138:141], v[194:197], v[58:61]
	v_mfma_f32_16x16x32_bf16 v[54:57], v[146:149], v[194:197], v[54:57]
	v_mfma_f32_16x16x32_bf16 v[42:45], v[138:141], v[182:185], v[42:45]
	v_mfma_f32_16x16x32_bf16 v[38:41], v[146:149], v[182:185], v[38:41]
	v_mfma_f32_16x16x32_bf16 v[26:29], v[138:141], v[186:189], v[26:29]
	v_mfma_f32_16x16x32_bf16 v[22:25], v[146:149], v[186:189], v[22:25]
	v_mfma_f32_16x16x32_bf16 v[10:13], v[138:141], v[170:173], v[10:13]
	v_mfma_f32_16x16x32_bf16 v[6:9], v[146:149], v[170:173], v[6:9]
	s_branch .LBB0_1005

; #define PG8_STAGE(bufoff, gbase, voff) do { _Pragma("unroll") for (int _i = 0; _i < 2; ++_i) \
;         __builtin_amdgcn_global_load_lds((const unsigned*)((const char*)(gbase) + (voff)[_i]), (LAS unsigned*)(lds + (bufoff) + ldsw + _i * 8192), 16, 0, 0); } while (0)
; #define PG8_LDA(dst, b, h) do { _Pragma("unroll") for (int m = 0; m < 4; ++m) _Pragma("unroll") for (int k = 0; k < 2; ++k) dst[m][k] = *(const LAS bf16x8*)(lds + PG8_SA(b, h) + ((aoff ^ (k * 64)) + m * 2048)); } while (0)
; #define PG8_LDB(dst, b, h) do { _Pragma("unroll") for (int n = 0; n < 2; ++n) _Pragma("unroll") for (int k = 0; k < 2; ++k) dst[n][k] = *(const LAS bf16x8*)(lds + PG8_SB(b, h) + ((boff ^ (k * 64)) + n * 2048)); } while (0)
; #define PG8_MMA(ai, bj, At, Bt) do { __builtin_amdgcn_s_setprio(1); _Pragma("unroll") for (int m = 0; m < 4; ++m) _Pragma("unroll") for (int n = 0; n < 2; ++n) _Pragma("unroll") for (int k = 0; k < 2; ++k) \
;         acc[ai][bj][m][n] = __builtin_amdgcn_mfma_f32_16x16x32_bf16(Bt[n][k], At[m][k], acc[ai][bj][m][n], 0, 0, 0); __builtin_amdgcn_s_setprio(0); } while (0)
; #define PG8_WAIT_V(n) asm volatile("s_waitcnt vmcnt(" #n ")" ::: "memory")
; #define PG8_WAIT_L(n) asm volatile("s_waitcnt lgkmcnt(" #n ")" ::: "memory")
; #define PG8_BAR __builtin_amdgcn_s_barrier()
; #define PG8_SCHED __builtin_amdgcn_sched_barrier(0)
;     ...
;         const int nt = (SPLITK && cur.kq >= 0) ? (cur.kq < 2 ? 12 : 10) : ntf;
;         const bool shortu = cur.pm >= SHORT_PM, do0 = (HALFM && cur.kq >= 0) ? cur.kq == 0 : (!shortu || wr == 0), do1 = (HALFM && cur.kq >= 0) ? cur.kq == 1 : !shortu;
;     ...
;             PG8_LDB(B0, 0, 0); PG8_LDB(B1, 0, 1); PG8_SCHED; PG8_LDA(At, 0, 0); PG8_STAGE(PG8_SA(1, 1), a1, voffA[1]);
;             PG8_WAIT_V(8); PG8_WAIT_L(0); PG8_BAR; if (do0) { PG8_MMA(0, 0, At, B0); PG8_MMA(0, 1, At, B1); } PG8_BAR; PG8_SCHED;
;             PG8_LDA(At, 0, 1); PG8_STAGE(PG8_SB(0, 0), b2, voffB); PG8_STAGE(PG8_SB(0, 1), b2 + hstep, voffB); PG8_STAGE(PG8_SA(0, 0), a2, vs[0]);
;             PG8_WAIT_V(8); PG8_WAIT_L(0); PG8_BAR; if (do1) { PG8_MMA(1, 0, At, B0); PG8_MMA(1, 1, At, B1); } PG8_BAR; PG8_SCHED;
.LBB0_1100:
	ds_read_b128 v[150:153], v218
	ds_read_b128 v[154:157], v219
	ds_read_b128 v[158:161], v220
	ds_read_b128 v[162:165], v221
	ds_read_b128 v[134:137], v222
	ds_read_b128 v[138:141], v223
	ds_read_b128 v[142:145], v224
	ds_read_b128 v[146:149], v225
	v_lshl_add_u64 v[4:5], s[22:23], 0, v[212:213]
	s_add_i32 m0, s28, 0xc000
	s_waitcnt lgkmcnt(0)
	ds_read_b128 v[190:193], v226
	ds_read_b128 v[178:181], v226 offset:2048
	ds_read_b128 v[194:197], v227
	ds_read_b128 v[182:185], v227 offset:2048
	ds_read_b128 v[174:177], v226 offset:4096
	ds_read_b128 v[166:169], v226 offset:6144
	ds_read_b128 v[186:189], v227 offset:4096
	ds_read_b128 v[170:173], v227 offset:6144
	global_load_lds_dwordx4 v[4:5], off
	v_lshl_add_u64 v[4:5], s[22:23], 0, v[214:215]
	s_add_i32 m0, s28, 0xe000
	v_cmp_ne_u32_e64 s[6:7], 1, v228
	global_load_lds_dwordx4 v[4:5], off
	s_waitcnt vmcnt(8)
	s_waitcnt lgkmcnt(0)
	s_andn2_b64 vcc, exec, s[20:21]
	s_barrier
	s_cbranch_vccnz .LBB0_1102
	s_waitcnt lgkmcnt(0)
	v_mfma_f32_16x16x32_bf16 v[66:69], v[150:153], v[190:193], v[66:69]
	v_mfma_f32_16x16x32_bf16 v[62:65], v[158:161], v[190:193], v[62:65]
	v_mfma_f32_16x16x32_bf16 v[50:53], v[150:153], v[178:181], v[50:53]
	v_mfma_f32_16x16x32_bf16 v[46:49], v[158:161], v[178:181], v[46:49]
	v_mfma_f32_16x16x32_bf16 v[34:37], v[150:153], v[174:177], v[34:37]
	v_mfma_f32_16x16x32_bf16 v[30:33], v[158:161], v[174:177], v[30:33]
	v_mfma_f32_16x16x32_bf16 v[18:21], v[150:153], v[166:169], v[18:21]
	v_mfma_f32_16x16x32_bf16 v[14:17], v[158:161], v[166:169], v[14:17]
	v_mfma_f32_16x16x32_bf16 v[66:69], v[154:157], v[194:197], v[66:69]
	v_mfma_f32_16x16x32_bf16 v[62:65], v[162:165], v[194:197], v[62:65]
	v_mfma_f32_16x16x32_bf16 v[50:53], v[154:157], v[182:185], v[50:53]
	v_mfma_f32_16x16x32_bf16 v[46:49], v[162:165], v[182:185], v[46:49]
	v_mfma_f32_16x16x32_bf16 v[34:37], v[154:157], v[186:189], v[34:37]
	v_mfma_f32_16x16x32_bf16 v[30:33], v[162:165], v[186:189], v[30:33]
	v_mfma_f32_16x16x32_bf16 v[18:21], v[154:157], v[170:173], v[18:21]
	v_mfma_f32_16x16x32_bf16 v[14:17], v[162:165], v[170:173], v[14:17]
	v_mfma_f32_16x16x32_bf16 v[58:61], v[134:137], v[190:193], v[58:61]
	v_mfma_f32_16x16x32_bf16 v[54:57], v[142:145], v[190:193], v[54:57]
	v_mfma_f32_16x16x32_bf16 v[42:45], v[134:137], v[178:181], v[42:45]
	v_mfma_f32_16x16x32_bf16 v[38:41], v[142:145], v[178:181], v[38:41]
	v_mfma_f32_16x16x32_bf16 v[26:29], v[134:137], v[174:177], v[26:29]
	v_mfma_f32_16x16x32_bf16 v[22:25], v[142:145], v[174:177], v[22:25]
	v_mfma_f32_16x16x32_bf16 v[10:13], v[134:137], v[166:169], v[10:13]
	v_mfma_f32_16x16x32_bf16 v[4:7], v[142:145], v[166:169], v[6:9]
	v_mfma_f32_16x16x32_bf16 v[58:61], v[138:141], v[194:197], v[58:61]
	v_mfma_f32_16x16x32_bf16 v[54:57], v[146:149], v[194:197], v[54:57]
	v_mfma_f32_16x16x32_bf16 v[42:45], v[138:141], v[182:185], v[42:45]
	v_mfma_f32_16x16x32_bf16 v[38:41], v[146:149], v[182:185], v[38:41]
	v_mfma_f32_16x16x32_bf16 v[26:29], v[138:141], v[186:189], v[26:29]
	v_mfma_f32_16x16x32_bf16 v[22:25], v[146:149], v[186:189], v[22:25]
	v_mfma_f32_16x16x32_bf16 v[10:13], v[138:141], v[170:173], v[10:13]
	v_mfma_f32_16x16x32_bf16 v[6:9], v[146:149], v[170:173], v[4:7]
.LBB0_1102:
	s_add_u32 s8, s22, 0x4000
	s_addc_u32 s9, s23, 0
	s_cmp_eq_u32 s61, s59
	s_cselect_b32 s27, s15, s9
	s_cselect_b32 s26, s14, s8
	s_cselect_b32 s25, s17, s63
	s_cselect_b32 s24, s16, s62
	s_barrier
	s_mov_b32 m0, s29
	v_lshl_add_u64 v[4:5], s[24:25], 0, v[208:209]
	s_add_u32 s8, s24, 0xb0000
	s_waitcnt lgkmcnt(0)
	ds_read_b128 v[190:193], v226 offset:16384
	ds_read_b128 v[178:181], v226 offset:18432
	ds_read_b128 v[194:197], v227 offset:16384
	ds_read_b128 v[182:185], v227 offset:18432
	ds_read_b128 v[174:177], v226 offset:20480
	ds_read_b128 v[166:169], v226 offset:22528
	ds_read_b128 v[186:189], v227 offset:20480
	ds_read_b128 v[170:173], v227 offset:22528
	global_load_lds_dwordx4 v[4:5], off
	v_lshl_add_u64 v[4:5], s[24:25], 0, v[210:211]
	s_mov_b32 m0, s30
	s_addc_u32 s9, s25, 0
	global_load_lds_dwordx4 v[4:5], off
	v_lshl_add_u64 v[4:5], s[8:9], 0, v[208:209]
	s_mov_b32 m0, s31
	v_cndmask_b32_e64 v3, 0, 1, s[18:19]
	global_load_lds_dwordx4 v[4:5], off
	v_lshl_add_u64 v[4:5], s[8:9], 0, v[210:211]
	s_mov_b32 m0, s34
	v_cmp_ne_u32_e64 s[8:9], 1, v3
	global_load_lds_dwordx4 v[4:5], off
	v_lshl_add_u64 v[4:5], s[26:27], 0, v[200:201]
	s_mov_b32 m0, s28
	s_andn2_b64 vcc, exec, s[18:19]
	global_load_lds_dwordx4 v[4:5], off
	v_lshl_add_u64 v[4:5], s[26:27], 0, v[202:203]
	s_mov_b32 m0, s35
	s_nop 0
	global_load_lds_dwordx4 v[4:5], off
	s_waitcnt vmcnt(8)
	s_waitcnt lgkmcnt(0)
	s_barrier
	s_cbranch_vccnz .LBB0_1104
	s_waitcnt lgkmcnt(0)
	v_mfma_f32_16x16x32_bf16 v[130:133], v[150:153], v[190:193], v[130:133]
	v_mfma_f32_16x16x32_bf16 v[126:129], v[158:161], v[190:193], v[126:129]
	v_mfma_f32_16x16x32_bf16 v[114:117], v[150:153], v[178:181], v[114:117]
	v_mfma_f32_16x16x32_bf16 v[110:113], v[158:161], v[178:181], v[110:113]
	v_mfma_f32_16x16x32_bf16 v[98:101], v[150:153], v[174:177], v[98:101]
	v_mfma_f32_16x16x32_bf16 v[94:97], v[158:161], v[174:177], v[94:97]
	v_mfma_f32_16x16x32_bf16 v[82:85], v[150:153], v[166:169], v[82:85]
	v_mfma_f32_16x16x32_bf16 v[78:81], v[158:161], v[166:169], v[78:81]
	v_mfma_f32_16x16x32_bf16 v[130:133], v[154:157], v[194:197], v[130:133]
	v_mfma_f32_16x16x32_bf16 v[126:129], v[162:165], v[194:197], v[126:129]
	v_mfma_f32_16x16x32_bf16 v[114:117], v[154:157], v[182:185], v[114:117]
	v_mfma_f32_16x16x32_bf16 v[110:113], v[162:165], v[182:185], v[110:113]
	v_mfma_f32_16x16x32_bf16 v[98:101], v[154:157], v[186:189], v[98:101]
	v_mfma_f32_16x16x32_bf16 v[94:97], v[162:165], v[186:189], v[94:97]
	v_mfma_f32_16x16x32_bf16 v[82:85], v[154:157], v[170:173], v[82:85]
	v_mfma_f32_16x16x32_bf16 v[78:81], v[162:165], v[170:173], v[78:81]
	v_mfma_f32_16x16x32_bf16 v[122:125], v[134:137], v[190:193], v[122:125]
	v_mfma_f32_16x16x32_bf16 v[118:121], v[142:145], v[190:193], v[118:121]
	v_mfma_f32_16x16x32_bf16 v[106:109], v[134:137], v[178:181], v[106:109]
	v_mfma_f32_16x16x32_bf16 v[102:105], v[142:145], v[178:181], v[102:105]
	v_mfma_f32_16x16x32_bf16 v[90:93], v[134:137], v[174:177], v[90:93]
	v_mfma_f32_16x16x32_bf16 v[86:89], v[142:145], v[174:177], v[86:89]
	v_mfma_f32_16x16x32_bf16 v[74:77], v[134:137], v[166:169], v[74:77]
	v_mfma_f32_16x16x32_bf16 v[70:73], v[142:145], v[166:169], v[70:73]
	v_mfma_f32_16x16x32_bf16 v[122:125], v[138:141], v[194:197], v[122:125]
	v_mfma_f32_16x16x32_bf16 v[118:121], v[146:149], v[194:197], v[118:121]
	v_mfma_f32_16x16x32_bf16 v[106:109], v[138:141], v[182:185], v[106:109]
	v_mfma_f32_16x16x32_bf16 v[102:105], v[146:149], v[182:185], v[102:105]
	v_mfma_f32_16x16x32_bf16 v[90:93], v[138:141], v[186:189], v[90:93]
	v_mfma_f32_16x16x32_bf16 v[86:89], v[146:149], v[186:189], v[86:89]
	v_mfma_f32_16x16x32_bf16 v[74:77], v[138:141], v[170:173], v[74:77]
	v_mfma_f32_16x16x32_bf16 v[70:73], v[146:149], v[170:173], v[70:73]
; #define PG8_STAGE(bufoff, gbase, voff) do { _Pragma("unroll") for (int _i = 0; _i < 2; ++_i) \
;         __builtin_amdgcn_global_load_lds((const unsigned*)((const char*)(gbase) + (voff)[_i]), (LAS unsigned*)(lds + (bufoff) + ldsw + _i * 8192), 16, 0, 0); } while (0)
; #define PG8_LDA(dst, b, h) do { _Pragma("unroll") for (int m = 0; m < 4; ++m) _Pragma("unroll") for (int k = 0; k < 2; ++k) dst[m][k] = *(const LAS bf16x8*)(lds + PG8_SA(b, h) + ((aoff ^ (k * 64)) + m * 2048)); } while (0)
; #define PG8_LDB(dst, b, h) do { _Pragma("unroll") for (int n = 0; n < 2; ++n) _Pragma("unroll") for (int k = 0; k < 2; ++k) dst[n][k] = *(const LAS bf16x8*)(lds + PG8_SB(b, h) + ((boff ^ (k * 64)) + n * 2048)); } while (0)
; #define PG8_MMA(ai, bj, At, Bt) do { __builtin_amdgcn_s_setprio(1); _Pragma("unroll") for (int m = 0; m < 4; ++m) _Pragma("unroll") for (int n = 0; n < 2; ++n) _Pragma("unroll") for (int k = 0; k < 2; ++k) \
;         acc[ai][bj][m][n] = __builtin_amdgcn_mfma_f32_16x16x32_bf16(Bt[n][k], At[m][k], acc[ai][bj][m][n], 0, 0, 0); __builtin_amdgcn_s_setprio(0); } while (0)
; #define PG8_WAIT_V(n) asm volatile("s_waitcnt vmcnt(" #n ")" ::: "memory")
; #define PG8_WAIT_L(n) asm volatile("s_waitcnt lgkmcnt(" #n ")" ::: "memory")
; #define PG8_BAR __builtin_amdgcn_s_barrier()
; #define PG8_SCHED __builtin_amdgcn_sched_barrier(0)
;     ...
;             PG8_LDB(B0, 1, 0); PG8_LDB(B1, 1, 1); PG8_SCHED; PG8_LDA(At, 1, 0); PG8_STAGE(PG8_SA(0, 1), a2, vs[1]);
;             PG8_WAIT_V(8); PG8_WAIT_L(0); PG8_BAR; if (do0) { PG8_MMA(0, 0, At, B0); PG8_MMA(0, 1, At, B1); } PG8_BAR; PG8_SCHED;
.LBB0_1104:
	s_barrier
	s_add_i32 s64, 0, 0x18000
	v_add_u32_e32 v3, s64, v199
	v_add_u32_e32 v4, s64, v216
	ds_read_b128 v[150:153], v3
	ds_read_b128 v[154:157], v4
	v_add_u32_e32 v3, s48, v199
	s_add_i32 s64, 0, 0x1c000
	v_add_u32_e32 v4, s48, v216
	ds_read_b128 v[158:161], v3
	ds_read_b128 v[162:165], v4
	v_add_u32_e32 v3, s64, v199
	v_add_u32_e32 v4, s64, v216
	ds_read_b128 v[134:137], v3
	ds_read_b128 v[138:141], v4
	v_add_u32_e32 v3, s49, v199
	v_add_u32_e32 v4, s49, v216
	ds_read_b128 v[142:145], v3
	ds_read_b128 v[146:149], v4
	s_mov_b32 m0, s36
	v_lshl_add_u64 v[4:5], s[26:27], 0, v[204:205]
	s_waitcnt lgkmcnt(0)
	ds_read_b128 v[190:193], v226 offset:32768
	ds_read_b128 v[178:181], v226 offset:34816
	ds_read_b128 v[194:197], v227 offset:32768
	ds_read_b128 v[182:185], v227 offset:34816
	ds_read_b128 v[174:177], v226 offset:36864
	ds_read_b128 v[166:169], v226 offset:38912
	ds_read_b128 v[186:189], v227 offset:36864
	ds_read_b128 v[170:173], v227 offset:38912
	global_load_lds_dwordx4 v[4:5], off
	v_lshl_add_u64 v[4:5], s[26:27], 0, v[206:207]
	s_mov_b32 m0, s37
	s_and_b64 vcc, exec, s[6:7]
	global_load_lds_dwordx4 v[4:5], off
	s_waitcnt vmcnt(8)
	s_waitcnt lgkmcnt(0)
	s_barrier
	s_cbranch_vccnz .LBB0_1106
	s_waitcnt lgkmcnt(0)
	v_mfma_f32_16x16x32_bf16 v[66:69], v[150:153], v[190:193], v[66:69]
	v_mfma_f32_16x16x32_bf16 v[62:65], v[158:161], v[190:193], v[62:65]
	v_mfma_f32_16x16x32_bf16 v[50:53], v[150:153], v[178:181], v[50:53]
	v_mfma_f32_16x16x32_bf16 v[46:49], v[158:161], v[178:181], v[46:49]
	v_mfma_f32_16x16x32_bf16 v[34:37], v[150:153], v[174:177], v[34:37]
	v_mfma_f32_16x16x32_bf16 v[30:33], v[158:161], v[174:177], v[30:33]
	v_mfma_f32_16x16x32_bf16 v[18:21], v[150:153], v[166:169], v[18:21]
	v_mfma_f32_16x16x32_bf16 v[14:17], v[158:161], v[166:169], v[14:17]
	v_mfma_f32_16x16x32_bf16 v[66:69], v[154:157], v[194:197], v[66:69]
	v_mfma_f32_16x16x32_bf16 v[62:65], v[162:165], v[194:197], v[62:65]
	v_mfma_f32_16x16x32_bf16 v[50:53], v[154:157], v[182:185], v[50:53]
	v_mfma_f32_16x16x32_bf16 v[46:49], v[162:165], v[182:185], v[46:49]
	v_mfma_f32_16x16x32_bf16 v[34:37], v[154:157], v[186:189], v[34:37]
	v_mfma_f32_16x16x32_bf16 v[30:33], v[162:165], v[186:189], v[30:33]
	v_mfma_f32_16x16x32_bf16 v[18:21], v[154:157], v[170:173], v[18:21]
	v_mfma_f32_16x16x32_bf16 v[14:17], v[162:165], v[170:173], v[14:17]
	v_mfma_f32_16x16x32_bf16 v[58:61], v[134:137], v[190:193], v[58:61]
	v_mfma_f32_16x16x32_bf16 v[54:57], v[142:145], v[190:193], v[54:57]
	v_mfma_f32_16x16x32_bf16 v[42:45], v[134:137], v[178:181], v[42:45]
	v_mfma_f32_16x16x32_bf16 v[38:41], v[142:145], v[178:181], v[38:41]
	v_mfma_f32_16x16x32_bf16 v[26:29], v[134:137], v[174:177], v[26:29]
	v_mfma_f32_16x16x32_bf16 v[22:25], v[142:145], v[174:177], v[22:25]
	v_mfma_f32_16x16x32_bf16 v[10:13], v[134:137], v[166:169], v[10:13]
	v_mfma_f32_16x16x32_bf16 v[4:7], v[142:145], v[166:169], v[6:9]
	v_mfma_f32_16x16x32_bf16 v[58:61], v[138:141], v[194:197], v[58:61]
	v_mfma_f32_16x16x32_bf16 v[54:57], v[146:149], v[194:197], v[54:57]
	v_mfma_f32_16x16x32_bf16 v[42:45], v[138:141], v[182:185], v[42:45]
	v_mfma_f32_16x16x32_bf16 v[38:41], v[146:149], v[182:185], v[38:41]
	v_mfma_f32_16x16x32_bf16 v[26:29], v[138:141], v[186:189], v[26:29]
	v_mfma_f32_16x16x32_bf16 v[22:25], v[146:149], v[186:189], v[22:25]
	v_mfma_f32_16x16x32_bf16 v[10:13], v[138:141], v[170:173], v[10:13]
	v_mfma_f32_16x16x32_bf16 v[6:9], v[146:149], v[170:173], v[4:7]
; #define PG8_STAGE(bufoff, gbase, voff) do { _Pragma("unroll") for (int _i = 0; _i < 2; ++_i) \
;         __builtin_amdgcn_global_load_lds((const unsigned*)((const char*)(gbase) + (voff)[_i]), (LAS unsigned*)(lds + (bufoff) + ldsw + _i * 8192), 16, 0, 0); } while (0)
; #define PG8_LDA(dst, b, h) do { _Pragma("unroll") for (int m = 0; m < 4; ++m) _Pragma("unroll") for (int k = 0; k < 2; ++k) dst[m][k] = *(const LAS bf16x8*)(lds + PG8_SA(b, h) + ((aoff ^ (k * 64)) + m * 2048)); } while (0)
; #define PG8_MMA(ai, bj, At, Bt) do { __builtin_amdgcn_s_setprio(1); _Pragma("unroll") for (int m = 0; m < 4; ++m) _Pragma("unroll") for (int n = 0; n < 2; ++n) _Pragma("unroll") for (int k = 0; k < 2; ++k) \
;         acc[ai][bj][m][n] = __builtin_amdgcn_mfma_f32_16x16x32_bf16(Bt[n][k], At[m][k], acc[ai][bj][m][n], 0, 0, 0); __builtin_amdgcn_s_setprio(0); } while (0)
; #define PG8_WAIT_V(n) asm volatile("s_waitcnt vmcnt(" #n ")" ::: "memory")
; #define PG8_WAIT_L(n) asm volatile("s_waitcnt lgkmcnt(" #n ")" ::: "memory")
; #define PG8_BAR __builtin_amdgcn_s_barrier()
; #define PG8_SCHED __builtin_amdgcn_sched_barrier(0)
;     ...
;             PG8_LDA(At, 1, 1); PG8_STAGE(PG8_SB(1, 0), b3, voffB); PG8_STAGE(PG8_SB(1, 1), b3 + hstep, voffB); PG8_STAGE(PG8_SA(1, 0), a3, vs[0]);
;             PG8_WAIT_V(8); PG8_WAIT_L(0); PG8_BAR; if (do1) { PG8_MMA(1, 0, At, B0); PG8_MMA(1, 1, At, B1); } PG8_BAR; PG8_SCHED;
;         }
.LBB0_1106:
	s_add_u32 s6, s26, 0x4000
	s_addc_u32 s7, s27, 0
	s_add_u32 s26, s24, 0x4000
	s_addc_u32 s27, s25, 0
	s_barrier
	s_mov_b32 m0, s39
	v_lshl_add_u64 v[4:5], s[26:27], 0, v[208:209]
	s_add_u32 s24, s24, 0xb4000
	s_waitcnt lgkmcnt(0)
	ds_read_b128 v[190:193], v226 offset:49152
	ds_read_b128 v[178:181], v226 offset:51200
	ds_read_b128 v[194:197], v227 offset:49152
	ds_read_b128 v[182:185], v227 offset:51200
	ds_read_b128 v[174:177], v226 offset:53248
	ds_read_b128 v[166:169], v226 offset:55296
	ds_read_b128 v[186:189], v227 offset:53248
	ds_read_b128 v[170:173], v227 offset:55296
	global_load_lds_dwordx4 v[4:5], off
	v_lshl_add_u64 v[4:5], s[26:27], 0, v[210:211]
	s_mov_b32 m0, s40
	s_addc_u32 s25, s25, 0
	global_load_lds_dwordx4 v[4:5], off
	v_lshl_add_u64 v[4:5], s[24:25], 0, v[208:209]
	s_mov_b32 m0, s43
	s_and_b64 vcc, exec, s[8:9]
	global_load_lds_dwordx4 v[4:5], off
	v_lshl_add_u64 v[4:5], s[24:25], 0, v[210:211]
	s_mov_b32 m0, s44
	s_nop 0
	global_load_lds_dwordx4 v[4:5], off
	v_lshl_add_u64 v[4:5], s[6:7], 0, v[200:201]
	s_mov_b32 m0, s41
	s_nop 0
	global_load_lds_dwordx4 v[4:5], off
	v_lshl_add_u64 v[4:5], s[6:7], 0, v[202:203]
	s_mov_b32 m0, s42
	s_nop 0
	global_load_lds_dwordx4 v[4:5], off
	s_waitcnt vmcnt(8)
	s_waitcnt lgkmcnt(0)
	s_barrier
	s_cbranch_vccnz .LBB0_1099
	s_waitcnt lgkmcnt(0)
	v_mfma_f32_16x16x32_bf16 v[130:133], v[150:153], v[190:193], v[130:133]
	v_mfma_f32_16x16x32_bf16 v[126:129], v[158:161], v[190:193], v[126:129]
	v_mfma_f32_16x16x32_bf16 v[114:117], v[150:153], v[178:181], v[114:117]
	v_mfma_f32_16x16x32_bf16 v[110:113], v[158:161], v[178:181], v[110:113]
	v_mfma_f32_16x16x32_bf16 v[98:101], v[150:153], v[174:177], v[98:101]
	v_mfma_f32_16x16x32_bf16 v[94:97], v[158:161], v[174:177], v[94:97]
	v_mfma_f32_16x16x32_bf16 v[82:85], v[150:153], v[166:169], v[82:85]
	v_mfma_f32_16x16x32_bf16 v[78:81], v[158:161], v[166:169], v[78:81]
	v_mfma_f32_16x16x32_bf16 v[130:133], v[154:157], v[194:197], v[130:133]
	v_mfma_f32_16x16x32_bf16 v[126:129], v[162:165], v[194:197], v[126:129]
	v_mfma_f32_16x16x32_bf16 v[114:117], v[154:157], v[182:185], v[114:117]
	v_mfma_f32_16x16x32_bf16 v[110:113], v[162:165], v[182:185], v[110:113]
	v_mfma_f32_16x16x32_bf16 v[98:101], v[154:157], v[186:189], v[98:101]
	v_mfma_f32_16x16x32_bf16 v[94:97], v[162:165], v[186:189], v[94:97]
	v_mfma_f32_16x16x32_bf16 v[82:85], v[154:157], v[170:173], v[82:85]
	v_mfma_f32_16x16x32_bf16 v[78:81], v[162:165], v[170:173], v[78:81]
	v_mfma_f32_16x16x32_bf16 v[122:125], v[134:137], v[190:193], v[122:125]
	v_mfma_f32_16x16x32_bf16 v[118:121], v[142:145], v[190:193], v[118:121]
	v_mfma_f32_16x16x32_bf16 v[106:109], v[134:137], v[178:181], v[106:109]
	v_mfma_f32_16x16x32_bf16 v[102:105], v[142:145], v[178:181], v[102:105]
	v_mfma_f32_16x16x32_bf16 v[90:93], v[134:137], v[174:177], v[90:93]
	v_mfma_f32_16x16x32_bf16 v[86:89], v[142:145], v[174:177], v[86:89]
	v_mfma_f32_16x16x32_bf16 v[74:77], v[134:137], v[166:169], v[74:77]
	v_mfma_f32_16x16x32_bf16 v[70:73], v[142:145], v[166:169], v[70:73]
	v_mfma_f32_16x16x32_bf16 v[122:125], v[138:141], v[194:197], v[122:125]
	v_mfma_f32_16x16x32_bf16 v[118:121], v[146:149], v[194:197], v[118:121]
	v_mfma_f32_16x16x32_bf16 v[106:109], v[138:141], v[182:185], v[106:109]
	v_mfma_f32_16x16x32_bf16 v[102:105], v[146:149], v[182:185], v[102:105]
	v_mfma_f32_16x16x32_bf16 v[90:93], v[138:141], v[186:189], v[90:93]
	v_mfma_f32_16x16x32_bf16 v[86:89], v[146:149], v[186:189], v[86:89]
	v_mfma_f32_16x16x32_bf16 v[74:77], v[138:141], v[170:173], v[74:77]
	v_mfma_f32_16x16x32_bf16 v[70:73], v[146:149], v[170:173], v[70:73]
	s_branch .LBB0_1099

; #define PG8_STAGE(bufoff, gbase, voff) do { _Pragma("unroll") for (int _i = 0; _i < 2; ++_i) \
;         __builtin_amdgcn_global_load_lds((const unsigned*)((const char*)(gbase) + (voff)[_i]), (LAS unsigned*)(lds + (bufoff) + ldsw + _i * 8192), 16, 0, 0); } while (0)
; #define PG8_LDA(dst, b, h) do { _Pragma("unroll") for (int m = 0; m < 4; ++m) _Pragma("unroll") for (int k = 0; k < 2; ++k) dst[m][k] = *(const LAS bf16x8*)(lds + PG8_SA(b, h) + ((aoff ^ (k * 64)) + m * 2048)); } while (0)
; #define PG8_LDB(dst, b, h) do { _Pragma("unroll") for (int n = 0; n < 2; ++n) _Pragma("unroll") for (int k = 0; k < 2; ++k) dst[n][k] = *(const LAS bf16x8*)(lds + PG8_SB(b, h) + ((boff ^ (k * 64)) + n * 2048)); } while (0)
; #define PG8_MMA(ai, bj, At, Bt) do { __builtin_amdgcn_s_setprio(1); _Pragma("unroll") for (int m = 0; m < 4; ++m) _Pragma("unroll") for (int n = 0; n < 2; ++n) _Pragma("unroll") for (int k = 0; k < 2; ++k) \
;         acc[ai][bj][m][n] = __builtin_amdgcn_mfma_f32_16x16x32_bf16(Bt[n][k], At[m][k], acc[ai][bj][m][n], 0, 0, 0); __builtin_amdgcn_s_setprio(0); } while (0)
; #define PG8_WAIT_V(n) asm volatile("s_waitcnt vmcnt(" #n ")" ::: "memory")
; #define PG8_WAIT_L(n) asm volatile("s_waitcnt lgkmcnt(" #n ")" ::: "memory")
; #define PG8_BAR __builtin_amdgcn_s_barrier()
; #define PG8_SCHED __builtin_amdgcn_sched_barrier(0)
;     ...
;             PG8_LDB(B0, 0, 0); PG8_LDB(B1, 0, 1); PG8_SCHED; PG8_LDA(At, 0, 0); PG8_STAGE(PG8_SA(1, 1), a1, voffA[1]);
;             PG8_WAIT_V(8); PG8_WAIT_L(0); PG8_BAR; if (do0) { PG8_MMA(0, 0, At, B0); PG8_MMA(0, 1, At, B1); } PG8_BAR; PG8_SCHED;
;             PG8_LDA(At, 0, 1); PG8_STAGE(PG8_SB(0, 0), b2, voffB); PG8_STAGE(PG8_SB(0, 1), b2 + hstep, voffB); PG8_STAGE(PG8_SA(0, 0), a2, vs[0]);
;             PG8_WAIT_V(8); PG8_WAIT_L(0); PG8_BAR; if (do1) { PG8_MMA(1, 0, At, B0); PG8_MMA(1, 1, At, B1); } PG8_BAR; PG8_SCHED;
.LBB0_1257:
	ds_read_b128 v[156:159], v176
	ds_read_b128 v[160:163], v177
	ds_read_b128 v[164:167], v178
	ds_read_b128 v[192:195], v179
	ds_read_b128 v[200:203], v180
	ds_read_b128 v[204:207], v181
	ds_read_b128 v[208:211], v182
	ds_read_b128 v[212:215], v183
	s_add_u32 s40, s38, 0x80
	s_addc_u32 s41, s39, 0
	s_cmp_eq_u32 s63, 12
	s_cselect_b32 s45, s3, s41
	s_cselect_b32 s44, s11, s40
	s_cselect_b32 s41, s12, s62
	s_cselect_b32 s40, s29, s31
	v_lshl_add_u64 v[168:169], s[38:39], 0, v[150:151]
	s_add_i32 m0, s47, 0xc000
	ds_read_b128 v[216:219], v184
	ds_read_b128 v[220:223], v184 offset:2048
	ds_read_b128 v[224:227], v185
	ds_read_b128 v[228:231], v185 offset:2048
	ds_read_b128 v[232:235], v184 offset:4096
	ds_read_b128 v[236:239], v184 offset:6144
	ds_read_b128 v[240:243], v185 offset:4096
	ds_read_b128 v[244:247], v185 offset:6144
	global_load_lds_dwordx4 v[168:169], off
	v_lshl_add_u64 v[168:169], s[38:39], 0, v[148:149]
	s_add_i32 m0, s47, 0xe000
	s_add_u32 s42, s40, 0x4000
	global_load_lds_dwordx4 v[168:169], off
	s_waitcnt vmcnt(8)
	s_waitcnt lgkmcnt(0)
	s_addc_u32 s43, s41, 0
	s_barrier
	s_waitcnt lgkmcnt(0)
	v_mfma_f32_16x16x32_bf16 v[126:129], v[156:159], v[216:219], v[126:129]
	v_mfma_f32_16x16x32_bf16 v[118:121], v[164:167], v[216:219], v[118:121]
	v_mfma_f32_16x16x32_bf16 v[110:113], v[156:159], v[220:223], v[110:113]
	v_mfma_f32_16x16x32_bf16 v[102:105], v[164:167], v[220:223], v[102:105]
	v_mfma_f32_16x16x32_bf16 v[94:97], v[156:159], v[232:235], v[94:97]
	v_mfma_f32_16x16x32_bf16 v[86:89], v[164:167], v[232:235], v[86:89]
	v_mfma_f32_16x16x32_bf16 v[78:81], v[156:159], v[236:239], v[78:81]
	v_mfma_f32_16x16x32_bf16 v[70:73], v[164:167], v[236:239], v[70:73]
	v_mfma_f32_16x16x32_bf16 v[126:129], v[160:163], v[224:227], v[126:129]
	v_mfma_f32_16x16x32_bf16 v[118:121], v[192:195], v[224:227], v[118:121]
	v_mfma_f32_16x16x32_bf16 v[110:113], v[160:163], v[228:231], v[110:113]
	v_mfma_f32_16x16x32_bf16 v[102:105], v[192:195], v[228:231], v[102:105]
	v_mfma_f32_16x16x32_bf16 v[94:97], v[160:163], v[240:243], v[94:97]
	v_mfma_f32_16x16x32_bf16 v[86:89], v[192:195], v[240:243], v[86:89]
	v_mfma_f32_16x16x32_bf16 v[78:81], v[160:163], v[244:247], v[78:81]
	v_mfma_f32_16x16x32_bf16 v[70:73], v[192:195], v[244:247], v[70:73]
	v_mfma_f32_16x16x32_bf16 v[122:125], v[200:203], v[216:219], v[122:125]
	v_mfma_f32_16x16x32_bf16 v[114:117], v[208:211], v[216:219], v[114:117]
	v_mfma_f32_16x16x32_bf16 v[106:109], v[200:203], v[220:223], v[106:109]
	v_mfma_f32_16x16x32_bf16 v[98:101], v[208:211], v[220:223], v[98:101]
	v_mfma_f32_16x16x32_bf16 v[90:93], v[200:203], v[232:235], v[90:93]
	v_mfma_f32_16x16x32_bf16 v[82:85], v[208:211], v[232:235], v[82:85]
	v_mfma_f32_16x16x32_bf16 v[74:77], v[200:203], v[236:239], v[74:77]
	v_mfma_f32_16x16x32_bf16 v[66:69], v[208:211], v[236:239], v[66:69]
	v_mfma_f32_16x16x32_bf16 v[122:125], v[204:207], v[224:227], v[122:125]
	v_mfma_f32_16x16x32_bf16 v[114:117], v[212:215], v[224:227], v[114:117]
	v_mfma_f32_16x16x32_bf16 v[106:109], v[204:207], v[228:231], v[106:109]
	v_mfma_f32_16x16x32_bf16 v[98:101], v[212:215], v[228:231], v[98:101]
	v_mfma_f32_16x16x32_bf16 v[90:93], v[204:207], v[240:243], v[90:93]
	v_mfma_f32_16x16x32_bf16 v[82:85], v[212:215], v[240:243], v[82:85]
	v_mfma_f32_16x16x32_bf16 v[74:77], v[204:207], v[244:247], v[74:77]
	v_mfma_f32_16x16x32_bf16 v[66:69], v[212:215], v[244:247], v[66:69]
	s_barrier
	s_add_i32 s64, s56, s46
	v_lshl_add_u64 v[168:169], s[40:41], 0, v[130:131]
	s_mov_b32 m0, s64
	ds_read_b128 v[216:219], v184 offset:16384
	ds_read_b128 v[220:223], v184 offset:18432
	ds_read_b128 v[224:227], v185 offset:16384
	ds_read_b128 v[228:231], v185 offset:18432
	ds_read_b128 v[232:235], v184 offset:20480
	ds_read_b128 v[236:239], v184 offset:22528
	ds_read_b128 v[240:243], v185 offset:20480
	ds_read_b128 v[244:247], v185 offset:22528
	global_load_lds_dwordx4 v[168:169], off
	s_add_i32 m0, s64, 0x2000
	s_add_u32 s64, s40, 0x40000
	v_lshl_add_u64 v[168:169], s[40:41], 0, v[132:133]
	s_addc_u32 s65, s41, 0
	s_add_i32 s66, s57, s46
	global_load_lds_dwordx4 v[168:169], off
	v_lshl_add_u64 v[168:169], s[64:65], 0, v[130:131]
	s_mov_b32 m0, s66
	v_lshl_add_u64 v[196:197], s[44:45], 0, v[136:137]
	global_load_lds_dwordx4 v[168:169], off
	v_lshl_add_u64 v[168:169], s[64:65], 0, v[132:133]
	s_add_i32 m0, s66, 0x2000
	s_nop 0
	global_load_lds_dwordx4 v[168:169], off
	v_lshl_add_u64 v[168:169], s[44:45], 0, v[134:135]
	s_mov_b32 m0, s47
	s_nop 0
	global_load_lds_dwordx4 v[168:169], off
	s_mov_b32 m0, s48
	s_nop 0
	global_load_lds_dwordx4 v[196:197], off
	s_waitcnt vmcnt(8)
	s_waitcnt lgkmcnt(0)
	s_barrier
; #define PG8_STAGE(bufoff, gbase, voff) do { _Pragma("unroll") for (int _i = 0; _i < 2; ++_i) \
;         __builtin_amdgcn_global_load_lds((const unsigned*)((const char*)(gbase) + (voff)[_i]), (LAS unsigned*)(lds + (bufoff) + ldsw + _i * 8192), 16, 0, 0); } while (0)
; #define PG8_LDA(dst, b, h) do { _Pragma("unroll") for (int m = 0; m < 4; ++m) _Pragma("unroll") for (int k = 0; k < 2; ++k) dst[m][k] = *(const LAS bf16x8*)(lds + PG8_SA(b, h) + ((aoff ^ (k * 64)) + m * 2048)); } while (0)
; #define PG8_LDB(dst, b, h) do { _Pragma("unroll") for (int n = 0; n < 2; ++n) _Pragma("unroll") for (int k = 0; k < 2; ++k) dst[n][k] = *(const LAS bf16x8*)(lds + PG8_SB(b, h) + ((boff ^ (k * 64)) + n * 2048)); } while (0)
; #define PG8_MMA(ai, bj, At, Bt) do { __builtin_amdgcn_s_setprio(1); _Pragma("unroll") for (int m = 0; m < 4; ++m) _Pragma("unroll") for (int n = 0; n < 2; ++n) _Pragma("unroll") for (int k = 0; k < 2; ++k) \
;         acc[ai][bj][m][n] = __builtin_amdgcn_mfma_f32_16x16x32_bf16(Bt[n][k], At[m][k], acc[ai][bj][m][n], 0, 0, 0); __builtin_amdgcn_s_setprio(0); } while (0)
; #define PG8_WAIT_V(n) asm volatile("s_waitcnt vmcnt(" #n ")" ::: "memory")
; #define PG8_WAIT_L(n) asm volatile("s_waitcnt lgkmcnt(" #n ")" ::: "memory")
; #define PG8_BAR __builtin_amdgcn_s_barrier()
; #define PG8_SCHED __builtin_amdgcn_sched_barrier(0)
;     ...
;             PG8_WAIT_V(8); PG8_WAIT_L(0); PG8_BAR; if (do1) { PG8_MMA(1, 0, At, B0); PG8_MMA(1, 1, At, B1); } PG8_BAR; PG8_SCHED;
;             PG8_LDB(B0, 1, 0); PG8_LDB(B1, 1, 1); PG8_SCHED; PG8_LDA(At, 1, 0); PG8_STAGE(PG8_SA(0, 1), a2, vs[1]);
;             PG8_WAIT_V(8); PG8_WAIT_L(0); PG8_BAR; if (do0) { PG8_MMA(0, 0, At, B0); PG8_MMA(0, 1, At, B1); } PG8_BAR; PG8_SCHED;
	s_waitcnt lgkmcnt(0)
	v_mfma_f32_16x16x32_bf16 v[62:65], v[156:159], v[216:219], v[62:65]
	v_mfma_f32_16x16x32_bf16 v[54:57], v[164:167], v[216:219], v[54:57]
	v_mfma_f32_16x16x32_bf16 v[46:49], v[156:159], v[220:223], v[46:49]
	v_mfma_f32_16x16x32_bf16 v[38:41], v[164:167], v[220:223], v[38:41]
	v_mfma_f32_16x16x32_bf16 v[30:33], v[156:159], v[232:235], v[30:33]
	v_mfma_f32_16x16x32_bf16 v[22:25], v[164:167], v[232:235], v[22:25]
	v_mfma_f32_16x16x32_bf16 v[14:17], v[156:159], v[236:239], v[14:17]
	v_mfma_f32_16x16x32_bf16 v[6:9], v[164:167], v[236:239], v[6:9]
	v_mfma_f32_16x16x32_bf16 v[62:65], v[160:163], v[224:227], v[62:65]
	v_mfma_f32_16x16x32_bf16 v[54:57], v[192:195], v[224:227], v[54:57]
	v_mfma_f32_16x16x32_bf16 v[46:49], v[160:163], v[228:231], v[46:49]
	v_mfma_f32_16x16x32_bf16 v[38:41], v[192:195], v[228:231], v[38:41]
	v_mfma_f32_16x16x32_bf16 v[30:33], v[160:163], v[240:243], v[30:33]
	v_mfma_f32_16x16x32_bf16 v[22:25], v[192:195], v[240:243], v[22:25]
	v_mfma_f32_16x16x32_bf16 v[14:17], v[160:163], v[244:247], v[14:17]
	v_mfma_f32_16x16x32_bf16 v[6:9], v[192:195], v[244:247], v[6:9]
	v_mfma_f32_16x16x32_bf16 v[58:61], v[200:203], v[216:219], v[58:61]
	v_mfma_f32_16x16x32_bf16 v[50:53], v[208:211], v[216:219], v[50:53]
	v_mfma_f32_16x16x32_bf16 v[42:45], v[200:203], v[220:223], v[42:45]
	v_mfma_f32_16x16x32_bf16 v[34:37], v[208:211], v[220:223], v[34:37]
	v_mfma_f32_16x16x32_bf16 v[26:29], v[200:203], v[232:235], v[26:29]
	v_mfma_f32_16x16x32_bf16 v[18:21], v[208:211], v[232:235], v[18:21]
	v_mfma_f32_16x16x32_bf16 v[10:13], v[200:203], v[236:239], v[10:13]
	v_mfma_f32_16x16x32_bf16 v[2:5], v[208:211], v[236:239], v[2:5]
	v_mfma_f32_16x16x32_bf16 v[58:61], v[204:207], v[224:227], v[58:61]
	v_mfma_f32_16x16x32_bf16 v[50:53], v[212:215], v[224:227], v[50:53]
	v_mfma_f32_16x16x32_bf16 v[42:45], v[204:207], v[228:231], v[42:45]
	v_mfma_f32_16x16x32_bf16 v[34:37], v[212:215], v[228:231], v[34:37]
	v_mfma_f32_16x16x32_bf16 v[26:29], v[204:207], v[240:243], v[26:29]
	v_mfma_f32_16x16x32_bf16 v[18:21], v[212:215], v[240:243], v[18:21]
	v_mfma_f32_16x16x32_bf16 v[10:13], v[204:207], v[244:247], v[10:13]
	v_mfma_f32_16x16x32_bf16 v[2:5], v[212:215], v[244:247], v[2:5]
	s_barrier
	s_add_i32 s64, 0, 0x18000
	v_add_u32_e32 v142, s64, v170
	v_add_u32_e32 v160, s64, v174
	s_add_i32 s65, 0, 0x1c000
	ds_read_b128 v[156:159], v142
	ds_read_b128 v[160:163], v160
	ds_read_b128 v[164:167], v186
	ds_read_b128 v[192:195], v187
	v_add_u32_e32 v142, s65, v170
	v_add_u32_e32 v191, s65, v174
	ds_read_b128 v[200:203], v142
	ds_read_b128 v[204:207], v191
	ds_read_b128 v[208:211], v188
	ds_read_b128 v[212:215], v189
	s_mov_b32 m0, s49
	v_lshl_add_u64 v[248:249], s[44:45], 0, v[138:139]
	ds_read_b128 v[216:219], v184 offset:32768
	ds_read_b128 v[220:223], v184 offset:34816
	ds_read_b128 v[224:227], v185 offset:32768
	ds_read_b128 v[228:231], v185 offset:34816
	ds_read_b128 v[232:235], v184 offset:36864
	ds_read_b128 v[236:239], v184 offset:38912
	ds_read_b128 v[240:243], v185 offset:36864
	ds_read_b128 v[244:247], v185 offset:38912
	global_load_lds_dwordx4 v[248:249], off
	v_lshl_add_u64 v[248:249], s[44:45], 0, v[140:141]
	s_mov_b32 m0, s50
	s_nop 0
	global_load_lds_dwordx4 v[248:249], off
	s_waitcnt vmcnt(8)
	s_waitcnt lgkmcnt(0)
	s_barrier
	s_waitcnt lgkmcnt(0)
	v_mfma_f32_16x16x32_bf16 v[126:129], v[156:159], v[216:219], v[126:129]
	v_mfma_f32_16x16x32_bf16 v[118:121], v[164:167], v[216:219], v[118:121]
	v_mfma_f32_16x16x32_bf16 v[110:113], v[156:159], v[220:223], v[110:113]
	v_mfma_f32_16x16x32_bf16 v[102:105], v[164:167], v[220:223], v[102:105]
	v_mfma_f32_16x16x32_bf16 v[94:97], v[156:159], v[232:235], v[94:97]
	v_mfma_f32_16x16x32_bf16 v[86:89], v[164:167], v[232:235], v[86:89]
	v_mfma_f32_16x16x32_bf16 v[78:81], v[156:159], v[236:239], v[78:81]
	v_mfma_f32_16x16x32_bf16 v[70:73], v[164:167], v[236:239], v[70:73]
	v_mfma_f32_16x16x32_bf16 v[126:129], v[160:163], v[224:227], v[126:129]
	v_mfma_f32_16x16x32_bf16 v[118:121], v[192:195], v[224:227], v[118:121]
	v_mfma_f32_16x16x32_bf16 v[110:113], v[160:163], v[228:231], v[110:113]
	v_mfma_f32_16x16x32_bf16 v[102:105], v[192:195], v[228:231], v[102:105]
	v_mfma_f32_16x16x32_bf16 v[94:97], v[160:163], v[240:243], v[94:97]
	v_mfma_f32_16x16x32_bf16 v[86:89], v[192:195], v[240:243], v[86:89]
	v_mfma_f32_16x16x32_bf16 v[78:81], v[160:163], v[244:247], v[78:81]
	v_mfma_f32_16x16x32_bf16 v[70:73], v[192:195], v[244:247], v[70:73]
	v_mfma_f32_16x16x32_bf16 v[122:125], v[200:203], v[216:219], v[122:125]
	v_mfma_f32_16x16x32_bf16 v[114:117], v[208:211], v[216:219], v[114:117]
	v_mfma_f32_16x16x32_bf16 v[106:109], v[200:203], v[220:223], v[106:109]
	v_mfma_f32_16x16x32_bf16 v[98:101], v[208:211], v[220:223], v[98:101]
	v_mfma_f32_16x16x32_bf16 v[90:93], v[200:203], v[232:235], v[90:93]
	v_mfma_f32_16x16x32_bf16 v[82:85], v[208:211], v[232:235], v[82:85]
	v_mfma_f32_16x16x32_bf16 v[74:77], v[200:203], v[236:239], v[74:77]
	v_mfma_f32_16x16x32_bf16 v[66:69], v[208:211], v[236:239], v[66:69]
	v_mfma_f32_16x16x32_bf16 v[122:125], v[204:207], v[224:227], v[122:125]
	v_mfma_f32_16x16x32_bf16 v[114:117], v[212:215], v[224:227], v[114:117]
	v_mfma_f32_16x16x32_bf16 v[106:109], v[204:207], v[228:231], v[106:109]
	v_mfma_f32_16x16x32_bf16 v[98:101], v[212:215], v[228:231], v[98:101]
	v_mfma_f32_16x16x32_bf16 v[90:93], v[204:207], v[240:243], v[90:93]
	v_mfma_f32_16x16x32_bf16 v[82:85], v[212:215], v[240:243], v[82:85]
	v_mfma_f32_16x16x32_bf16 v[74:77], v[204:207], v[244:247], v[74:77]
	v_mfma_f32_16x16x32_bf16 v[66:69], v[212:215], v[244:247], v[66:69]
	s_barrier
; #define PG8_STAGE(bufoff, gbase, voff) do { _Pragma("unroll") for (int _i = 0; _i < 2; ++_i) \
;         __builtin_amdgcn_global_load_lds((const unsigned*)((const char*)(gbase) + (voff)[_i]), (LAS unsigned*)(lds + (bufoff) + ldsw + _i * 8192), 16, 0, 0); } while (0)
; #define PG8_LDA(dst, b, h) do { _Pragma("unroll") for (int m = 0; m < 4; ++m) _Pragma("unroll") for (int k = 0; k < 2; ++k) dst[m][k] = *(const LAS bf16x8*)(lds + PG8_SA(b, h) + ((aoff ^ (k * 64)) + m * 2048)); } while (0)
; #define PG8_MMA(ai, bj, At, Bt) do { __builtin_amdgcn_s_setprio(1); _Pragma("unroll") for (int m = 0; m < 4; ++m) _Pragma("unroll") for (int n = 0; n < 2; ++n) _Pragma("unroll") for (int k = 0; k < 2; ++k) \
;         acc[ai][bj][m][n] = __builtin_amdgcn_mfma_f32_16x16x32_bf16(Bt[n][k], At[m][k], acc[ai][bj][m][n], 0, 0, 0); __builtin_amdgcn_s_setprio(0); } while (0)
; #define PG8_WAIT_V(n) asm volatile("s_waitcnt vmcnt(" #n ")" ::: "memory")
; #define PG8_WAIT_L(n) asm volatile("s_waitcnt lgkmcnt(" #n ")" ::: "memory")
; #define PG8_BAR __builtin_amdgcn_s_barrier()
; #define PG8_SCHED __builtin_amdgcn_sched_barrier(0)
;     ...
;             PG8_LDA(At, 1, 1); PG8_STAGE(PG8_SB(1, 0), b3, voffB); PG8_STAGE(PG8_SB(1, 1), b3 + hstep, voffB); PG8_STAGE(PG8_SA(1, 0), a3, vs[0]);
;             PG8_WAIT_V(8); PG8_WAIT_L(0); PG8_BAR; if (do1) { PG8_MMA(1, 0, At, B0); PG8_MMA(1, 1, At, B1); } PG8_BAR; PG8_SCHED;
;         }
;         if (wr == 0) PG8_BAR;
	s_add_i32 s44, s64, s46
	v_lshl_add_u64 v[248:249], s[42:43], 0, v[130:131]
	s_mov_b32 m0, s44
	ds_read_b128 v[216:219], v184 offset:49152
	ds_read_b128 v[220:223], v184 offset:51200
	ds_read_b128 v[224:227], v185 offset:49152
	ds_read_b128 v[228:231], v185 offset:51200
	ds_read_b128 v[232:235], v184 offset:53248
	ds_read_b128 v[236:239], v184 offset:55296
	ds_read_b128 v[240:243], v185 offset:53248
	ds_read_b128 v[244:247], v185 offset:55296
	global_load_lds_dwordx4 v[248:249], off
	s_add_i32 m0, s44, 0x2000
	s_add_u32 s40, s40, 0x44000
	v_lshl_add_u64 v[248:249], s[42:43], 0, v[132:133]
	s_addc_u32 s41, s41, 0
	s_add_i32 s42, s65, s46
	global_load_lds_dwordx4 v[248:249], off
	v_lshl_add_u64 v[248:249], s[40:41], 0, v[130:131]
	s_mov_b32 m0, s42
	v_lshl_add_u64 v[168:169], v[168:169], 0, s[20:21]
	global_load_lds_dwordx4 v[248:249], off
	v_lshl_add_u64 v[248:249], s[40:41], 0, v[132:133]
	s_add_i32 m0, s42, 0x2000
	s_nop 0
	global_load_lds_dwordx4 v[248:249], off
	s_mov_b32 m0, s52
	s_nop 0
	global_load_lds_dwordx4 v[168:169], off
	v_lshl_add_u64 v[168:169], v[196:197], 0, s[20:21]
	s_mov_b32 m0, s53
	s_nop 0
	global_load_lds_dwordx4 v[168:169], off
	s_waitcnt vmcnt(8)
	s_waitcnt lgkmcnt(0)
	s_barrier
	s_waitcnt lgkmcnt(0)
	v_mfma_f32_16x16x32_bf16 v[62:65], v[156:159], v[216:219], v[62:65]
	v_mfma_f32_16x16x32_bf16 v[54:57], v[164:167], v[216:219], v[54:57]
	v_mfma_f32_16x16x32_bf16 v[46:49], v[156:159], v[220:223], v[46:49]
	v_mfma_f32_16x16x32_bf16 v[38:41], v[164:167], v[220:223], v[38:41]
	v_mfma_f32_16x16x32_bf16 v[30:33], v[156:159], v[232:235], v[30:33]
	v_mfma_f32_16x16x32_bf16 v[22:25], v[164:167], v[232:235], v[22:25]
	v_mfma_f32_16x16x32_bf16 v[14:17], v[156:159], v[236:239], v[14:17]
	v_mfma_f32_16x16x32_bf16 v[6:9], v[164:167], v[236:239], v[6:9]
	v_mfma_f32_16x16x32_bf16 v[62:65], v[160:163], v[224:227], v[62:65]
	v_mfma_f32_16x16x32_bf16 v[54:57], v[192:195], v[224:227], v[54:57]
	v_mfma_f32_16x16x32_bf16 v[46:49], v[160:163], v[228:231], v[46:49]
	v_mfma_f32_16x16x32_bf16 v[38:41], v[192:195], v[228:231], v[38:41]
	v_mfma_f32_16x16x32_bf16 v[30:33], v[160:163], v[240:243], v[30:33]
	v_mfma_f32_16x16x32_bf16 v[22:25], v[192:195], v[240:243], v[22:25]
	v_mfma_f32_16x16x32_bf16 v[14:17], v[160:163], v[244:247], v[14:17]
	v_mfma_f32_16x16x32_bf16 v[6:9], v[192:195], v[244:247], v[6:9]
	v_mfma_f32_16x16x32_bf16 v[58:61], v[200:203], v[216:219], v[58:61]
	v_mfma_f32_16x16x32_bf16 v[50:53], v[208:211], v[216:219], v[50:53]
	v_mfma_f32_16x16x32_bf16 v[42:45], v[200:203], v[220:223], v[42:45]
	v_mfma_f32_16x16x32_bf16 v[34:37], v[208:211], v[220:223], v[34:37]
	v_mfma_f32_16x16x32_bf16 v[26:29], v[200:203], v[232:235], v[26:29]
	v_mfma_f32_16x16x32_bf16 v[18:21], v[208:211], v[232:235], v[18:21]
	v_mfma_f32_16x16x32_bf16 v[10:13], v[200:203], v[236:239], v[10:13]
	v_mfma_f32_16x16x32_bf16 v[2:5], v[208:211], v[236:239], v[2:5]
	v_mfma_f32_16x16x32_bf16 v[58:61], v[204:207], v[224:227], v[58:61]
	v_mfma_f32_16x16x32_bf16 v[50:53], v[212:215], v[224:227], v[50:53]
	v_mfma_f32_16x16x32_bf16 v[42:45], v[204:207], v[228:231], v[42:45]
	v_mfma_f32_16x16x32_bf16 v[34:37], v[212:215], v[228:231], v[34:37]
	v_mfma_f32_16x16x32_bf16 v[26:29], v[204:207], v[240:243], v[26:29]
	v_mfma_f32_16x16x32_bf16 v[18:21], v[212:215], v[240:243], v[18:21]
	v_mfma_f32_16x16x32_bf16 v[10:13], v[204:207], v[244:247], v[10:13]
	v_mfma_f32_16x16x32_bf16 v[2:5], v[212:215], v[244:247], v[2:5]
	s_barrier
	s_add_i32 s63, s63, 2
	s_add_u32 s31, s31, 0x8000
	s_addc_u32 s62, s62, 0
	s_add_u32 s38, s38, 0x100
	s_addc_u32 s39, s39, 0
	s_cmp_gt_u32 s63, 13
	s_cbranch_scc0 .LBB0_1257
	s_and_b64 vcc, exec, s[22:23]
	s_cbranch_vccz .LBB0_1260
	s_barrier

; #define PG8_STAGE(bufoff, gbase, voff) do { _Pragma("unroll") for (int _i = 0; _i < 2; ++_i) \
;         __builtin_amdgcn_global_load_lds((const unsigned*)((const char*)(gbase) + (voff)[_i]), (LAS unsigned*)(lds + (bufoff) + ldsw + _i * 8192), 16, 0, 0); } while (0)
; #define PG8_LDA(dst, b, h) do { _Pragma("unroll") for (int m = 0; m < 4; ++m) _Pragma("unroll") for (int k = 0; k < 2; ++k) dst[m][k] = *(const LAS bf16x8*)(lds + PG8_SA(b, h) + ((aoff ^ (k * 64)) + m * 2048)); } while (0)
; #define PG8_LDB(dst, b, h) do { _Pragma("unroll") for (int n = 0; n < 2; ++n) _Pragma("unroll") for (int k = 0; k < 2; ++k) dst[n][k] = *(const LAS bf16x8*)(lds + PG8_SB(b, h) + ((boff ^ (k * 64)) + n * 2048)); } while (0)
; #define PG8_MMA(ai, bj, At, Bt) do { __builtin_amdgcn_s_setprio(1); _Pragma("unroll") for (int m = 0; m < 4; ++m) _Pragma("unroll") for (int n = 0; n < 2; ++n) _Pragma("unroll") for (int k = 0; k < 2; ++k) \
;         acc[ai][bj][m][n] = __builtin_amdgcn_mfma_f32_16x16x32_bf16(Bt[n][k], At[m][k], acc[ai][bj][m][n], 0, 0, 0); __builtin_amdgcn_s_setprio(0); } while (0)
; #define PG8_WAIT_V(n) asm volatile("s_waitcnt vmcnt(" #n ")" ::: "memory")
; #define PG8_WAIT_L(n) asm volatile("s_waitcnt lgkmcnt(" #n ")" ::: "memory")
; #define PG8_BAR __builtin_amdgcn_s_barrier()
; #define PG8_SCHED __builtin_amdgcn_sched_barrier(0)
;     ...
;             PG8_LDB(B0, 0, 0); PG8_LDB(B1, 0, 1); PG8_SCHED; PG8_LDA(At, 0, 0); PG8_STAGE(PG8_SA(1, 1), a1, voffA[1]);
;             PG8_WAIT_V(8); PG8_WAIT_L(0); PG8_BAR; if (do0) { PG8_MMA(0, 0, At, B0); PG8_MMA(0, 1, At, B1); } PG8_BAR; PG8_SCHED;
;             PG8_LDA(At, 0, 1); PG8_STAGE(PG8_SB(0, 0), b2, voffB); PG8_STAGE(PG8_SB(0, 1), b2 + hstep, voffB); PG8_STAGE(PG8_SA(0, 0), a2, vs[0]);
;             PG8_WAIT_V(8); PG8_WAIT_L(0); PG8_BAR; if (do1) { PG8_MMA(1, 0, At, B0); PG8_MMA(1, 1, At, B1); } PG8_BAR; PG8_SCHED;
.LBB0_1343:
	v_add_u32_e32 v130, s92, v161
	v_add_u32_e32 v134, s92, v188
	v_add_u32_e32 v138, s93, v161
	v_add_u32_e32 v142, s93, v188
	v_add_u32_e32 v158, s62, v161
	ds_read_b128 v[130:133], v130
	ds_read_b128 v[134:137], v134
	ds_read_b128 v[138:141], v138
	ds_read_b128 v[142:145], v142
	v_add_u32_e32 v184, s62, v188
	ds_read_b128 v[180:183], v158
	ds_read_b128 v[200:203], v184
	v_add_u32_e32 v158, s63, v161
	s_add_u32 s56, s0, 0x4000
	v_add_u32_e32 v184, s63, v188
	ds_read_b128 v[204:207], v158
	ds_read_b128 v[208:211], v184
	s_addc_u32 s57, s1, 0
	s_cmp_eq_u32 s95, 12
	s_cselect_b32 s60, s23, s56
	s_cselect_b32 s61, s3, s57
	s_cselect_b32 s58, s47, s74
	s_cselect_b32 s59, s45, s94
	s_add_u32 s56, s60, 0x4000
	s_addc_u32 s57, s61, 0
	v_lshl_add_u64 v[184:185], s[0:1], 0, v[176:177]
	s_add_i32 m0, s55, 0xc000
	ds_read_b128 v[212:215], v193
	ds_read_b128 v[216:219], v193 offset:2048
	ds_read_b128 v[220:223], v194
	ds_read_b128 v[224:227], v194 offset:2048
	ds_read_b128 v[228:231], v193 offset:4096
	ds_read_b128 v[232:235], v193 offset:6144
	ds_read_b128 v[236:239], v194 offset:4096
	ds_read_b128 v[240:243], v194 offset:6144
	global_load_lds_dwordx4 v[184:185], off
	v_lshl_add_u64 v[184:185], s[0:1], 0, v[178:179]
	s_add_i32 m0, s55, 0xe000
	s_nop 0
	global_load_lds_dwordx4 v[184:185], off
	s_waitcnt vmcnt(8)
	s_waitcnt lgkmcnt(0)
	s_barrier
	s_waitcnt lgkmcnt(0)
	v_mfma_f32_16x16x32_bf16 v[126:129], v[130:133], v[212:215], v[126:129]
	v_mfma_f32_16x16x32_bf16 v[122:125], v[138:141], v[212:215], v[122:125]
	v_mfma_f32_16x16x32_bf16 v[94:97], v[130:133], v[216:219], v[94:97]
	v_mfma_f32_16x16x32_bf16 v[90:93], v[138:141], v[216:219], v[90:93]
	v_mfma_f32_16x16x32_bf16 v[62:65], v[130:133], v[228:231], v[62:65]
	v_mfma_f32_16x16x32_bf16 v[58:61], v[138:141], v[228:231], v[58:61]
	v_mfma_f32_16x16x32_bf16 v[30:33], v[130:133], v[232:235], v[30:33]
	v_mfma_f32_16x16x32_bf16 v[26:29], v[138:141], v[232:235], v[26:29]
	v_mfma_f32_16x16x32_bf16 v[126:129], v[134:137], v[220:223], v[126:129]
	v_mfma_f32_16x16x32_bf16 v[122:125], v[142:145], v[220:223], v[122:125]
	v_mfma_f32_16x16x32_bf16 v[94:97], v[134:137], v[224:227], v[94:97]
	v_mfma_f32_16x16x32_bf16 v[90:93], v[142:145], v[224:227], v[90:93]
	v_mfma_f32_16x16x32_bf16 v[62:65], v[134:137], v[236:239], v[62:65]
	v_mfma_f32_16x16x32_bf16 v[58:61], v[142:145], v[236:239], v[58:61]
	v_mfma_f32_16x16x32_bf16 v[30:33], v[134:137], v[240:243], v[30:33]
	v_mfma_f32_16x16x32_bf16 v[26:29], v[142:145], v[240:243], v[26:29]
	v_mfma_f32_16x16x32_bf16 v[110:113], v[180:183], v[212:215], v[110:113]
	v_mfma_f32_16x16x32_bf16 v[106:109], v[204:207], v[212:215], v[106:109]
	v_mfma_f32_16x16x32_bf16 v[78:81], v[180:183], v[216:219], v[78:81]
	v_mfma_f32_16x16x32_bf16 v[74:77], v[204:207], v[216:219], v[74:77]
	v_mfma_f32_16x16x32_bf16 v[46:49], v[180:183], v[228:231], v[46:49]
	v_mfma_f32_16x16x32_bf16 v[42:45], v[204:207], v[228:231], v[42:45]
	v_mfma_f32_16x16x32_bf16 v[14:17], v[180:183], v[232:235], v[14:17]
	v_mfma_f32_16x16x32_bf16 v[10:13], v[204:207], v[232:235], v[10:13]
	v_mfma_f32_16x16x32_bf16 v[110:113], v[200:203], v[220:223], v[110:113]
	v_mfma_f32_16x16x32_bf16 v[106:109], v[208:211], v[220:223], v[106:109]
	v_mfma_f32_16x16x32_bf16 v[78:81], v[200:203], v[224:227], v[78:81]
	v_mfma_f32_16x16x32_bf16 v[74:77], v[208:211], v[224:227], v[74:77]
	v_mfma_f32_16x16x32_bf16 v[46:49], v[200:203], v[236:239], v[46:49]
	v_mfma_f32_16x16x32_bf16 v[42:45], v[208:211], v[236:239], v[42:45]
	v_mfma_f32_16x16x32_bf16 v[14:17], v[200:203], v[240:243], v[14:17]
	v_mfma_f32_16x16x32_bf16 v[10:13], v[208:211], v[240:243], v[10:13]
	s_barrier
	s_add_i32 vcc_lo, s92, s64
	v_lshl_add_u64 v[184:185], s[58:59], 0, v[146:147]
	s_mov_b32 m0, vcc_lo
	ds_read_b128 v[212:215], v193 offset:16384
	ds_read_b128 v[216:219], v193 offset:18432
	ds_read_b128 v[220:223], v194 offset:16384
	ds_read_b128 v[224:227], v194 offset:18432
	ds_read_b128 v[228:231], v193 offset:20480
	ds_read_b128 v[232:235], v193 offset:22528
	ds_read_b128 v[236:239], v194 offset:20480
	ds_read_b128 v[240:243], v194 offset:22528
	global_load_lds_dwordx4 v[184:185], off
	s_add_i32 m0, vcc_lo, 0x2000
	s_add_u32 vcc_lo, s58, 0x40000
	v_lshl_add_u64 v[196:197], s[58:59], 0, v[148:149]
	s_addc_u32 vcc_hi, s59, 0
	s_add_i32 s18, s62, s64
	global_load_lds_dwordx4 v[196:197], off
	v_lshl_add_u64 v[244:245], vcc, 0, v[146:147]
	s_mov_b32 m0, s18
	s_nop 0
	global_load_lds_dwordx4 v[244:245], off
	v_lshl_add_u64 v[244:245], vcc, 0, v[148:149]
	s_add_i32 m0, s18, 0x2000
	s_nop 0
	global_load_lds_dwordx4 v[244:245], off
	v_lshl_add_u64 v[244:245], s[60:61], 0, v[150:151]
	s_mov_b32 m0, s55
	s_nop 0
	global_load_lds_dwordx4 v[244:245], off
	v_lshl_add_u64 v[244:245], s[60:61], 0, v[152:153]
	s_mov_b32 m0, s65
	s_nop 0
	global_load_lds_dwordx4 v[244:245], off
	s_waitcnt vmcnt(8)
	s_waitcnt lgkmcnt(0)
	s_barrier
; #define PG8_STAGE(bufoff, gbase, voff) do { _Pragma("unroll") for (int _i = 0; _i < 2; ++_i) \
;         __builtin_amdgcn_global_load_lds((const unsigned*)((const char*)(gbase) + (voff)[_i]), (LAS unsigned*)(lds + (bufoff) + ldsw + _i * 8192), 16, 0, 0); } while (0)
; #define PG8_LDA(dst, b, h) do { _Pragma("unroll") for (int m = 0; m < 4; ++m) _Pragma("unroll") for (int k = 0; k < 2; ++k) dst[m][k] = *(const LAS bf16x8*)(lds + PG8_SA(b, h) + ((aoff ^ (k * 64)) + m * 2048)); } while (0)
; #define PG8_LDB(dst, b, h) do { _Pragma("unroll") for (int n = 0; n < 2; ++n) _Pragma("unroll") for (int k = 0; k < 2; ++k) dst[n][k] = *(const LAS bf16x8*)(lds + PG8_SB(b, h) + ((boff ^ (k * 64)) + n * 2048)); } while (0)
; #define PG8_MMA(ai, bj, At, Bt) do { __builtin_amdgcn_s_setprio(1); _Pragma("unroll") for (int m = 0; m < 4; ++m) _Pragma("unroll") for (int n = 0; n < 2; ++n) _Pragma("unroll") for (int k = 0; k < 2; ++k) \
;         acc[ai][bj][m][n] = __builtin_amdgcn_mfma_f32_16x16x32_bf16(Bt[n][k], At[m][k], acc[ai][bj][m][n], 0, 0, 0); __builtin_amdgcn_s_setprio(0); } while (0)
; #define PG8_WAIT_V(n) asm volatile("s_waitcnt vmcnt(" #n ")" ::: "memory")
; #define PG8_WAIT_L(n) asm volatile("s_waitcnt lgkmcnt(" #n ")" ::: "memory")
; #define PG8_BAR __builtin_amdgcn_s_barrier()
; #define PG8_SCHED __builtin_amdgcn_sched_barrier(0)
;     ...
;             PG8_WAIT_V(8); PG8_WAIT_L(0); PG8_BAR; if (do1) { PG8_MMA(1, 0, At, B0); PG8_MMA(1, 1, At, B1); } PG8_BAR; PG8_SCHED;
;             PG8_LDB(B0, 1, 0); PG8_LDB(B1, 1, 1); PG8_SCHED; PG8_LDA(At, 1, 0); PG8_STAGE(PG8_SA(0, 1), a2, vs[1]);
;             PG8_WAIT_V(8); PG8_WAIT_L(0); PG8_BAR; if (do0) { PG8_MMA(0, 0, At, B0); PG8_MMA(0, 1, At, B1); } PG8_BAR; PG8_SCHED;
	s_waitcnt lgkmcnt(0)
	v_mfma_f32_16x16x32_bf16 v[118:121], v[130:133], v[212:215], v[118:121]
	v_mfma_f32_16x16x32_bf16 v[114:117], v[138:141], v[212:215], v[114:117]
	v_mfma_f32_16x16x32_bf16 v[86:89], v[130:133], v[216:219], v[86:89]
	v_mfma_f32_16x16x32_bf16 v[82:85], v[138:141], v[216:219], v[82:85]
	v_mfma_f32_16x16x32_bf16 v[54:57], v[130:133], v[228:231], v[54:57]
	v_mfma_f32_16x16x32_bf16 v[50:53], v[138:141], v[228:231], v[50:53]
	v_mfma_f32_16x16x32_bf16 v[22:25], v[130:133], v[232:235], v[22:25]
	v_mfma_f32_16x16x32_bf16 v[18:21], v[138:141], v[232:235], v[18:21]
	v_mfma_f32_16x16x32_bf16 v[118:121], v[134:137], v[220:223], v[118:121]
	v_mfma_f32_16x16x32_bf16 v[114:117], v[142:145], v[220:223], v[114:117]
	v_mfma_f32_16x16x32_bf16 v[86:89], v[134:137], v[224:227], v[86:89]
	v_mfma_f32_16x16x32_bf16 v[82:85], v[142:145], v[224:227], v[82:85]
	v_mfma_f32_16x16x32_bf16 v[54:57], v[134:137], v[236:239], v[54:57]
	v_mfma_f32_16x16x32_bf16 v[50:53], v[142:145], v[236:239], v[50:53]
	v_mfma_f32_16x16x32_bf16 v[22:25], v[134:137], v[240:243], v[22:25]
	v_mfma_f32_16x16x32_bf16 v[18:21], v[142:145], v[240:243], v[18:21]
	v_mfma_f32_16x16x32_bf16 v[102:105], v[180:183], v[212:215], v[102:105]
	v_mfma_f32_16x16x32_bf16 v[98:101], v[204:207], v[212:215], v[98:101]
	v_mfma_f32_16x16x32_bf16 v[70:73], v[180:183], v[216:219], v[70:73]
	v_mfma_f32_16x16x32_bf16 v[66:69], v[204:207], v[216:219], v[66:69]
	v_mfma_f32_16x16x32_bf16 v[38:41], v[180:183], v[228:231], v[38:41]
	v_mfma_f32_16x16x32_bf16 v[34:37], v[204:207], v[228:231], v[34:37]
	v_mfma_f32_16x16x32_bf16 v[6:9], v[180:183], v[232:235], v[6:9]
	v_mfma_f32_16x16x32_bf16 v[2:5], v[204:207], v[232:235], v[2:5]
	v_mfma_f32_16x16x32_bf16 v[102:105], v[200:203], v[220:223], v[102:105]
	v_mfma_f32_16x16x32_bf16 v[98:101], v[208:211], v[220:223], v[98:101]
	v_mfma_f32_16x16x32_bf16 v[70:73], v[200:203], v[224:227], v[70:73]
	v_mfma_f32_16x16x32_bf16 v[66:69], v[208:211], v[224:227], v[66:69]
	v_mfma_f32_16x16x32_bf16 v[38:41], v[200:203], v[236:239], v[38:41]
	v_mfma_f32_16x16x32_bf16 v[34:37], v[208:211], v[236:239], v[34:37]
	v_mfma_f32_16x16x32_bf16 v[6:9], v[200:203], v[240:243], v[6:9]
	v_mfma_f32_16x16x32_bf16 v[2:5], v[208:211], v[240:243], v[2:5]
	s_barrier
	s_add_i32 s18, 0, 0x18000
	s_add_i32 s19, 0, 0x1c000
	v_add_u32_e32 v130, s18, v161
	v_add_u32_e32 v134, s18, v188
	v_add_u32_e32 v138, s72, v161
	v_add_u32_e32 v142, s72, v188
	v_add_u32_e32 v158, s19, v161
	ds_read_b128 v[130:133], v130
	ds_read_b128 v[134:137], v134
	ds_read_b128 v[138:141], v138
	ds_read_b128 v[142:145], v142
	v_add_u32_e32 v195, s19, v188
	ds_read_b128 v[180:183], v158
	ds_read_b128 v[200:203], v195
	v_add_u32_e32 v158, s73, v161
	v_add_u32_e32 v195, s73, v188
	ds_read_b128 v[204:207], v158
	ds_read_b128 v[208:211], v195
	s_mov_b32 m0, s66
	v_lshl_add_u64 v[244:245], s[60:61], 0, v[154:155]
	ds_read_b128 v[212:215], v193 offset:32768
	ds_read_b128 v[216:219], v193 offset:34816
	ds_read_b128 v[220:223], v194 offset:32768
	ds_read_b128 v[224:227], v194 offset:34816
	ds_read_b128 v[228:231], v193 offset:36864
	ds_read_b128 v[232:235], v193 offset:38912
	ds_read_b128 v[236:239], v194 offset:36864
	ds_read_b128 v[240:243], v194 offset:38912
	global_load_lds_dwordx4 v[244:245], off
	v_lshl_add_u64 v[244:245], s[60:61], 0, v[156:157]
	s_mov_b32 m0, s67
	s_nop 0
	global_load_lds_dwordx4 v[244:245], off
	s_waitcnt vmcnt(8)
	s_waitcnt lgkmcnt(0)
	s_barrier
	s_waitcnt lgkmcnt(0)
	v_mfma_f32_16x16x32_bf16 v[126:129], v[130:133], v[212:215], v[126:129]
	v_mfma_f32_16x16x32_bf16 v[122:125], v[138:141], v[212:215], v[122:125]
	v_mfma_f32_16x16x32_bf16 v[94:97], v[130:133], v[216:219], v[94:97]
	v_mfma_f32_16x16x32_bf16 v[90:93], v[138:141], v[216:219], v[90:93]
	v_mfma_f32_16x16x32_bf16 v[62:65], v[130:133], v[228:231], v[62:65]
	v_mfma_f32_16x16x32_bf16 v[58:61], v[138:141], v[228:231], v[58:61]
	v_mfma_f32_16x16x32_bf16 v[30:33], v[130:133], v[232:235], v[30:33]
	v_mfma_f32_16x16x32_bf16 v[26:29], v[138:141], v[232:235], v[26:29]
	v_mfma_f32_16x16x32_bf16 v[126:129], v[134:137], v[220:223], v[126:129]
	v_mfma_f32_16x16x32_bf16 v[122:125], v[142:145], v[220:223], v[122:125]
	v_mfma_f32_16x16x32_bf16 v[94:97], v[134:137], v[224:227], v[94:97]
	v_mfma_f32_16x16x32_bf16 v[90:93], v[142:145], v[224:227], v[90:93]
	v_mfma_f32_16x16x32_bf16 v[62:65], v[134:137], v[236:239], v[62:65]
	v_mfma_f32_16x16x32_bf16 v[58:61], v[142:145], v[236:239], v[58:61]
	v_mfma_f32_16x16x32_bf16 v[30:33], v[134:137], v[240:243], v[30:33]
	v_mfma_f32_16x16x32_bf16 v[26:29], v[142:145], v[240:243], v[26:29]
	v_mfma_f32_16x16x32_bf16 v[110:113], v[180:183], v[212:215], v[110:113]
	v_mfma_f32_16x16x32_bf16 v[106:109], v[204:207], v[212:215], v[106:109]
	v_mfma_f32_16x16x32_bf16 v[78:81], v[180:183], v[216:219], v[78:81]
	v_mfma_f32_16x16x32_bf16 v[74:77], v[204:207], v[216:219], v[74:77]
	v_mfma_f32_16x16x32_bf16 v[46:49], v[180:183], v[228:231], v[46:49]
	v_mfma_f32_16x16x32_bf16 v[42:45], v[204:207], v[228:231], v[42:45]
	v_mfma_f32_16x16x32_bf16 v[14:17], v[180:183], v[232:235], v[14:17]
	v_mfma_f32_16x16x32_bf16 v[10:13], v[204:207], v[232:235], v[10:13]
	v_mfma_f32_16x16x32_bf16 v[110:113], v[200:203], v[220:223], v[110:113]
	v_mfma_f32_16x16x32_bf16 v[106:109], v[208:211], v[220:223], v[106:109]
	v_mfma_f32_16x16x32_bf16 v[78:81], v[200:203], v[224:227], v[78:81]
	v_mfma_f32_16x16x32_bf16 v[74:77], v[208:211], v[224:227], v[74:77]
	v_mfma_f32_16x16x32_bf16 v[46:49], v[200:203], v[236:239], v[46:49]
	v_mfma_f32_16x16x32_bf16 v[42:45], v[208:211], v[236:239], v[42:45]
	v_mfma_f32_16x16x32_bf16 v[14:17], v[200:203], v[240:243], v[14:17]
	v_mfma_f32_16x16x32_bf16 v[10:13], v[208:211], v[240:243], v[10:13]
	s_barrier
; #define PG8_STAGE(bufoff, gbase, voff) do { _Pragma("unroll") for (int _i = 0; _i < 2; ++_i) \
;         __builtin_amdgcn_global_load_lds((const unsigned*)((const char*)(gbase) + (voff)[_i]), (LAS unsigned*)(lds + (bufoff) + ldsw + _i * 8192), 16, 0, 0); } while (0)
; #define PG8_LDA(dst, b, h) do { _Pragma("unroll") for (int m = 0; m < 4; ++m) _Pragma("unroll") for (int k = 0; k < 2; ++k) dst[m][k] = *(const LAS bf16x8*)(lds + PG8_SA(b, h) + ((aoff ^ (k * 64)) + m * 2048)); } while (0)
; #define PG8_MMA(ai, bj, At, Bt) do { __builtin_amdgcn_s_setprio(1); _Pragma("unroll") for (int m = 0; m < 4; ++m) _Pragma("unroll") for (int n = 0; n < 2; ++n) _Pragma("unroll") for (int k = 0; k < 2; ++k) \
;         acc[ai][bj][m][n] = __builtin_amdgcn_mfma_f32_16x16x32_bf16(Bt[n][k], At[m][k], acc[ai][bj][m][n], 0, 0, 0); __builtin_amdgcn_s_setprio(0); } while (0)
; #define PG8_WAIT_V(n) asm volatile("s_waitcnt vmcnt(" #n ")" ::: "memory")
; #define PG8_WAIT_L(n) asm volatile("s_waitcnt lgkmcnt(" #n ")" ::: "memory")
; #define PG8_BAR __builtin_amdgcn_s_barrier()
; #define PG8_SCHED __builtin_amdgcn_sched_barrier(0)
;     ...
;             PG8_LDA(At, 1, 1); PG8_STAGE(PG8_SB(1, 0), b3, voffB); PG8_STAGE(PG8_SB(1, 1), b3 + hstep, voffB); PG8_STAGE(PG8_SA(1, 0), a3, vs[0]);
;             PG8_WAIT_V(8); PG8_WAIT_L(0); PG8_BAR; if (do1) { PG8_MMA(1, 0, At, B0); PG8_MMA(1, 1, At, B1); } PG8_BAR; PG8_SCHED;
;         }
	s_add_i32 s18, s18, s64
	v_lshl_add_u64 v[184:185], v[184:185], 0, s[10:11]
	s_mov_b32 m0, s18
	ds_read_b128 v[212:215], v193 offset:49152
	ds_read_b128 v[216:219], v193 offset:51200
	ds_read_b128 v[220:223], v194 offset:49152
	ds_read_b128 v[224:227], v194 offset:51200
	ds_read_b128 v[228:231], v193 offset:53248
	ds_read_b128 v[232:235], v193 offset:55296
	ds_read_b128 v[236:239], v194 offset:53248
	ds_read_b128 v[240:243], v194 offset:55296
	global_load_lds_dwordx4 v[184:185], off
	s_add_i32 m0, s18, 0x2000
	s_add_u32 s58, s58, 0x40080
	v_lshl_add_u64 v[184:185], v[196:197], 0, s[10:11]
	s_addc_u32 s59, s59, 0
	s_add_i32 s18, s19, s64
	global_load_lds_dwordx4 v[184:185], off
	v_lshl_add_u64 v[184:185], s[58:59], 0, v[146:147]
	s_mov_b32 m0, s18
	s_nop 0
	global_load_lds_dwordx4 v[184:185], off
	v_lshl_add_u64 v[184:185], s[58:59], 0, v[148:149]
	s_add_i32 m0, s18, 0x2000
	s_nop 0
	global_load_lds_dwordx4 v[184:185], off
	v_lshl_add_u64 v[184:185], s[56:57], 0, v[150:151]
	s_mov_b32 m0, s70
	s_nop 0
	global_load_lds_dwordx4 v[184:185], off
	v_lshl_add_u64 v[184:185], s[56:57], 0, v[152:153]
	s_mov_b32 m0, s71
	s_nop 0
	global_load_lds_dwordx4 v[184:185], off
	s_waitcnt vmcnt(8)
	s_waitcnt lgkmcnt(0)
	s_barrier
	s_waitcnt lgkmcnt(0)
	v_mfma_f32_16x16x32_bf16 v[118:121], v[130:133], v[212:215], v[118:121]
	v_mfma_f32_16x16x32_bf16 v[114:117], v[138:141], v[212:215], v[114:117]
	v_mfma_f32_16x16x32_bf16 v[86:89], v[130:133], v[216:219], v[86:89]
	v_mfma_f32_16x16x32_bf16 v[82:85], v[138:141], v[216:219], v[82:85]
	v_mfma_f32_16x16x32_bf16 v[54:57], v[130:133], v[228:231], v[54:57]
	v_mfma_f32_16x16x32_bf16 v[50:53], v[138:141], v[228:231], v[50:53]
	v_mfma_f32_16x16x32_bf16 v[22:25], v[130:133], v[232:235], v[22:25]
	v_mfma_f32_16x16x32_bf16 v[18:21], v[138:141], v[232:235], v[18:21]
	v_mfma_f32_16x16x32_bf16 v[118:121], v[134:137], v[220:223], v[118:121]
	v_mfma_f32_16x16x32_bf16 v[114:117], v[142:145], v[220:223], v[114:117]
	v_mfma_f32_16x16x32_bf16 v[86:89], v[134:137], v[224:227], v[86:89]
	v_mfma_f32_16x16x32_bf16 v[82:85], v[142:145], v[224:227], v[82:85]
	v_mfma_f32_16x16x32_bf16 v[54:57], v[134:137], v[236:239], v[54:57]
	v_mfma_f32_16x16x32_bf16 v[50:53], v[142:145], v[236:239], v[50:53]
	v_mfma_f32_16x16x32_bf16 v[22:25], v[134:137], v[240:243], v[22:25]
	v_mfma_f32_16x16x32_bf16 v[18:21], v[142:145], v[240:243], v[18:21]
	v_mfma_f32_16x16x32_bf16 v[102:105], v[180:183], v[212:215], v[102:105]
	v_mfma_f32_16x16x32_bf16 v[98:101], v[204:207], v[212:215], v[98:101]
	v_mfma_f32_16x16x32_bf16 v[70:73], v[180:183], v[216:219], v[70:73]
	v_mfma_f32_16x16x32_bf16 v[66:69], v[204:207], v[216:219], v[66:69]
	v_mfma_f32_16x16x32_bf16 v[38:41], v[180:183], v[228:231], v[38:41]
	v_mfma_f32_16x16x32_bf16 v[34:37], v[204:207], v[228:231], v[34:37]
	v_mfma_f32_16x16x32_bf16 v[6:9], v[180:183], v[232:235], v[6:9]
	v_mfma_f32_16x16x32_bf16 v[2:5], v[204:207], v[232:235], v[2:5]
	v_mfma_f32_16x16x32_bf16 v[102:105], v[200:203], v[220:223], v[102:105]
	v_mfma_f32_16x16x32_bf16 v[98:101], v[208:211], v[220:223], v[98:101]
	v_mfma_f32_16x16x32_bf16 v[70:73], v[200:203], v[224:227], v[70:73]
	v_mfma_f32_16x16x32_bf16 v[66:69], v[208:211], v[224:227], v[66:69]
	v_mfma_f32_16x16x32_bf16 v[38:41], v[200:203], v[236:239], v[38:41]
	v_mfma_f32_16x16x32_bf16 v[34:37], v[208:211], v[236:239], v[34:37]
	v_mfma_f32_16x16x32_bf16 v[6:9], v[200:203], v[240:243], v[6:9]
	v_mfma_f32_16x16x32_bf16 v[2:5], v[208:211], v[240:243], v[2:5]
	s_barrier
	s_add_i32 s95, s95, 2
	s_add_u32 s74, s74, 0x100
	s_addc_u32 s94, s94, 0
	s_add_u32 s0, s0, 0x8000
	s_addc_u32 s1, s1, 0
	s_cmp_gt_u32 s95, 13
	s_cbranch_scc0 .LBB0_1343
	s_and_b64 vcc, exec, s[12:13]
	s_cbranch_vccz .LBB0_1346
	s_barrier

; #define PG8_WAIT_V(n) asm volatile("s_waitcnt vmcnt(" #n ")" ::: "memory")
; #define PG8_WAIT_L(n) asm volatile("s_waitcnt lgkmcnt(" #n ")" ::: "memory")
; #define PG8_BAR __builtin_amdgcn_s_barrier()
;     ...
;         for (int t = 0; t < nt; t += 2) {
;             const bool last = (t == nt - 2);
;             const char* a1 = cA + (size_t)(t + 1) * kstepA;
;             const char* a2 = last ? nA : cA + (size_t)(t + 2) * kstepA; const char* b2 = last ? nB : cB + (size_t)(t + 2) * kstepB;
;             const char* a3 = a2 + kstepA; const char* b3 = b2 + kstepB;
;             unsigned vs[2][2];
;             if constexpr (GATHER) {
;                 if (last && has_next) {
; #pragma unroll
;                     for (int hh = 0; hh < 2; ++hh)
; #pragma unroll
;                         for (int i = 0; i < 2; ++i) voffN[hh][i] = (unsigned)idxl[(ui + 1) * 256 + hh * HALF + sR[i]] * (unsigned)(K * 2) + (unsigned)sC[i] * 2u;
;                 }
; #pragma unroll
;                 for (int hh = 0; hh < 2; ++hh)
; #pragma unroll
;                     for (int i = 0; i < 2; ++i) vs[hh][i] = last ? voffN[hh][i] : voffA[hh][i];
;             } else {
; #pragma unroll
;                 for (int hh = 0; hh < 2; ++hh)
; #pragma unroll
;                     for (int i = 0; i < 2; ++i) vs[hh][i] = voffA[hh][i];
;             }
;             PG8_LDB(B0, 0, 0); PG8_LDB(B1, 0, 1); PG8_SCHED; PG8_LDA(At, 0, 0); PG8_STAGE(PG8_SA(1, 1), a1, voffA[1]);
;             PG8_WAIT_V(8); PG8_WAIT_L(0); PG8_BAR; if (do0) { PG8_MMA(0, 0, At, B0); PG8_MMA(0, 1, At, B1); } PG8_BAR; PG8_SCHED;
;             PG8_LDA(At, 0, 1); PG8_STAGE(PG8_SB(0, 0), b2, voffB); PG8_STAGE(PG8_SB(0, 1), b2 + hstep, voffB); PG8_STAGE(PG8_SA(0, 0), a2, vs[0]);
;             PG8_WAIT_V(8); PG8_WAIT_L(0); PG8_BAR; if (do1) { PG8_MMA(1, 0, At, B0); PG8_MMA(1, 1, At, B1); } PG8_BAR; PG8_SCHED;
;             PG8_LDB(B0, 1, 0); PG8_LDB(B1, 1, 1); PG8_SCHED; PG8_LDA(At, 1, 0); PG8_STAGE(PG8_SA(0, 1), a2, vs[1]);
;             PG8_WAIT_V(8); PG8_WAIT_L(0); PG8_BAR; if (do0) { PG8_MMA(0, 0, At, B0); PG8_MMA(0, 1, At, B1); } PG8_BAR; PG8_SCHED;
;             PG8_LDA(At, 1, 1); PG8_STAGE(PG8_SB(1, 0), b3, voffB); PG8_STAGE(PG8_SB(1, 1), b3 + hstep, voffB); PG8_STAGE(PG8_SA(1, 0), a3, vs[0]);
;             PG8_WAIT_V(8); PG8_WAIT_L(0); PG8_BAR; if (do1) { PG8_MMA(1, 0, At, B0); PG8_MMA(1, 1, At, B1); } PG8_BAR; PG8_SCHED;
.LBB0_1498:
	v_add_u32_e32 v130, s70, v153
	v_add_u32_e32 v134, s70, v184
	v_add_u32_e32 v150, s71, v153
	v_add_u32_e32 v176, s71, v184
	ds_read_b128 v[130:133], v130
	ds_read_b128 v[134:137], v134
	ds_read_b128 v[172:175], v150
	ds_read_b128 v[176:179], v176
	v_add_u32_e32 v150, s92, v153
	v_add_u32_e32 v180, s92, v184
	ds_read_b128 v[192:195], v150
	ds_read_b128 v[200:203], v180
	v_add_u32_e32 v150, s93, v153
	s_add_u32 s6, s0, 0x4000
	v_add_u32_e32 v180, s93, v184
	ds_read_b128 v[204:207], v150
	ds_read_b128 v[208:211], v180
	s_addc_u32 s7, s1, 0
	s_cmp_eq_u32 s63, 12
	s_cselect_b32 s58, s9, s6
	s_cselect_b32 s59, s3, s7
	s_cselect_b32 s56, s37, s49
	s_cselect_b32 s57, s23, s62
	s_add_u32 s6, s58, 0x4000
	s_addc_u32 s7, s59, 0
	v_lshl_add_u64 v[180:181], s[0:1], 0, v[168:169]
	s_add_i32 m0, s61, 0xc000
	ds_read_b128 v[212:215], v189
	ds_read_b128 v[216:219], v189 offset:2048
	ds_read_b128 v[220:223], v190
	ds_read_b128 v[224:227], v190 offset:2048
	ds_read_b128 v[228:231], v189 offset:4096
	ds_read_b128 v[232:235], v189 offset:6144
	ds_read_b128 v[236:239], v190 offset:4096
	ds_read_b128 v[240:243], v190 offset:6144
	global_load_lds_dwordx4 v[180:181], off
	v_lshl_add_u64 v[180:181], s[0:1], 0, v[170:171]
	s_add_i32 m0, s61, 0xe000
	s_nop 0
	global_load_lds_dwordx4 v[180:181], off
	s_waitcnt vmcnt(8)
	s_waitcnt lgkmcnt(0)
	s_barrier
	s_waitcnt lgkmcnt(0)
	v_mfma_f32_16x16x32_bf16 v[126:129], v[130:133], v[212:215], v[126:129]
	v_mfma_f32_16x16x32_bf16 v[122:125], v[172:175], v[212:215], v[122:125]
	v_mfma_f32_16x16x32_bf16 v[94:97], v[130:133], v[216:219], v[94:97]
	v_mfma_f32_16x16x32_bf16 v[90:93], v[172:175], v[216:219], v[90:93]
	v_mfma_f32_16x16x32_bf16 v[62:65], v[130:133], v[228:231], v[62:65]
	v_mfma_f32_16x16x32_bf16 v[58:61], v[172:175], v[228:231], v[58:61]
	v_mfma_f32_16x16x32_bf16 v[30:33], v[130:133], v[232:235], v[30:33]
	v_mfma_f32_16x16x32_bf16 v[26:29], v[172:175], v[232:235], v[26:29]
	v_mfma_f32_16x16x32_bf16 v[126:129], v[134:137], v[220:223], v[126:129]
	v_mfma_f32_16x16x32_bf16 v[122:125], v[176:179], v[220:223], v[122:125]
	v_mfma_f32_16x16x32_bf16 v[94:97], v[134:137], v[224:227], v[94:97]
	v_mfma_f32_16x16x32_bf16 v[90:93], v[176:179], v[224:227], v[90:93]
	v_mfma_f32_16x16x32_bf16 v[62:65], v[134:137], v[236:239], v[62:65]
	v_mfma_f32_16x16x32_bf16 v[58:61], v[176:179], v[236:239], v[58:61]
	v_mfma_f32_16x16x32_bf16 v[30:33], v[134:137], v[240:243], v[30:33]
	v_mfma_f32_16x16x32_bf16 v[26:29], v[176:179], v[240:243], v[26:29]
	v_mfma_f32_16x16x32_bf16 v[110:113], v[192:195], v[212:215], v[110:113]
	v_mfma_f32_16x16x32_bf16 v[106:109], v[204:207], v[212:215], v[106:109]
	v_mfma_f32_16x16x32_bf16 v[78:81], v[192:195], v[216:219], v[78:81]
	v_mfma_f32_16x16x32_bf16 v[74:77], v[204:207], v[216:219], v[74:77]
	v_mfma_f32_16x16x32_bf16 v[46:49], v[192:195], v[228:231], v[46:49]
	v_mfma_f32_16x16x32_bf16 v[42:45], v[204:207], v[228:231], v[42:45]
	v_mfma_f32_16x16x32_bf16 v[14:17], v[192:195], v[232:235], v[14:17]
	v_mfma_f32_16x16x32_bf16 v[10:13], v[204:207], v[232:235], v[10:13]
	v_mfma_f32_16x16x32_bf16 v[110:113], v[200:203], v[220:223], v[110:113]
	v_mfma_f32_16x16x32_bf16 v[106:109], v[208:211], v[220:223], v[106:109]
	v_mfma_f32_16x16x32_bf16 v[78:81], v[200:203], v[224:227], v[78:81]
	v_mfma_f32_16x16x32_bf16 v[74:77], v[208:211], v[224:227], v[74:77]
	v_mfma_f32_16x16x32_bf16 v[46:49], v[200:203], v[236:239], v[46:49]
	v_mfma_f32_16x16x32_bf16 v[42:45], v[208:211], v[236:239], v[42:45]
	v_mfma_f32_16x16x32_bf16 v[14:17], v[200:203], v[240:243], v[14:17]
	v_mfma_f32_16x16x32_bf16 v[10:13], v[208:211], v[240:243], v[10:13]
	s_barrier
	s_add_i32 s18, s70, s60
	v_lshl_add_u64 v[180:181], s[56:57], 0, v[138:139]
	s_mov_b32 m0, s18
	ds_read_b128 v[212:215], v189 offset:16384
	ds_read_b128 v[216:219], v189 offset:18432
	ds_read_b128 v[220:223], v190 offset:16384
	ds_read_b128 v[224:227], v190 offset:18432
	ds_read_b128 v[228:231], v189 offset:20480
	ds_read_b128 v[232:235], v189 offset:22528
	ds_read_b128 v[236:239], v190 offset:20480
	ds_read_b128 v[240:243], v190 offset:22528
	global_load_lds_dwordx4 v[180:181], off
	s_add_i32 m0, s18, 0x2000
	s_add_u32 s72, s56, 0x40000
	v_lshl_add_u64 v[196:197], s[56:57], 0, v[140:141]
	s_addc_u32 s73, s57, 0
	s_add_i32 s18, s92, s60
	global_load_lds_dwordx4 v[196:197], off
	v_lshl_add_u64 v[244:245], s[72:73], 0, v[138:139]
	s_mov_b32 m0, s18
	s_nop 0
	global_load_lds_dwordx4 v[244:245], off
	v_lshl_add_u64 v[244:245], s[72:73], 0, v[140:141]
	s_add_i32 m0, s18, 0x2000
	s_nop 0
	global_load_lds_dwordx4 v[244:245], off
	v_lshl_add_u64 v[244:245], s[58:59], 0, v[142:143]
	s_mov_b32 m0, s61
	s_nop 0
	global_load_lds_dwordx4 v[244:245], off
	v_lshl_add_u64 v[244:245], s[58:59], 0, v[144:145]
	s_mov_b32 m0, s64
	s_nop 0
	global_load_lds_dwordx4 v[244:245], off
	s_waitcnt vmcnt(8)
	s_waitcnt lgkmcnt(0)
	s_barrier
; #define PG8_STAGE(bufoff, gbase, voff) do { _Pragma("unroll") for (int _i = 0; _i < 2; ++_i) \
;         __builtin_amdgcn_global_load_lds((const unsigned*)((const char*)(gbase) + (voff)[_i]), (LAS unsigned*)(lds + (bufoff) + ldsw + _i * 8192), 16, 0, 0); } while (0)
; #define PG8_LDA(dst, b, h) do { _Pragma("unroll") for (int m = 0; m < 4; ++m) _Pragma("unroll") for (int k = 0; k < 2; ++k) dst[m][k] = *(const LAS bf16x8*)(lds + PG8_SA(b, h) + ((aoff ^ (k * 64)) + m * 2048)); } while (0)
; #define PG8_LDB(dst, b, h) do { _Pragma("unroll") for (int n = 0; n < 2; ++n) _Pragma("unroll") for (int k = 0; k < 2; ++k) dst[n][k] = *(const LAS bf16x8*)(lds + PG8_SB(b, h) + ((boff ^ (k * 64)) + n * 2048)); } while (0)
; #define PG8_MMA(ai, bj, At, Bt) do { __builtin_amdgcn_s_setprio(1); _Pragma("unroll") for (int m = 0; m < 4; ++m) _Pragma("unroll") for (int n = 0; n < 2; ++n) _Pragma("unroll") for (int k = 0; k < 2; ++k) \
;         acc[ai][bj][m][n] = __builtin_amdgcn_mfma_f32_16x16x32_bf16(Bt[n][k], At[m][k], acc[ai][bj][m][n], 0, 0, 0); __builtin_amdgcn_s_setprio(0); } while (0)
; #define PG8_WAIT_V(n) asm volatile("s_waitcnt vmcnt(" #n ")" ::: "memory")
; #define PG8_WAIT_L(n) asm volatile("s_waitcnt lgkmcnt(" #n ")" ::: "memory")
; #define PG8_BAR __builtin_amdgcn_s_barrier()
;     ...
;             PG8_LDB(B0, 0, 0); PG8_LDB(B1, 0, 1); PG8_SCHED; PG8_LDA(At, 0, 0); PG8_STAGE(PG8_SA(1, 1), a1, voffA[1]);
;             PG8_WAIT_V(8); PG8_WAIT_L(0); PG8_BAR; if (do0) { PG8_MMA(0, 0, At, B0); PG8_MMA(0, 1, At, B1); } PG8_BAR; PG8_SCHED;
;             PG8_LDA(At, 0, 1); PG8_STAGE(PG8_SB(0, 0), b2, voffB); PG8_STAGE(PG8_SB(0, 1), b2 + hstep, voffB); PG8_STAGE(PG8_SA(0, 0), a2, vs[0]);
;             PG8_WAIT_V(8); PG8_WAIT_L(0); PG8_BAR; if (do1) { PG8_MMA(1, 0, At, B0); PG8_MMA(1, 1, At, B1); } PG8_BAR; PG8_SCHED;
;             PG8_LDB(B0, 1, 0); PG8_LDB(B1, 1, 1); PG8_SCHED; PG8_LDA(At, 1, 0); PG8_STAGE(PG8_SA(0, 1), a2, vs[1]);
;             PG8_WAIT_V(8); PG8_WAIT_L(0); PG8_BAR; if (do0) { PG8_MMA(0, 0, At, B0); PG8_MMA(0, 1, At, B1); } PG8_BAR; PG8_SCHED;
;             PG8_LDA(At, 1, 1); PG8_STAGE(PG8_SB(1, 0), b3, voffB); PG8_STAGE(PG8_SB(1, 1), b3 + hstep, voffB); PG8_STAGE(PG8_SA(1, 0), a3, vs[0]);
;             PG8_WAIT_V(8); PG8_WAIT_L(0); PG8_BAR; if (do1) { PG8_MMA(1, 0, At, B0); PG8_MMA(1, 1, At, B1); } PG8_BAR; PG8_SCHED;
	s_waitcnt lgkmcnt(0)
	v_mfma_f32_16x16x32_bf16 v[118:121], v[130:133], v[212:215], v[118:121]
	v_mfma_f32_16x16x32_bf16 v[114:117], v[172:175], v[212:215], v[114:117]
	v_mfma_f32_16x16x32_bf16 v[86:89], v[130:133], v[216:219], v[86:89]
	v_mfma_f32_16x16x32_bf16 v[82:85], v[172:175], v[216:219], v[82:85]
	v_mfma_f32_16x16x32_bf16 v[54:57], v[130:133], v[228:231], v[54:57]
	v_mfma_f32_16x16x32_bf16 v[50:53], v[172:175], v[228:231], v[50:53]
	v_mfma_f32_16x16x32_bf16 v[22:25], v[130:133], v[232:235], v[22:25]
	v_mfma_f32_16x16x32_bf16 v[18:21], v[172:175], v[232:235], v[18:21]
	v_mfma_f32_16x16x32_bf16 v[118:121], v[134:137], v[220:223], v[118:121]
	v_mfma_f32_16x16x32_bf16 v[114:117], v[176:179], v[220:223], v[114:117]
	v_mfma_f32_16x16x32_bf16 v[86:89], v[134:137], v[224:227], v[86:89]
	v_mfma_f32_16x16x32_bf16 v[82:85], v[176:179], v[224:227], v[82:85]
	v_mfma_f32_16x16x32_bf16 v[54:57], v[134:137], v[236:239], v[54:57]
	v_mfma_f32_16x16x32_bf16 v[50:53], v[176:179], v[236:239], v[50:53]
	v_mfma_f32_16x16x32_bf16 v[22:25], v[134:137], v[240:243], v[22:25]
	v_mfma_f32_16x16x32_bf16 v[18:21], v[176:179], v[240:243], v[18:21]
	v_mfma_f32_16x16x32_bf16 v[102:105], v[192:195], v[212:215], v[102:105]
	v_mfma_f32_16x16x32_bf16 v[98:101], v[204:207], v[212:215], v[98:101]
	v_mfma_f32_16x16x32_bf16 v[70:73], v[192:195], v[216:219], v[70:73]
	v_mfma_f32_16x16x32_bf16 v[66:69], v[204:207], v[216:219], v[66:69]
	v_mfma_f32_16x16x32_bf16 v[38:41], v[192:195], v[228:231], v[38:41]
	v_mfma_f32_16x16x32_bf16 v[34:37], v[204:207], v[228:231], v[34:37]
	v_mfma_f32_16x16x32_bf16 v[6:9], v[192:195], v[232:235], v[6:9]
	v_mfma_f32_16x16x32_bf16 v[2:5], v[204:207], v[232:235], v[2:5]
	v_mfma_f32_16x16x32_bf16 v[102:105], v[200:203], v[220:223], v[102:105]
	v_mfma_f32_16x16x32_bf16 v[98:101], v[208:211], v[220:223], v[98:101]
	v_mfma_f32_16x16x32_bf16 v[70:73], v[200:203], v[224:227], v[70:73]
	v_mfma_f32_16x16x32_bf16 v[66:69], v[208:211], v[224:227], v[66:69]
	v_mfma_f32_16x16x32_bf16 v[38:41], v[200:203], v[236:239], v[38:41]
	v_mfma_f32_16x16x32_bf16 v[34:37], v[208:211], v[236:239], v[34:37]
	v_mfma_f32_16x16x32_bf16 v[6:9], v[200:203], v[240:243], v[6:9]
	v_mfma_f32_16x16x32_bf16 v[2:5], v[208:211], v[240:243], v[2:5]
	s_barrier
	s_add_i32 s18, 0, 0x18000
	v_add_u32_e32 v130, s18, v153
	v_add_u32_e32 v134, s18, v184
	v_add_u32_e32 v150, s12, v153
	v_add_u32_e32 v176, s12, v184
	s_add_i32 s19, 0, 0x1c000
	ds_read_b128 v[130:133], v130
	ds_read_b128 v[134:137], v134
	ds_read_b128 v[172:175], v150
	ds_read_b128 v[176:179], v176
	v_add_u32_e32 v150, s19, v153
	v_add_u32_e32 v191, s19, v184
	ds_read_b128 v[192:195], v150
	ds_read_b128 v[200:203], v191
	v_add_u32_e32 v150, s13, v153
	v_add_u32_e32 v191, s13, v184
	ds_read_b128 v[204:207], v150
	ds_read_b128 v[208:211], v191
	s_mov_b32 m0, s65
	v_lshl_add_u64 v[244:245], s[58:59], 0, v[146:147]
	ds_read_b128 v[212:215], v189 offset:32768
	ds_read_b128 v[216:219], v189 offset:34816
	ds_read_b128 v[220:223], v190 offset:32768
	ds_read_b128 v[224:227], v190 offset:34816
	ds_read_b128 v[228:231], v189 offset:36864
	ds_read_b128 v[232:235], v189 offset:38912
	ds_read_b128 v[236:239], v190 offset:36864
	ds_read_b128 v[240:243], v190 offset:38912
	global_load_lds_dwordx4 v[244:245], off
	v_lshl_add_u64 v[244:245], s[58:59], 0, v[148:149]
	s_mov_b32 m0, s66
	s_nop 0
	global_load_lds_dwordx4 v[244:245], off
	s_waitcnt vmcnt(8)
	s_waitcnt lgkmcnt(0)
	s_barrier
	s_waitcnt lgkmcnt(0)
	v_mfma_f32_16x16x32_bf16 v[126:129], v[130:133], v[212:215], v[126:129]
	v_mfma_f32_16x16x32_bf16 v[122:125], v[172:175], v[212:215], v[122:125]
	v_mfma_f32_16x16x32_bf16 v[94:97], v[130:133], v[216:219], v[94:97]
	v_mfma_f32_16x16x32_bf16 v[90:93], v[172:175], v[216:219], v[90:93]
	v_mfma_f32_16x16x32_bf16 v[62:65], v[130:133], v[228:231], v[62:65]
	v_mfma_f32_16x16x32_bf16 v[58:61], v[172:175], v[228:231], v[58:61]
	v_mfma_f32_16x16x32_bf16 v[30:33], v[130:133], v[232:235], v[30:33]
	v_mfma_f32_16x16x32_bf16 v[26:29], v[172:175], v[232:235], v[26:29]
	v_mfma_f32_16x16x32_bf16 v[126:129], v[134:137], v[220:223], v[126:129]
	v_mfma_f32_16x16x32_bf16 v[122:125], v[176:179], v[220:223], v[122:125]
	v_mfma_f32_16x16x32_bf16 v[94:97], v[134:137], v[224:227], v[94:97]
	v_mfma_f32_16x16x32_bf16 v[90:93], v[176:179], v[224:227], v[90:93]
	v_mfma_f32_16x16x32_bf16 v[62:65], v[134:137], v[236:239], v[62:65]
	v_mfma_f32_16x16x32_bf16 v[58:61], v[176:179], v[236:239], v[58:61]
	v_mfma_f32_16x16x32_bf16 v[30:33], v[134:137], v[240:243], v[30:33]
	v_mfma_f32_16x16x32_bf16 v[26:29], v[176:179], v[240:243], v[26:29]
	v_mfma_f32_16x16x32_bf16 v[110:113], v[192:195], v[212:215], v[110:113]
	v_mfma_f32_16x16x32_bf16 v[106:109], v[204:207], v[212:215], v[106:109]
	v_mfma_f32_16x16x32_bf16 v[78:81], v[192:195], v[216:219], v[78:81]
	v_mfma_f32_16x16x32_bf16 v[74:77], v[204:207], v[216:219], v[74:77]
	v_mfma_f32_16x16x32_bf16 v[46:49], v[192:195], v[228:231], v[46:49]
	v_mfma_f32_16x16x32_bf16 v[42:45], v[204:207], v[228:231], v[42:45]
	v_mfma_f32_16x16x32_bf16 v[14:17], v[192:195], v[232:235], v[14:17]
	v_mfma_f32_16x16x32_bf16 v[10:13], v[204:207], v[232:235], v[10:13]
	v_mfma_f32_16x16x32_bf16 v[110:113], v[200:203], v[220:223], v[110:113]
	v_mfma_f32_16x16x32_bf16 v[106:109], v[208:211], v[220:223], v[106:109]
	v_mfma_f32_16x16x32_bf16 v[78:81], v[200:203], v[224:227], v[78:81]
	v_mfma_f32_16x16x32_bf16 v[74:77], v[208:211], v[224:227], v[74:77]
	v_mfma_f32_16x16x32_bf16 v[46:49], v[200:203], v[236:239], v[46:49]
	v_mfma_f32_16x16x32_bf16 v[42:45], v[208:211], v[236:239], v[42:45]
	v_mfma_f32_16x16x32_bf16 v[14:17], v[200:203], v[240:243], v[14:17]
	v_mfma_f32_16x16x32_bf16 v[10:13], v[208:211], v[240:243], v[10:13]
	s_barrier
; #define PG8_STAGE(bufoff, gbase, voff) do { _Pragma("unroll") for (int _i = 0; _i < 2; ++_i) \
;         __builtin_amdgcn_global_load_lds((const unsigned*)((const char*)(gbase) + (voff)[_i]), (LAS unsigned*)(lds + (bufoff) + ldsw + _i * 8192), 16, 0, 0); } while (0)
; #define PG8_LDA(dst, b, h) do { _Pragma("unroll") for (int m = 0; m < 4; ++m) _Pragma("unroll") for (int k = 0; k < 2; ++k) dst[m][k] = *(const LAS bf16x8*)(lds + PG8_SA(b, h) + ((aoff ^ (k * 64)) + m * 2048)); } while (0)
; #define PG8_MMA(ai, bj, At, Bt) do { __builtin_amdgcn_s_setprio(1); _Pragma("unroll") for (int m = 0; m < 4; ++m) _Pragma("unroll") for (int n = 0; n < 2; ++n) _Pragma("unroll") for (int k = 0; k < 2; ++k) \
;         acc[ai][bj][m][n] = __builtin_amdgcn_mfma_f32_16x16x32_bf16(Bt[n][k], At[m][k], acc[ai][bj][m][n], 0, 0, 0); __builtin_amdgcn_s_setprio(0); } while (0)
; #define PG8_WAIT_V(n) asm volatile("s_waitcnt vmcnt(" #n ")" ::: "memory")
; #define PG8_WAIT_L(n) asm volatile("s_waitcnt lgkmcnt(" #n ")" ::: "memory")
; #define PG8_BAR __builtin_amdgcn_s_barrier()
; #define PG8_SCHED __builtin_amdgcn_sched_barrier(0)
;     ...
;             PG8_LDA(At, 1, 1); PG8_STAGE(PG8_SB(1, 0), b3, voffB); PG8_STAGE(PG8_SB(1, 1), b3 + hstep, voffB); PG8_STAGE(PG8_SA(1, 0), a3, vs[0]);
;             PG8_WAIT_V(8); PG8_WAIT_L(0); PG8_BAR; if (do1) { PG8_MMA(1, 0, At, B0); PG8_MMA(1, 1, At, B1); } PG8_BAR; PG8_SCHED;
;         }
	s_add_i32 s18, s18, s60
	v_lshl_add_u64 v[180:181], v[180:181], 0, s[24:25]
	s_mov_b32 m0, s18
	ds_read_b128 v[212:215], v189 offset:49152
	ds_read_b128 v[216:219], v189 offset:51200
	ds_read_b128 v[220:223], v190 offset:49152
	ds_read_b128 v[224:227], v190 offset:51200
	ds_read_b128 v[228:231], v189 offset:53248
	ds_read_b128 v[232:235], v189 offset:55296
	ds_read_b128 v[236:239], v190 offset:53248
	ds_read_b128 v[240:243], v190 offset:55296
	global_load_lds_dwordx4 v[180:181], off
	s_add_i32 m0, s18, 0x2000
	s_add_u32 s56, s56, 0x40080
	v_lshl_add_u64 v[180:181], v[196:197], 0, s[24:25]
	s_addc_u32 s57, s57, 0
	s_add_i32 s18, s19, s60
	global_load_lds_dwordx4 v[180:181], off
	v_lshl_add_u64 v[180:181], s[56:57], 0, v[138:139]
	s_mov_b32 m0, s18
	s_nop 0
	global_load_lds_dwordx4 v[180:181], off
	v_lshl_add_u64 v[180:181], s[56:57], 0, v[140:141]
	s_add_i32 m0, s18, 0x2000
	s_nop 0
	global_load_lds_dwordx4 v[180:181], off
	v_lshl_add_u64 v[180:181], s[6:7], 0, v[142:143]
	s_mov_b32 m0, s68
	s_nop 0
	global_load_lds_dwordx4 v[180:181], off
	v_lshl_add_u64 v[180:181], s[6:7], 0, v[144:145]
	s_mov_b32 m0, s69
	s_nop 0
	global_load_lds_dwordx4 v[180:181], off
	s_waitcnt vmcnt(8)
	s_waitcnt lgkmcnt(0)
	s_barrier
	s_waitcnt lgkmcnt(0)
	v_mfma_f32_16x16x32_bf16 v[118:121], v[130:133], v[212:215], v[118:121]
	v_mfma_f32_16x16x32_bf16 v[114:117], v[172:175], v[212:215], v[114:117]
	v_mfma_f32_16x16x32_bf16 v[86:89], v[130:133], v[216:219], v[86:89]
	v_mfma_f32_16x16x32_bf16 v[82:85], v[172:175], v[216:219], v[82:85]
	v_mfma_f32_16x16x32_bf16 v[54:57], v[130:133], v[228:231], v[54:57]
	v_mfma_f32_16x16x32_bf16 v[50:53], v[172:175], v[228:231], v[50:53]
	v_mfma_f32_16x16x32_bf16 v[22:25], v[130:133], v[232:235], v[22:25]
	v_mfma_f32_16x16x32_bf16 v[18:21], v[172:175], v[232:235], v[18:21]
	v_mfma_f32_16x16x32_bf16 v[118:121], v[134:137], v[220:223], v[118:121]
	v_mfma_f32_16x16x32_bf16 v[114:117], v[176:179], v[220:223], v[114:117]
	v_mfma_f32_16x16x32_bf16 v[86:89], v[134:137], v[224:227], v[86:89]
	v_mfma_f32_16x16x32_bf16 v[82:85], v[176:179], v[224:227], v[82:85]
	v_mfma_f32_16x16x32_bf16 v[54:57], v[134:137], v[236:239], v[54:57]
	v_mfma_f32_16x16x32_bf16 v[50:53], v[176:179], v[236:239], v[50:53]
	v_mfma_f32_16x16x32_bf16 v[22:25], v[134:137], v[240:243], v[22:25]
	v_mfma_f32_16x16x32_bf16 v[18:21], v[176:179], v[240:243], v[18:21]
	v_mfma_f32_16x16x32_bf16 v[102:105], v[192:195], v[212:215], v[102:105]
	v_mfma_f32_16x16x32_bf16 v[98:101], v[204:207], v[212:215], v[98:101]
	v_mfma_f32_16x16x32_bf16 v[70:73], v[192:195], v[216:219], v[70:73]
	v_mfma_f32_16x16x32_bf16 v[66:69], v[204:207], v[216:219], v[66:69]
	v_mfma_f32_16x16x32_bf16 v[38:41], v[192:195], v[228:231], v[38:41]
	v_mfma_f32_16x16x32_bf16 v[34:37], v[204:207], v[228:231], v[34:37]
	v_mfma_f32_16x16x32_bf16 v[6:9], v[192:195], v[232:235], v[6:9]
	v_mfma_f32_16x16x32_bf16 v[2:5], v[204:207], v[232:235], v[2:5]
	v_mfma_f32_16x16x32_bf16 v[102:105], v[200:203], v[220:223], v[102:105]
	v_mfma_f32_16x16x32_bf16 v[98:101], v[208:211], v[220:223], v[98:101]
	v_mfma_f32_16x16x32_bf16 v[70:73], v[200:203], v[224:227], v[70:73]
	v_mfma_f32_16x16x32_bf16 v[66:69], v[208:211], v[224:227], v[66:69]
	v_mfma_f32_16x16x32_bf16 v[38:41], v[200:203], v[236:239], v[38:41]
	v_mfma_f32_16x16x32_bf16 v[34:37], v[208:211], v[236:239], v[34:37]
	v_mfma_f32_16x16x32_bf16 v[6:9], v[200:203], v[240:243], v[6:9]
	v_mfma_f32_16x16x32_bf16 v[2:5], v[208:211], v[240:243], v[2:5]
	s_barrier
	s_add_i32 s63, s63, 2
	s_add_u32 s49, s49, 0x100
	s_addc_u32 s62, s62, 0
	s_add_u32 s0, s0, 0x8000
	s_addc_u32 s1, s1, 0
	s_cmp_gt_u32 s63, 13
	s_cbranch_scc0 .LBB0_1498
	s_and_b64 vcc, exec, s[26:27]
	s_cbranch_vccz .LBB0_1502
	s_barrier
	s_cmp_gt_i32 s8, 7
	s_mov_b64 s[0:1], -1
	s_cbranch_scc1 .LBB0_1503

;     ...
;         const bool shortu = cur.pm >= SHORT_PM, do0 = (HALFM && cur.kq >= 0) ? cur.kq == 0 : (!shortu || wr == 0), do1 = (HALFM && cur.kq >= 0) ? cur.kq == 1 : !shortu;
;         for (int t = 0; t < nt; t += 2) {
;             const bool last = (t == nt - 2);
;             const char* a1 = cA + (size_t)(t + 1) * kstepA;
;             const char* a2 = last ? nA : cA + (size_t)(t + 2) * kstepA; const char* b2 = last ? nB : cB + (size_t)(t + 2) * kstepB;
;             const char* a3 = a2 + kstepA; const char* b3 = b2 + kstepB;
;             unsigned vs[2][2];
;             if constexpr (GATHER) {
;                 if (last && has_next) {
; #pragma unroll
;                     for (int hh = 0; hh < 2; ++hh)
; #pragma unroll
;                         for (int i = 0; i < 2; ++i) voffN[hh][i] = (unsigned)idxl[(ui + 1) * 256 + hh * HALF + sR[i]] * (unsigned)(K * 2) + (unsigned)sC[i] * 2u;
;                 }
; #pragma unroll
;                 for (int hh = 0; hh < 2; ++hh)
; #pragma unroll
;                     for (int i = 0; i < 2; ++i) vs[hh][i] = last ? voffN[hh][i] : voffA[hh][i];
;             } else {
; #pragma unroll
;                 for (int hh = 0; hh < 2; ++hh)
; #pragma unroll
;                     for (int i = 0; i < 2; ++i) vs[hh][i] = voffA[hh][i];
;             }
;             PG8_LDB(B0, 0, 0); PG8_LDB(B1, 0, 1); PG8_SCHED; PG8_LDA(At, 0, 0); PG8_STAGE(PG8_SA(1, 1), a1, voffA[1]);
;             PG8_WAIT_V(8); PG8_WAIT_L(0); PG8_BAR; if (do0) { PG8_MMA(0, 0, At, B0); PG8_MMA(0, 1, At, B1); } PG8_BAR; PG8_SCHED;
;             PG8_LDA(At, 0, 1); PG8_STAGE(PG8_SB(0, 0), b2, voffB); PG8_STAGE(PG8_SB(0, 1), b2 + hstep, voffB); PG8_STAGE(PG8_SA(0, 0), a2, vs[0]);
;             PG8_WAIT_V(8); PG8_WAIT_L(0); PG8_BAR; if (do1) { PG8_MMA(1, 0, At, B0); PG8_MMA(1, 1, At, B1); } PG8_BAR; PG8_SCHED;
;             PG8_LDB(B0, 1, 0); PG8_LDB(B1, 1, 1); PG8_SCHED; PG8_LDA(At, 1, 0); PG8_STAGE(PG8_SA(0, 1), a2, vs[1]);
;             PG8_WAIT_V(8); PG8_WAIT_L(0); PG8_BAR; if (do0) { PG8_MMA(0, 0, At, B0); PG8_MMA(0, 1, At, B1); } PG8_BAR; PG8_SCHED;
;             PG8_LDA(At, 1, 1); PG8_STAGE(PG8_SB(1, 0), b3, voffB); PG8_STAGE(PG8_SB(1, 1), b3 + hstep, voffB); PG8_STAGE(PG8_SA(1, 0), a3, vs[0]);
;             PG8_WAIT_V(8); PG8_WAIT_L(0); PG8_BAR; if (do1) { PG8_MMA(1, 0, At, B0); PG8_MMA(1, 1, At, B1); } PG8_BAR; PG8_SCHED;
.LBB0_1659:
	ds_read_b128 v[146:149], v218
	ds_read_b128 v[150:153], v219
	ds_read_b128 v[154:157], v220
	ds_read_b128 v[158:161], v221
	ds_read_b128 v[130:133], v222
	ds_read_b128 v[134:137], v223
	ds_read_b128 v[138:141], v224
	ds_read_b128 v[142:145], v225
	s_mov_b32 m0, s54
	v_lshl_add_u64 v[212:213], s[90:91], 0, v[208:209]
	s_waitcnt lgkmcnt(0)
	ds_read_b128 v[186:189], v226
	ds_read_b128 v[174:177], v226 offset:2048
	ds_read_b128 v[190:193], v227
	ds_read_b128 v[178:181], v227 offset:2048
	ds_read_b128 v[170:173], v226 offset:4096
	ds_read_b128 v[162:165], v226 offset:6144
	ds_read_b128 v[182:185], v227 offset:4096
	ds_read_b128 v[166:169], v227 offset:6144
	global_load_lds_dwordx4 v[212:213], off
	v_lshl_add_u64 v[212:213], s[90:91], 0, v[210:211]
	s_mov_b32 m0, s55
	s_and_b64 vcc, exec, s[0:1]
	global_load_lds_dwordx4 v[212:213], off
	s_waitcnt vmcnt(8)
	s_waitcnt lgkmcnt(0)
	s_barrier
	s_cbranch_vccnz .LBB0_1661
	s_waitcnt lgkmcnt(0)
	v_mfma_f32_16x16x32_bf16 v[114:117], v[146:149], v[186:189], v[114:117]
	v_mfma_f32_16x16x32_bf16 v[118:121], v[154:157], v[186:189], v[118:121]
	v_mfma_f32_16x16x32_bf16 v[82:85], v[146:149], v[174:177], v[82:85]
	v_mfma_f32_16x16x32_bf16 v[86:89], v[154:157], v[174:177], v[86:89]
	v_mfma_f32_16x16x32_bf16 v[50:53], v[146:149], v[170:173], v[50:53]
	v_mfma_f32_16x16x32_bf16 v[54:57], v[154:157], v[170:173], v[54:57]
	v_mfma_f32_16x16x32_bf16 v[18:21], v[146:149], v[162:165], v[18:21]
	v_mfma_f32_16x16x32_bf16 v[22:25], v[154:157], v[162:165], v[22:25]
	v_mfma_f32_16x16x32_bf16 v[114:117], v[150:153], v[190:193], v[114:117]
	v_mfma_f32_16x16x32_bf16 v[118:121], v[158:161], v[190:193], v[118:121]
	v_mfma_f32_16x16x32_bf16 v[82:85], v[150:153], v[178:181], v[82:85]
	v_mfma_f32_16x16x32_bf16 v[86:89], v[158:161], v[178:181], v[86:89]
	v_mfma_f32_16x16x32_bf16 v[50:53], v[150:153], v[182:185], v[50:53]
	v_mfma_f32_16x16x32_bf16 v[54:57], v[158:161], v[182:185], v[54:57]
	v_mfma_f32_16x16x32_bf16 v[18:21], v[150:153], v[166:169], v[18:21]
	v_mfma_f32_16x16x32_bf16 v[22:25], v[158:161], v[166:169], v[22:25]
	v_mfma_f32_16x16x32_bf16 v[98:101], v[130:133], v[186:189], v[98:101]
	v_mfma_f32_16x16x32_bf16 v[102:105], v[138:141], v[186:189], v[102:105]
	v_mfma_f32_16x16x32_bf16 v[66:69], v[130:133], v[174:177], v[66:69]
	v_mfma_f32_16x16x32_bf16 v[70:73], v[138:141], v[174:177], v[70:73]
	v_mfma_f32_16x16x32_bf16 v[34:37], v[130:133], v[170:173], v[34:37]
	v_mfma_f32_16x16x32_bf16 v[38:41], v[138:141], v[170:173], v[38:41]
	v_mfma_f32_16x16x32_bf16 v[6:9], v[130:133], v[162:165], v[6:9]
	v_mfma_f32_16x16x32_bf16 v[10:13], v[138:141], v[162:165], v[10:13]
	v_mfma_f32_16x16x32_bf16 v[98:101], v[134:137], v[190:193], v[98:101]
	v_mfma_f32_16x16x32_bf16 v[102:105], v[142:145], v[190:193], v[102:105]
	v_mfma_f32_16x16x32_bf16 v[66:69], v[134:137], v[178:181], v[66:69]
	v_mfma_f32_16x16x32_bf16 v[70:73], v[142:145], v[178:181], v[70:73]
	v_mfma_f32_16x16x32_bf16 v[34:37], v[134:137], v[182:185], v[34:37]
	v_mfma_f32_16x16x32_bf16 v[38:41], v[142:145], v[182:185], v[38:41]
	v_mfma_f32_16x16x32_bf16 v[6:9], v[134:137], v[166:169], v[6:9]
	v_mfma_f32_16x16x32_bf16 v[10:13], v[142:145], v[166:169], v[10:13]
.LBB0_1661:
	s_add_u32 s6, s90, s51
	s_addc_u32 s7, s91, s52
	s_add_u32 s18, s90, s50
	s_addc_u32 s19, s91, s41
	s_cmp_eq_u32 s53, 12
	s_cselect_b32 s27, s13, s7
	s_cselect_b32 s26, s12, s6
	s_cselect_b32 s25, s11, s19
	s_cselect_b32 s24, s10, s18
	s_barrier
	s_mov_b32 m0, s34
	v_lshl_add_u64 v[212:213], s[24:25], 0, v[196:197]
	s_add_u32 s6, s24, 0x40000
	s_waitcnt lgkmcnt(0)
	ds_read_b128 v[186:189], v226 offset:16384
	ds_read_b128 v[174:177], v226 offset:18432
	ds_read_b128 v[190:193], v227 offset:16384
	ds_read_b128 v[178:181], v227 offset:18432
	ds_read_b128 v[170:173], v226 offset:20480
	ds_read_b128 v[162:165], v226 offset:22528
	ds_read_b128 v[182:185], v227 offset:20480
	ds_read_b128 v[166:169], v227 offset:22528
	global_load_lds_dwordx4 v[212:213], off
	v_lshl_add_u64 v[214:215], s[24:25], 0, v[194:195]
	s_mov_b32 m0, s35
	s_addc_u32 s7, s25, 0
	global_load_lds_dwordx4 v[214:215], off
	v_lshl_add_u64 v[228:229], s[6:7], 0, v[196:197]
	s_mov_b32 m0, s36
	s_andn2_b64 vcc, exec, s[2:3]
	global_load_lds_dwordx4 v[228:229], off
	v_lshl_add_u64 v[228:229], s[6:7], 0, v[194:195]
	s_mov_b32 m0, s37
	s_nop 0
	global_load_lds_dwordx4 v[228:229], off
	v_lshl_add_u64 v[228:229], s[26:27], 0, v[200:201]
	s_mov_b32 m0, s31
	s_nop 0
	global_load_lds_dwordx4 v[228:229], off
	v_lshl_add_u64 v[228:229], s[26:27], 0, v[202:203]
	s_mov_b32 m0, s38
	s_nop 0
	global_load_lds_dwordx4 v[228:229], off
	s_waitcnt vmcnt(8)
	s_waitcnt lgkmcnt(0)
	v_cndmask_b32_e64 v228, 0, 1, s[2:3]
	v_cmp_ne_u32_e64 s[6:7], 1, v228
	s_barrier
	s_cbranch_vccnz .LBB0_1663
	s_waitcnt lgkmcnt(0)
	v_mfma_f32_16x16x32_bf16 v[126:129], v[146:149], v[186:189], v[126:129]
	v_mfma_f32_16x16x32_bf16 v[122:125], v[154:157], v[186:189], v[122:125]
	v_mfma_f32_16x16x32_bf16 v[94:97], v[146:149], v[174:177], v[94:97]
	v_mfma_f32_16x16x32_bf16 v[90:93], v[154:157], v[174:177], v[90:93]
	v_mfma_f32_16x16x32_bf16 v[62:65], v[146:149], v[170:173], v[62:65]
	v_mfma_f32_16x16x32_bf16 v[58:61], v[154:157], v[170:173], v[58:61]
	v_mfma_f32_16x16x32_bf16 v[30:33], v[146:149], v[162:165], v[30:33]
	v_mfma_f32_16x16x32_bf16 v[26:29], v[154:157], v[162:165], v[26:29]
	v_mfma_f32_16x16x32_bf16 v[126:129], v[150:153], v[190:193], v[126:129]
	v_mfma_f32_16x16x32_bf16 v[122:125], v[158:161], v[190:193], v[122:125]
	v_mfma_f32_16x16x32_bf16 v[94:97], v[150:153], v[178:181], v[94:97]
	v_mfma_f32_16x16x32_bf16 v[90:93], v[158:161], v[178:181], v[90:93]
	v_mfma_f32_16x16x32_bf16 v[62:65], v[150:153], v[182:185], v[62:65]
	v_mfma_f32_16x16x32_bf16 v[58:61], v[158:161], v[182:185], v[58:61]
	v_mfma_f32_16x16x32_bf16 v[30:33], v[150:153], v[166:169], v[30:33]
	v_mfma_f32_16x16x32_bf16 v[26:29], v[158:161], v[166:169], v[26:29]
	v_mfma_f32_16x16x32_bf16 v[110:113], v[130:133], v[186:189], v[110:113]
	v_mfma_f32_16x16x32_bf16 v[106:109], v[138:141], v[186:189], v[106:109]
	v_mfma_f32_16x16x32_bf16 v[78:81], v[130:133], v[174:177], v[78:81]
	v_mfma_f32_16x16x32_bf16 v[74:77], v[138:141], v[174:177], v[74:77]
	v_mfma_f32_16x16x32_bf16 v[46:49], v[130:133], v[170:173], v[46:49]
	v_mfma_f32_16x16x32_bf16 v[42:45], v[138:141], v[170:173], v[42:45]
	v_mfma_f32_16x16x32_bf16 v[14:17], v[130:133], v[162:165], v[14:17]
	v_mfma_f32_16x16x32_bf16 v[2:5], v[138:141], v[162:165], v[2:5]
	v_mfma_f32_16x16x32_bf16 v[110:113], v[134:137], v[190:193], v[110:113]
	v_mfma_f32_16x16x32_bf16 v[106:109], v[142:145], v[190:193], v[106:109]
	v_mfma_f32_16x16x32_bf16 v[78:81], v[134:137], v[178:181], v[78:81]
	v_mfma_f32_16x16x32_bf16 v[74:77], v[142:145], v[178:181], v[74:77]
	v_mfma_f32_16x16x32_bf16 v[46:49], v[134:137], v[182:185], v[46:49]
	v_mfma_f32_16x16x32_bf16 v[42:45], v[142:145], v[182:185], v[42:45]
	v_mfma_f32_16x16x32_bf16 v[14:17], v[134:137], v[166:169], v[14:17]
	v_mfma_f32_16x16x32_bf16 v[2:5], v[142:145], v[166:169], v[2:5]
; #define PG8_STAGE(bufoff, gbase, voff) do { _Pragma("unroll") for (int _i = 0; _i < 2; ++_i) \
;         __builtin_amdgcn_global_load_lds((const unsigned*)((const char*)(gbase) + (voff)[_i]), (LAS unsigned*)(lds + (bufoff) + ldsw + _i * 8192), 16, 0, 0); } while (0)
; #define PG8_LDA(dst, b, h) do { _Pragma("unroll") for (int m = 0; m < 4; ++m) _Pragma("unroll") for (int k = 0; k < 2; ++k) dst[m][k] = *(const LAS bf16x8*)(lds + PG8_SA(b, h) + ((aoff ^ (k * 64)) + m * 2048)); } while (0)
; #define PG8_LDB(dst, b, h) do { _Pragma("unroll") for (int n = 0; n < 2; ++n) _Pragma("unroll") for (int k = 0; k < 2; ++k) dst[n][k] = *(const LAS bf16x8*)(lds + PG8_SB(b, h) + ((boff ^ (k * 64)) + n * 2048)); } while (0)
; #define PG8_MMA(ai, bj, At, Bt) do { __builtin_amdgcn_s_setprio(1); _Pragma("unroll") for (int m = 0; m < 4; ++m) _Pragma("unroll") for (int n = 0; n < 2; ++n) _Pragma("unroll") for (int k = 0; k < 2; ++k) \
;         acc[ai][bj][m][n] = __builtin_amdgcn_mfma_f32_16x16x32_bf16(Bt[n][k], At[m][k], acc[ai][bj][m][n], 0, 0, 0); __builtin_amdgcn_s_setprio(0); } while (0)
; #define PG8_WAIT_V(n) asm volatile("s_waitcnt vmcnt(" #n ")" ::: "memory")
; #define PG8_WAIT_L(n) asm volatile("s_waitcnt lgkmcnt(" #n ")" ::: "memory")
; #define PG8_BAR __builtin_amdgcn_s_barrier()
;     ...
;             PG8_LDB(B0, 0, 0); PG8_LDB(B1, 0, 1); PG8_SCHED; PG8_LDA(At, 0, 0); PG8_STAGE(PG8_SA(1, 1), a1, voffA[1]);
;             PG8_WAIT_V(8); PG8_WAIT_L(0); PG8_BAR; if (do0) { PG8_MMA(0, 0, At, B0); PG8_MMA(0, 1, At, B1); } PG8_BAR; PG8_SCHED;
;             PG8_LDA(At, 0, 1); PG8_STAGE(PG8_SB(0, 0), b2, voffB); PG8_STAGE(PG8_SB(0, 1), b2 + hstep, voffB); PG8_STAGE(PG8_SA(0, 0), a2, vs[0]);
;             PG8_WAIT_V(8); PG8_WAIT_L(0); PG8_BAR; if (do1) { PG8_MMA(1, 0, At, B0); PG8_MMA(1, 1, At, B1); } PG8_BAR; PG8_SCHED;
;             PG8_LDB(B0, 1, 0); PG8_LDB(B1, 1, 1); PG8_SCHED; PG8_LDA(At, 1, 0); PG8_STAGE(PG8_SA(0, 1), a2, vs[1]);
;             PG8_WAIT_V(8); PG8_WAIT_L(0); PG8_BAR; if (do0) { PG8_MMA(0, 0, At, B0); PG8_MMA(0, 1, At, B1); } PG8_BAR; PG8_SCHED;
;             PG8_LDA(At, 1, 1); PG8_STAGE(PG8_SB(1, 0), b3, voffB); PG8_STAGE(PG8_SB(1, 1), b3 + hstep, voffB); PG8_STAGE(PG8_SA(1, 0), a3, vs[0]);
;             PG8_WAIT_V(8); PG8_WAIT_L(0); PG8_BAR; if (do1) { PG8_MMA(1, 0, At, B0); PG8_MMA(1, 1, At, B1); } PG8_BAR; PG8_SCHED;
.LBB0_1663:
	s_barrier
	v_add_u32_e32 v130, s58, v216
	v_add_u32_e32 v131, s58, v217
	ds_read_b128 v[146:149], v130
	ds_read_b128 v[150:153], v131
	v_add_u32_e32 v130, s56, v216
	v_add_u32_e32 v131, s56, v217
	ds_read_b128 v[154:157], v130
	ds_read_b128 v[158:161], v131
	v_add_u32_e32 v130, s59, v216
	v_add_u32_e32 v134, s59, v217
	v_add_u32_e32 v138, s57, v216
	v_add_u32_e32 v142, s57, v217
	ds_read_b128 v[130:133], v130
	ds_read_b128 v[134:137], v134
	ds_read_b128 v[138:141], v138
	ds_read_b128 v[142:145], v142
	s_mov_b32 m0, s39
	v_lshl_add_u64 v[228:229], s[26:27], 0, v[204:205]
	s_waitcnt lgkmcnt(0)
	ds_read_b128 v[186:189], v226 offset:32768
	ds_read_b128 v[174:177], v226 offset:34816
	ds_read_b128 v[190:193], v227 offset:32768
	ds_read_b128 v[178:181], v227 offset:34816
	ds_read_b128 v[170:173], v226 offset:36864
	ds_read_b128 v[162:165], v226 offset:38912
	ds_read_b128 v[182:185], v227 offset:36864
	ds_read_b128 v[166:169], v227 offset:38912
	global_load_lds_dwordx4 v[228:229], off
	v_lshl_add_u64 v[228:229], s[26:27], 0, v[206:207]
	s_mov_b32 m0, s40
	s_and_b64 vcc, exec, s[0:1]
	global_load_lds_dwordx4 v[228:229], off
	s_waitcnt vmcnt(8)
	s_waitcnt lgkmcnt(0)
	s_barrier
	s_cbranch_vccnz .LBB0_1665
	s_waitcnt lgkmcnt(0)
	v_mfma_f32_16x16x32_bf16 v[114:117], v[146:149], v[186:189], v[114:117]
	v_mfma_f32_16x16x32_bf16 v[118:121], v[154:157], v[186:189], v[118:121]
	v_mfma_f32_16x16x32_bf16 v[82:85], v[146:149], v[174:177], v[82:85]
	v_mfma_f32_16x16x32_bf16 v[86:89], v[154:157], v[174:177], v[86:89]
	v_mfma_f32_16x16x32_bf16 v[50:53], v[146:149], v[170:173], v[50:53]
	v_mfma_f32_16x16x32_bf16 v[54:57], v[154:157], v[170:173], v[54:57]
	v_mfma_f32_16x16x32_bf16 v[18:21], v[146:149], v[162:165], v[18:21]
	v_mfma_f32_16x16x32_bf16 v[22:25], v[154:157], v[162:165], v[22:25]
	v_mfma_f32_16x16x32_bf16 v[114:117], v[150:153], v[190:193], v[114:117]
	v_mfma_f32_16x16x32_bf16 v[118:121], v[158:161], v[190:193], v[118:121]
	v_mfma_f32_16x16x32_bf16 v[82:85], v[150:153], v[178:181], v[82:85]
	v_mfma_f32_16x16x32_bf16 v[86:89], v[158:161], v[178:181], v[86:89]
	v_mfma_f32_16x16x32_bf16 v[50:53], v[150:153], v[182:185], v[50:53]
	v_mfma_f32_16x16x32_bf16 v[54:57], v[158:161], v[182:185], v[54:57]
	v_mfma_f32_16x16x32_bf16 v[18:21], v[150:153], v[166:169], v[18:21]
	v_mfma_f32_16x16x32_bf16 v[22:25], v[158:161], v[166:169], v[22:25]
	v_mfma_f32_16x16x32_bf16 v[98:101], v[130:133], v[186:189], v[98:101]
	v_mfma_f32_16x16x32_bf16 v[102:105], v[138:141], v[186:189], v[102:105]
	v_mfma_f32_16x16x32_bf16 v[66:69], v[130:133], v[174:177], v[66:69]
	v_mfma_f32_16x16x32_bf16 v[70:73], v[138:141], v[174:177], v[70:73]
	v_mfma_f32_16x16x32_bf16 v[34:37], v[130:133], v[170:173], v[34:37]
	v_mfma_f32_16x16x32_bf16 v[38:41], v[138:141], v[170:173], v[38:41]
	v_mfma_f32_16x16x32_bf16 v[6:9], v[130:133], v[162:165], v[6:9]
	v_mfma_f32_16x16x32_bf16 v[10:13], v[138:141], v[162:165], v[10:13]
	v_mfma_f32_16x16x32_bf16 v[98:101], v[134:137], v[190:193], v[98:101]
	v_mfma_f32_16x16x32_bf16 v[102:105], v[142:145], v[190:193], v[102:105]
	v_mfma_f32_16x16x32_bf16 v[66:69], v[134:137], v[178:181], v[66:69]
	v_mfma_f32_16x16x32_bf16 v[70:73], v[142:145], v[178:181], v[70:73]
	v_mfma_f32_16x16x32_bf16 v[34:37], v[134:137], v[182:185], v[34:37]
	v_mfma_f32_16x16x32_bf16 v[38:41], v[142:145], v[182:185], v[38:41]
	v_mfma_f32_16x16x32_bf16 v[6:9], v[134:137], v[166:169], v[6:9]
	v_mfma_f32_16x16x32_bf16 v[10:13], v[142:145], v[166:169], v[10:13]
; #define PG8_STAGE(bufoff, gbase, voff) do { _Pragma("unroll") for (int _i = 0; _i < 2; ++_i) \
;         __builtin_amdgcn_global_load_lds((const unsigned*)((const char*)(gbase) + (voff)[_i]), (LAS unsigned*)(lds + (bufoff) + ldsw + _i * 8192), 16, 0, 0); } while (0)
; #define PG8_LDA(dst, b, h) do { _Pragma("unroll") for (int m = 0; m < 4; ++m) _Pragma("unroll") for (int k = 0; k < 2; ++k) dst[m][k] = *(const LAS bf16x8*)(lds + PG8_SA(b, h) + ((aoff ^ (k * 64)) + m * 2048)); } while (0)
; #define PG8_MMA(ai, bj, At, Bt) do { __builtin_amdgcn_s_setprio(1); _Pragma("unroll") for (int m = 0; m < 4; ++m) _Pragma("unroll") for (int n = 0; n < 2; ++n) _Pragma("unroll") for (int k = 0; k < 2; ++k) \
;         acc[ai][bj][m][n] = __builtin_amdgcn_mfma_f32_16x16x32_bf16(Bt[n][k], At[m][k], acc[ai][bj][m][n], 0, 0, 0); __builtin_amdgcn_s_setprio(0); } while (0)
; #define PG8_WAIT_V(n) asm volatile("s_waitcnt vmcnt(" #n ")" ::: "memory")
; #define PG8_WAIT_L(n) asm volatile("s_waitcnt lgkmcnt(" #n ")" ::: "memory")
; #define PG8_BAR __builtin_amdgcn_s_barrier()
; #define PG8_SCHED __builtin_amdgcn_sched_barrier(0)
;     ...
;             PG8_LDA(At, 1, 1); PG8_STAGE(PG8_SB(1, 0), b3, voffB); PG8_STAGE(PG8_SB(1, 1), b3 + hstep, voffB); PG8_STAGE(PG8_SA(1, 0), a3, vs[0]);
;             PG8_WAIT_V(8); PG8_WAIT_L(0); PG8_BAR; if (do1) { PG8_MMA(1, 0, At, B0); PG8_MMA(1, 1, At, B1); } PG8_BAR; PG8_SCHED;
;         }
.LBB0_1665:
	s_add_u32 s26, s26, 0x4000
	s_addc_u32 s27, s27, 0
	s_barrier
	s_mov_b32 m0, s44
	v_lshl_add_u64 v[212:213], v[212:213], 0, s[14:15]
	s_add_u32 s24, s24, 0x40080
	s_waitcnt lgkmcnt(0)
	ds_read_b128 v[186:189], v226 offset:49152
	ds_read_b128 v[174:177], v226 offset:51200
	ds_read_b128 v[190:193], v227 offset:49152
	ds_read_b128 v[178:181], v227 offset:51200
	ds_read_b128 v[170:173], v226 offset:53248
	ds_read_b128 v[162:165], v226 offset:55296
	ds_read_b128 v[182:185], v227 offset:53248
	ds_read_b128 v[166:169], v227 offset:55296
	global_load_lds_dwordx4 v[212:213], off
	v_lshl_add_u64 v[212:213], v[214:215], 0, s[14:15]
	s_mov_b32 m0, s45
	s_addc_u32 s25, s25, 0
	global_load_lds_dwordx4 v[212:213], off
	v_lshl_add_u64 v[212:213], s[24:25], 0, v[196:197]
	s_mov_b32 m0, s48
	s_and_b64 vcc, exec, s[6:7]
	global_load_lds_dwordx4 v[212:213], off
	v_lshl_add_u64 v[212:213], s[24:25], 0, v[194:195]
	s_mov_b32 m0, s49
	s_nop 0
	global_load_lds_dwordx4 v[212:213], off
	v_lshl_add_u64 v[212:213], s[26:27], 0, v[200:201]
	s_mov_b32 m0, s46
	s_nop 0
	global_load_lds_dwordx4 v[212:213], off
	v_lshl_add_u64 v[212:213], s[26:27], 0, v[202:203]
	s_mov_b32 m0, s47
	s_nop 0
	global_load_lds_dwordx4 v[212:213], off
	s_waitcnt vmcnt(8)
	s_waitcnt lgkmcnt(0)
	s_barrier
	s_cbranch_vccnz .LBB0_1658
	s_waitcnt lgkmcnt(0)
	v_mfma_f32_16x16x32_bf16 v[126:129], v[146:149], v[186:189], v[126:129]
	v_mfma_f32_16x16x32_bf16 v[122:125], v[154:157], v[186:189], v[122:125]
	v_mfma_f32_16x16x32_bf16 v[94:97], v[146:149], v[174:177], v[94:97]
	v_mfma_f32_16x16x32_bf16 v[90:93], v[154:157], v[174:177], v[90:93]
	v_mfma_f32_16x16x32_bf16 v[62:65], v[146:149], v[170:173], v[62:65]
	v_mfma_f32_16x16x32_bf16 v[58:61], v[154:157], v[170:173], v[58:61]
	v_mfma_f32_16x16x32_bf16 v[30:33], v[146:149], v[162:165], v[30:33]
	v_mfma_f32_16x16x32_bf16 v[26:29], v[154:157], v[162:165], v[26:29]
	v_mfma_f32_16x16x32_bf16 v[126:129], v[150:153], v[190:193], v[126:129]
	v_mfma_f32_16x16x32_bf16 v[122:125], v[158:161], v[190:193], v[122:125]
	v_mfma_f32_16x16x32_bf16 v[94:97], v[150:153], v[178:181], v[94:97]
	v_mfma_f32_16x16x32_bf16 v[90:93], v[158:161], v[178:181], v[90:93]
	v_mfma_f32_16x16x32_bf16 v[62:65], v[150:153], v[182:185], v[62:65]
	v_mfma_f32_16x16x32_bf16 v[58:61], v[158:161], v[182:185], v[58:61]
	v_mfma_f32_16x16x32_bf16 v[30:33], v[150:153], v[166:169], v[30:33]
	v_mfma_f32_16x16x32_bf16 v[26:29], v[158:161], v[166:169], v[26:29]
	v_mfma_f32_16x16x32_bf16 v[110:113], v[130:133], v[186:189], v[110:113]
	v_mfma_f32_16x16x32_bf16 v[106:109], v[138:141], v[186:189], v[106:109]
	v_mfma_f32_16x16x32_bf16 v[78:81], v[130:133], v[174:177], v[78:81]
	v_mfma_f32_16x16x32_bf16 v[74:77], v[138:141], v[174:177], v[74:77]
	v_mfma_f32_16x16x32_bf16 v[46:49], v[130:133], v[170:173], v[46:49]
	v_mfma_f32_16x16x32_bf16 v[42:45], v[138:141], v[170:173], v[42:45]
	v_mfma_f32_16x16x32_bf16 v[14:17], v[130:133], v[162:165], v[14:17]
	v_mfma_f32_16x16x32_bf16 v[2:5], v[138:141], v[162:165], v[2:5]
	v_mfma_f32_16x16x32_bf16 v[110:113], v[134:137], v[190:193], v[110:113]
	v_mfma_f32_16x16x32_bf16 v[106:109], v[142:145], v[190:193], v[106:109]
	v_mfma_f32_16x16x32_bf16 v[78:81], v[134:137], v[178:181], v[78:81]
	v_mfma_f32_16x16x32_bf16 v[74:77], v[142:145], v[178:181], v[74:77]
	v_mfma_f32_16x16x32_bf16 v[46:49], v[134:137], v[182:185], v[46:49]
	v_mfma_f32_16x16x32_bf16 v[42:45], v[142:145], v[182:185], v[42:45]
	v_mfma_f32_16x16x32_bf16 v[14:17], v[134:137], v[166:169], v[14:17]
	v_mfma_f32_16x16x32_bf16 v[2:5], v[142:145], v[166:169], v[2:5]
	s_branch .LBB0_1658

; #define PG8_WAIT_V(n) asm volatile("s_waitcnt vmcnt(" #n ")" ::: "memory")
; #define PG8_WAIT_L(n) asm volatile("s_waitcnt lgkmcnt(" #n ")" ::: "memory")
; #define PG8_BAR __builtin_amdgcn_s_barrier()
;     ...
;         for (int t = 0; t < nt; t += 2) {
;             const bool last = (t == nt - 2);
;             const char* a1 = cA + (size_t)(t + 1) * kstepA;
;             const char* a2 = last ? nA : cA + (size_t)(t + 2) * kstepA; const char* b2 = last ? nB : cB + (size_t)(t + 2) * kstepB;
;             const char* a3 = a2 + kstepA; const char* b3 = b2 + kstepB;
;             unsigned vs[2][2];
;             if constexpr (GATHER) {
;                 if (last && has_next) {
; #pragma unroll
;                     for (int hh = 0; hh < 2; ++hh)
; #pragma unroll
;                         for (int i = 0; i < 2; ++i) voffN[hh][i] = (unsigned)idxl[(ui + 1) * 256 + hh * HALF + sR[i]] * (unsigned)(K * 2) + (unsigned)sC[i] * 2u;
;                 }
; #pragma unroll
;                 for (int hh = 0; hh < 2; ++hh)
; #pragma unroll
;                     for (int i = 0; i < 2; ++i) vs[hh][i] = last ? voffN[hh][i] : voffA[hh][i];
;             } else {
; #pragma unroll
;                 for (int hh = 0; hh < 2; ++hh)
; #pragma unroll
;                     for (int i = 0; i < 2; ++i) vs[hh][i] = voffA[hh][i];
;             }
;             PG8_LDB(B0, 0, 0); PG8_LDB(B1, 0, 1); PG8_SCHED; PG8_LDA(At, 0, 0); PG8_STAGE(PG8_SA(1, 1), a1, voffA[1]);
;             PG8_WAIT_V(8); PG8_WAIT_L(0); PG8_BAR; if (do0) { PG8_MMA(0, 0, At, B0); PG8_MMA(0, 1, At, B1); } PG8_BAR; PG8_SCHED;
;             PG8_LDA(At, 0, 1); PG8_STAGE(PG8_SB(0, 0), b2, voffB); PG8_STAGE(PG8_SB(0, 1), b2 + hstep, voffB); PG8_STAGE(PG8_SA(0, 0), a2, vs[0]);
;             PG8_WAIT_V(8); PG8_WAIT_L(0); PG8_BAR; if (do1) { PG8_MMA(1, 0, At, B0); PG8_MMA(1, 1, At, B1); } PG8_BAR; PG8_SCHED;
;             PG8_LDB(B0, 1, 0); PG8_LDB(B1, 1, 1); PG8_SCHED; PG8_LDA(At, 1, 0); PG8_STAGE(PG8_SA(0, 1), a2, vs[1]);
;             PG8_WAIT_V(8); PG8_WAIT_L(0); PG8_BAR; if (do0) { PG8_MMA(0, 0, At, B0); PG8_MMA(0, 1, At, B1); } PG8_BAR; PG8_SCHED;
;             PG8_LDA(At, 1, 1); PG8_STAGE(PG8_SB(1, 0), b3, voffB); PG8_STAGE(PG8_SB(1, 1), b3 + hstep, voffB); PG8_STAGE(PG8_SA(1, 0), a3, vs[0]);
;             PG8_WAIT_V(8); PG8_WAIT_L(0); PG8_BAR; if (do1) { PG8_MMA(1, 0, At, B0); PG8_MMA(1, 1, At, B1); } PG8_BAR; PG8_SCHED;
.LBB0_1934:
	ds_read_b128 v[74:77], v191
	ds_read_b128 v[78:81], v192
	ds_read_b128 v[102:105], v193
	ds_read_b128 v[106:109], v194
	ds_read_b128 v[168:171], v195
	ds_read_b128 v[172:175], v196
	ds_read_b128 v[176:179], v197
	ds_read_b128 v[180:183], v199
	s_add_u32 s38, s0, 0x80
	s_addc_u32 s39, s1, 0
	s_cmp_eq_u32 s45, 28
	s_cselect_b32 s43, s7, s39
	s_cselect_b32 s42, s8, s38
	s_cselect_b32 s39, s27, s44
	s_cselect_b32 s38, s29, s37
	v_lshl_add_u64 v[184:185], s[0:1], 0, v[162:163]
	s_add_i32 m0, s52, 0xc000
	ds_read_b128 v[210:213], v200
	ds_read_b128 v[214:217], v200 offset:2048
	ds_read_b128 v[218:221], v201
	ds_read_b128 v[222:225], v201 offset:2048
	ds_read_b128 v[226:229], v200 offset:4096
	ds_read_b128 v[230:233], v200 offset:6144
	ds_read_b128 v[234:237], v201 offset:4096
	ds_read_b128 v[238:241], v201 offset:6144
	global_load_lds_dwordx4 v[184:185], off
	v_lshl_add_u64 v[184:185], s[0:1], 0, v[160:161]
	s_add_i32 m0, s52, 0xe000
	s_add_u32 s40, s38, 0x4000
	global_load_lds_dwordx4 v[184:185], off
	s_waitcnt vmcnt(8)
	s_waitcnt lgkmcnt(0)
	s_addc_u32 s41, s39, 0
	s_barrier
	s_waitcnt lgkmcnt(0)
	v_mfma_f32_16x16x32_bf16 v[142:145], v[74:77], v[210:213], v[142:145]
	v_mfma_f32_16x16x32_bf16 v[10:13], v[102:105], v[210:213], v[10:13]
	v_mfma_f32_16x16x32_bf16 v[134:137], v[74:77], v[214:217], v[134:137]
	v_mfma_f32_16x16x32_bf16 v[18:21], v[102:105], v[214:217], v[18:21]
	v_mfma_f32_16x16x32_bf16 v[126:129], v[74:77], v[226:229], v[126:129]
	v_mfma_f32_16x16x32_bf16 v[22:25], v[102:105], v[226:229], v[22:25]
	v_mfma_f32_16x16x32_bf16 v[118:121], v[74:77], v[230:233], v[118:121]
	v_mfma_f32_16x16x32_bf16 v[34:37], v[102:105], v[230:233], v[34:37]
	v_mfma_f32_16x16x32_bf16 v[142:145], v[78:81], v[218:221], v[142:145]
	v_mfma_f32_16x16x32_bf16 v[10:13], v[106:109], v[218:221], v[10:13]
	v_mfma_f32_16x16x32_bf16 v[134:137], v[78:81], v[222:225], v[134:137]
	v_mfma_f32_16x16x32_bf16 v[18:21], v[106:109], v[222:225], v[18:21]
	v_mfma_f32_16x16x32_bf16 v[126:129], v[78:81], v[234:237], v[126:129]
	v_mfma_f32_16x16x32_bf16 v[22:25], v[106:109], v[234:237], v[22:25]
	v_mfma_f32_16x16x32_bf16 v[118:121], v[78:81], v[238:241], v[118:121]
	v_mfma_f32_16x16x32_bf16 v[34:37], v[106:109], v[238:241], v[34:37]
	v_mfma_f32_16x16x32_bf16 v[138:141], v[168:171], v[210:213], v[138:141]
	v_mfma_f32_16x16x32_bf16 v[14:17], v[176:179], v[210:213], v[14:17]
	v_mfma_f32_16x16x32_bf16 v[130:133], v[168:171], v[214:217], v[130:133]
	v_mfma_f32_16x16x32_bf16 v[30:33], v[176:179], v[214:217], v[30:33]
	v_mfma_f32_16x16x32_bf16 v[122:125], v[168:171], v[226:229], v[122:125]
	v_mfma_f32_16x16x32_bf16 v[26:29], v[176:179], v[226:229], v[26:29]
	v_mfma_f32_16x16x32_bf16 v[114:117], v[168:171], v[230:233], v[114:117]
	v_mfma_f32_16x16x32_bf16 v[46:49], v[176:179], v[230:233], v[46:49]
	v_mfma_f32_16x16x32_bf16 v[138:141], v[172:175], v[218:221], v[138:141]
	v_mfma_f32_16x16x32_bf16 v[14:17], v[180:183], v[218:221], v[14:17]
	v_mfma_f32_16x16x32_bf16 v[130:133], v[172:175], v[222:225], v[130:133]
	v_mfma_f32_16x16x32_bf16 v[30:33], v[180:183], v[222:225], v[30:33]
	v_mfma_f32_16x16x32_bf16 v[122:125], v[172:175], v[234:237], v[122:125]
	v_mfma_f32_16x16x32_bf16 v[26:29], v[180:183], v[234:237], v[26:29]
	v_mfma_f32_16x16x32_bf16 v[114:117], v[172:175], v[238:241], v[114:117]
	v_mfma_f32_16x16x32_bf16 v[46:49], v[180:183], v[238:241], v[46:49]
	s_barrier
	s_add_i32 s46, s67, s51
	v_lshl_add_u64 v[184:185], s[38:39], 0, v[146:147]
	s_mov_b32 m0, s46
	ds_read_b128 v[210:213], v200 offset:16384
	ds_read_b128 v[214:217], v200 offset:18432
	ds_read_b128 v[218:221], v201 offset:16384
	ds_read_b128 v[222:225], v201 offset:18432
	ds_read_b128 v[226:229], v200 offset:20480
	ds_read_b128 v[230:233], v200 offset:22528
	ds_read_b128 v[234:237], v201 offset:20480
	ds_read_b128 v[238:241], v201 offset:22528
	global_load_lds_dwordx4 v[184:185], off
	s_add_i32 m0, s46, 0x2000
	s_add_u32 s46, s38, 0x80000
	v_lshl_add_u64 v[184:185], s[38:39], 0, v[148:149]
	s_addc_u32 s47, s39, 0
	s_add_i32 s72, s68, s51
	global_load_lds_dwordx4 v[184:185], off
	v_lshl_add_u64 v[184:185], s[46:47], 0, v[146:147]
	s_mov_b32 m0, s72
	v_lshl_add_u64 v[242:243], s[42:43], 0, v[152:153]
	global_load_lds_dwordx4 v[184:185], off
	v_lshl_add_u64 v[184:185], s[46:47], 0, v[148:149]
	s_add_i32 m0, s72, 0x2000
	s_nop 0
	global_load_lds_dwordx4 v[184:185], off
	v_lshl_add_u64 v[184:185], s[42:43], 0, v[150:151]
	s_mov_b32 m0, s52
	s_nop 0
	global_load_lds_dwordx4 v[184:185], off
	s_mov_b32 m0, s53
	s_nop 0
	global_load_lds_dwordx4 v[242:243], off
	s_waitcnt vmcnt(8)
	s_waitcnt lgkmcnt(0)
	s_barrier
; #define PG8_STAGE(bufoff, gbase, voff) do { _Pragma("unroll") for (int _i = 0; _i < 2; ++_i) \
;         __builtin_amdgcn_global_load_lds((const unsigned*)((const char*)(gbase) + (voff)[_i]), (LAS unsigned*)(lds + (bufoff) + ldsw + _i * 8192), 16, 0, 0); } while (0)
; #define PG8_LDA(dst, b, h) do { _Pragma("unroll") for (int m = 0; m < 4; ++m) _Pragma("unroll") for (int k = 0; k < 2; ++k) dst[m][k] = *(const LAS bf16x8*)(lds + PG8_SA(b, h) + ((aoff ^ (k * 64)) + m * 2048)); } while (0)
; #define PG8_LDB(dst, b, h) do { _Pragma("unroll") for (int n = 0; n < 2; ++n) _Pragma("unroll") for (int k = 0; k < 2; ++k) dst[n][k] = *(const LAS bf16x8*)(lds + PG8_SB(b, h) + ((boff ^ (k * 64)) + n * 2048)); } while (0)
; #define PG8_MMA(ai, bj, At, Bt) do { __builtin_amdgcn_s_setprio(1); _Pragma("unroll") for (int m = 0; m < 4; ++m) _Pragma("unroll") for (int n = 0; n < 2; ++n) _Pragma("unroll") for (int k = 0; k < 2; ++k) \
;         acc[ai][bj][m][n] = __builtin_amdgcn_mfma_f32_16x16x32_bf16(Bt[n][k], At[m][k], acc[ai][bj][m][n], 0, 0, 0); __builtin_amdgcn_s_setprio(0); } while (0)
; #define PG8_WAIT_V(n) asm volatile("s_waitcnt vmcnt(" #n ")" ::: "memory")
; #define PG8_WAIT_L(n) asm volatile("s_waitcnt lgkmcnt(" #n ")" ::: "memory")
; #define PG8_BAR __builtin_amdgcn_s_barrier()
;     ...
;             PG8_LDB(B0, 0, 0); PG8_LDB(B1, 0, 1); PG8_SCHED; PG8_LDA(At, 0, 0); PG8_STAGE(PG8_SA(1, 1), a1, voffA[1]);
;             PG8_WAIT_V(8); PG8_WAIT_L(0); PG8_BAR; if (do0) { PG8_MMA(0, 0, At, B0); PG8_MMA(0, 1, At, B1); } PG8_BAR; PG8_SCHED;
;             PG8_LDA(At, 0, 1); PG8_STAGE(PG8_SB(0, 0), b2, voffB); PG8_STAGE(PG8_SB(0, 1), b2 + hstep, voffB); PG8_STAGE(PG8_SA(0, 0), a2, vs[0]);
;             PG8_WAIT_V(8); PG8_WAIT_L(0); PG8_BAR; if (do1) { PG8_MMA(1, 0, At, B0); PG8_MMA(1, 1, At, B1); } PG8_BAR; PG8_SCHED;
;             PG8_LDB(B0, 1, 0); PG8_LDB(B1, 1, 1); PG8_SCHED; PG8_LDA(At, 1, 0); PG8_STAGE(PG8_SA(0, 1), a2, vs[1]);
;             PG8_WAIT_V(8); PG8_WAIT_L(0); PG8_BAR; if (do0) { PG8_MMA(0, 0, At, B0); PG8_MMA(0, 1, At, B1); } PG8_BAR; PG8_SCHED;
;             PG8_LDA(At, 1, 1); PG8_STAGE(PG8_SB(1, 0), b3, voffB); PG8_STAGE(PG8_SB(1, 1), b3 + hstep, voffB); PG8_STAGE(PG8_SA(1, 0), a3, vs[0]);
;             PG8_WAIT_V(8); PG8_WAIT_L(0); PG8_BAR; if (do1) { PG8_MMA(1, 0, At, B0); PG8_MMA(1, 1, At, B1); } PG8_BAR; PG8_SCHED;
	s_waitcnt lgkmcnt(0)
	v_mfma_f32_16x16x32_bf16 v[110:113], v[74:77], v[210:213], v[110:113]
	v_mfma_f32_16x16x32_bf16 v[58:61], v[102:105], v[210:213], v[58:61]
	v_mfma_f32_16x16x32_bf16 v[94:97], v[74:77], v[214:217], v[94:97]
	v_mfma_f32_16x16x32_bf16 v[82:85], v[102:105], v[214:217], v[82:85]
	v_mfma_f32_16x16x32_bf16 v[66:69], v[74:77], v[226:229], v[66:69]
	v_mfma_f32_16x16x32_bf16 v[62:65], v[102:105], v[226:229], v[62:65]
	v_mfma_f32_16x16x32_bf16 v[42:45], v[74:77], v[230:233], v[42:45]
	v_mfma_f32_16x16x32_bf16 v[38:41], v[102:105], v[230:233], v[38:41]
	v_mfma_f32_16x16x32_bf16 v[110:113], v[78:81], v[218:221], v[110:113]
	v_mfma_f32_16x16x32_bf16 v[58:61], v[106:109], v[218:221], v[58:61]
	v_mfma_f32_16x16x32_bf16 v[94:97], v[78:81], v[222:225], v[94:97]
	v_mfma_f32_16x16x32_bf16 v[82:85], v[106:109], v[222:225], v[82:85]
	v_mfma_f32_16x16x32_bf16 v[66:69], v[78:81], v[234:237], v[66:69]
	v_mfma_f32_16x16x32_bf16 v[62:65], v[106:109], v[234:237], v[62:65]
	v_mfma_f32_16x16x32_bf16 v[42:45], v[78:81], v[238:241], v[42:45]
	v_mfma_f32_16x16x32_bf16 v[38:41], v[106:109], v[238:241], v[38:41]
	v_mfma_f32_16x16x32_bf16 v[70:73], v[176:179], v[210:213], v[70:73]
	v_mfma_f32_16x16x32_bf16 v[86:89], v[176:179], v[214:217], v[86:89]
	v_mfma_f32_16x16x32_bf16 v[54:57], v[168:171], v[226:229], v[54:57]
	v_mfma_f32_16x16x32_bf16 v[50:53], v[176:179], v[226:229], v[50:53]
	v_mfma_f32_16x16x32_bf16 v[6:9], v[168:171], v[230:233], v[6:9]
	v_mfma_f32_16x16x32_bf16 v[2:5], v[176:179], v[230:233], v[2:5]
	v_mfma_f32_16x16x32_bf16 v[74:77], v[168:171], v[210:213], v[98:101]
	v_mfma_f32_16x16x32_bf16 v[70:73], v[180:183], v[218:221], v[70:73]
	v_mfma_f32_16x16x32_bf16 v[78:81], v[168:171], v[214:217], v[90:93]
	v_mfma_f32_16x16x32_bf16 v[86:89], v[180:183], v[222:225], v[86:89]
	v_mfma_f32_16x16x32_bf16 v[54:57], v[172:175], v[234:237], v[54:57]
	v_mfma_f32_16x16x32_bf16 v[50:53], v[180:183], v[234:237], v[50:53]
	v_mfma_f32_16x16x32_bf16 v[6:9], v[172:175], v[238:241], v[6:9]
	v_mfma_f32_16x16x32_bf16 v[2:5], v[180:183], v[238:241], v[2:5]
	v_mfma_f32_16x16x32_bf16 v[74:77], v[172:175], v[218:221], v[74:77]
	v_mfma_f32_16x16x32_bf16 v[78:81], v[172:175], v[222:225], v[78:81]
	s_barrier
	s_add_i32 s46, 0, 0x18000
	s_add_i32 s47, 0, 0x1c000
	v_add_u32_e32 v90, s46, v189
	v_add_u32_e32 v98, s46, v190
	v_add_u32_e32 v158, s47, v189
	v_add_u32_e32 v172, s47, v190
	ds_read_b128 v[90:93], v90
	ds_read_b128 v[98:101], v98
	ds_read_b128 v[102:105], v202
	ds_read_b128 v[106:109], v203
	ds_read_b128 v[168:171], v158
	ds_read_b128 v[172:175], v172
	ds_read_b128 v[176:179], v204
	ds_read_b128 v[180:183], v205
	s_mov_b32 m0, s54
	v_lshl_add_u64 v[244:245], s[42:43], 0, v[154:155]
	ds_read_b128 v[210:213], v200 offset:32768
	ds_read_b128 v[214:217], v200 offset:34816
	ds_read_b128 v[218:221], v201 offset:32768
	ds_read_b128 v[222:225], v201 offset:34816
	ds_read_b128 v[226:229], v200 offset:36864
	ds_read_b128 v[230:233], v200 offset:38912
	ds_read_b128 v[234:237], v201 offset:36864
	ds_read_b128 v[238:241], v201 offset:38912
	global_load_lds_dwordx4 v[244:245], off
	v_lshl_add_u64 v[244:245], s[42:43], 0, v[156:157]
	s_mov_b32 m0, s55
	s_nop 0
	global_load_lds_dwordx4 v[244:245], off
	s_waitcnt vmcnt(8)
	s_waitcnt lgkmcnt(0)
	s_barrier
	s_waitcnt lgkmcnt(0)
	v_mfma_f32_16x16x32_bf16 v[142:145], v[90:93], v[210:213], v[142:145]
	v_mfma_f32_16x16x32_bf16 v[10:13], v[102:105], v[210:213], v[10:13]
	v_mfma_f32_16x16x32_bf16 v[134:137], v[90:93], v[214:217], v[134:137]
	v_mfma_f32_16x16x32_bf16 v[18:21], v[102:105], v[214:217], v[18:21]
	v_mfma_f32_16x16x32_bf16 v[126:129], v[90:93], v[226:229], v[126:129]
	v_mfma_f32_16x16x32_bf16 v[22:25], v[102:105], v[226:229], v[22:25]
	v_mfma_f32_16x16x32_bf16 v[118:121], v[90:93], v[230:233], v[118:121]
	v_mfma_f32_16x16x32_bf16 v[34:37], v[102:105], v[230:233], v[34:37]
	v_mfma_f32_16x16x32_bf16 v[142:145], v[98:101], v[218:221], v[142:145]
	v_mfma_f32_16x16x32_bf16 v[10:13], v[106:109], v[218:221], v[10:13]
	v_mfma_f32_16x16x32_bf16 v[134:137], v[98:101], v[222:225], v[134:137]
	v_mfma_f32_16x16x32_bf16 v[18:21], v[106:109], v[222:225], v[18:21]
	v_mfma_f32_16x16x32_bf16 v[126:129], v[98:101], v[234:237], v[126:129]
	v_mfma_f32_16x16x32_bf16 v[22:25], v[106:109], v[234:237], v[22:25]
	v_mfma_f32_16x16x32_bf16 v[118:121], v[98:101], v[238:241], v[118:121]
	v_mfma_f32_16x16x32_bf16 v[34:37], v[106:109], v[238:241], v[34:37]
	v_mfma_f32_16x16x32_bf16 v[138:141], v[168:171], v[210:213], v[138:141]
	v_mfma_f32_16x16x32_bf16 v[14:17], v[176:179], v[210:213], v[14:17]
	v_mfma_f32_16x16x32_bf16 v[130:133], v[168:171], v[214:217], v[130:133]
	v_mfma_f32_16x16x32_bf16 v[30:33], v[176:179], v[214:217], v[30:33]
	v_mfma_f32_16x16x32_bf16 v[122:125], v[168:171], v[226:229], v[122:125]
	v_mfma_f32_16x16x32_bf16 v[26:29], v[176:179], v[226:229], v[26:29]
	v_mfma_f32_16x16x32_bf16 v[114:117], v[168:171], v[230:233], v[114:117]
	v_mfma_f32_16x16x32_bf16 v[46:49], v[176:179], v[230:233], v[46:49]
	v_mfma_f32_16x16x32_bf16 v[138:141], v[172:175], v[218:221], v[138:141]
	v_mfma_f32_16x16x32_bf16 v[14:17], v[180:183], v[218:221], v[14:17]
	v_mfma_f32_16x16x32_bf16 v[130:133], v[172:175], v[222:225], v[130:133]
	v_mfma_f32_16x16x32_bf16 v[30:33], v[180:183], v[222:225], v[30:33]
	v_mfma_f32_16x16x32_bf16 v[122:125], v[172:175], v[234:237], v[122:125]
	v_mfma_f32_16x16x32_bf16 v[26:29], v[180:183], v[234:237], v[26:29]
	v_mfma_f32_16x16x32_bf16 v[114:117], v[172:175], v[238:241], v[114:117]
	v_mfma_f32_16x16x32_bf16 v[46:49], v[180:183], v[238:241], v[46:49]
	s_barrier
; #define PG8_STAGE(bufoff, gbase, voff) do { _Pragma("unroll") for (int _i = 0; _i < 2; ++_i) \
;         __builtin_amdgcn_global_load_lds((const unsigned*)((const char*)(gbase) + (voff)[_i]), (LAS unsigned*)(lds + (bufoff) + ldsw + _i * 8192), 16, 0, 0); } while (0)
; #define PG8_LDA(dst, b, h) do { _Pragma("unroll") for (int m = 0; m < 4; ++m) _Pragma("unroll") for (int k = 0; k < 2; ++k) dst[m][k] = *(const LAS bf16x8*)(lds + PG8_SA(b, h) + ((aoff ^ (k * 64)) + m * 2048)); } while (0)
; #define PG8_MMA(ai, bj, At, Bt) do { __builtin_amdgcn_s_setprio(1); _Pragma("unroll") for (int m = 0; m < 4; ++m) _Pragma("unroll") for (int n = 0; n < 2; ++n) _Pragma("unroll") for (int k = 0; k < 2; ++k) \
;         acc[ai][bj][m][n] = __builtin_amdgcn_mfma_f32_16x16x32_bf16(Bt[n][k], At[m][k], acc[ai][bj][m][n], 0, 0, 0); __builtin_amdgcn_s_setprio(0); } while (0)
; #define PG8_WAIT_V(n) asm volatile("s_waitcnt vmcnt(" #n ")" ::: "memory")
; #define PG8_WAIT_L(n) asm volatile("s_waitcnt lgkmcnt(" #n ")" ::: "memory")
; #define PG8_BAR __builtin_amdgcn_s_barrier()
; #define PG8_SCHED __builtin_amdgcn_sched_barrier(0)
;     ...
;             PG8_LDA(At, 1, 1); PG8_STAGE(PG8_SB(1, 0), b3, voffB); PG8_STAGE(PG8_SB(1, 1), b3 + hstep, voffB); PG8_STAGE(PG8_SA(1, 0), a3, vs[0]);
;             PG8_WAIT_V(8); PG8_WAIT_L(0); PG8_BAR; if (do1) { PG8_MMA(1, 0, At, B0); PG8_MMA(1, 1, At, B1); } PG8_BAR; PG8_SCHED;
;         }
	s_add_i32 s42, s46, s51
	v_lshl_add_u64 v[244:245], s[40:41], 0, v[146:147]
	s_mov_b32 m0, s42
	ds_read_b128 v[210:213], v200 offset:49152
	ds_read_b128 v[214:217], v200 offset:51200
	ds_read_b128 v[218:221], v201 offset:49152
	ds_read_b128 v[222:225], v201 offset:51200
	ds_read_b128 v[226:229], v200 offset:53248
	ds_read_b128 v[230:233], v200 offset:55296
	ds_read_b128 v[234:237], v201 offset:53248
	ds_read_b128 v[238:241], v201 offset:55296
	global_load_lds_dwordx4 v[244:245], off
	s_add_i32 m0, s42, 0x2000
	s_add_u32 s38, s38, 0x84000
	v_lshl_add_u64 v[244:245], s[40:41], 0, v[148:149]
	s_addc_u32 s39, s39, 0
	s_add_i32 s40, s47, s51
	global_load_lds_dwordx4 v[244:245], off
	v_lshl_add_u64 v[244:245], s[38:39], 0, v[146:147]
	s_mov_b32 m0, s40
	v_lshl_add_u64 v[184:185], v[184:185], 0, s[16:17]
	global_load_lds_dwordx4 v[244:245], off
	v_lshl_add_u64 v[244:245], s[38:39], 0, v[148:149]
	s_add_i32 m0, s40, 0x2000
	s_nop 0
	global_load_lds_dwordx4 v[244:245], off
	s_mov_b32 m0, s57
	s_nop 0
	global_load_lds_dwordx4 v[184:185], off
	v_lshl_add_u64 v[184:185], v[242:243], 0, s[16:17]
	s_mov_b32 m0, s58
	s_nop 0
	global_load_lds_dwordx4 v[184:185], off
	s_waitcnt vmcnt(8)
	s_waitcnt lgkmcnt(0)
	s_barrier
	s_waitcnt lgkmcnt(0)
	v_mfma_f32_16x16x32_bf16 v[110:113], v[90:93], v[210:213], v[110:113]
	v_mfma_f32_16x16x32_bf16 v[58:61], v[102:105], v[210:213], v[58:61]
	v_mfma_f32_16x16x32_bf16 v[94:97], v[90:93], v[214:217], v[94:97]
	v_mfma_f32_16x16x32_bf16 v[82:85], v[102:105], v[214:217], v[82:85]
	v_mfma_f32_16x16x32_bf16 v[66:69], v[90:93], v[226:229], v[66:69]
	v_mfma_f32_16x16x32_bf16 v[62:65], v[102:105], v[226:229], v[62:65]
	v_mfma_f32_16x16x32_bf16 v[42:45], v[90:93], v[230:233], v[42:45]
	v_mfma_f32_16x16x32_bf16 v[38:41], v[102:105], v[230:233], v[38:41]
	v_mfma_f32_16x16x32_bf16 v[110:113], v[98:101], v[218:221], v[110:113]
	v_mfma_f32_16x16x32_bf16 v[58:61], v[106:109], v[218:221], v[58:61]
	v_mfma_f32_16x16x32_bf16 v[94:97], v[98:101], v[222:225], v[94:97]
	v_mfma_f32_16x16x32_bf16 v[82:85], v[106:109], v[222:225], v[82:85]
	v_mfma_f32_16x16x32_bf16 v[66:69], v[98:101], v[234:237], v[66:69]
	v_mfma_f32_16x16x32_bf16 v[62:65], v[106:109], v[234:237], v[62:65]
	v_mfma_f32_16x16x32_bf16 v[42:45], v[98:101], v[238:241], v[42:45]
	v_mfma_f32_16x16x32_bf16 v[38:41], v[106:109], v[238:241], v[38:41]
	v_mfma_f32_16x16x32_bf16 v[74:77], v[168:171], v[210:213], v[74:77]
	v_mfma_f32_16x16x32_bf16 v[98:101], v[172:175], v[218:221], v[74:77]
	v_mfma_f32_16x16x32_bf16 v[74:77], v[168:171], v[214:217], v[78:81]
	v_mfma_f32_16x16x32_bf16 v[70:73], v[176:179], v[210:213], v[70:73]
	v_mfma_f32_16x16x32_bf16 v[90:93], v[172:175], v[222:225], v[74:77]
	v_mfma_f32_16x16x32_bf16 v[74:77], v[176:179], v[214:217], v[86:89]
	v_mfma_f32_16x16x32_bf16 v[54:57], v[168:171], v[226:229], v[54:57]
	v_mfma_f32_16x16x32_bf16 v[50:53], v[176:179], v[226:229], v[50:53]
	v_mfma_f32_16x16x32_bf16 v[6:9], v[168:171], v[230:233], v[6:9]
	v_mfma_f32_16x16x32_bf16 v[2:5], v[176:179], v[230:233], v[2:5]
	v_mfma_f32_16x16x32_bf16 v[70:73], v[180:183], v[218:221], v[70:73]
	v_mfma_f32_16x16x32_bf16 v[86:89], v[180:183], v[222:225], v[74:77]
	v_mfma_f32_16x16x32_bf16 v[54:57], v[172:175], v[234:237], v[54:57]
	v_mfma_f32_16x16x32_bf16 v[50:53], v[180:183], v[234:237], v[50:53]
	v_mfma_f32_16x16x32_bf16 v[6:9], v[172:175], v[238:241], v[6:9]
	v_mfma_f32_16x16x32_bf16 v[2:5], v[180:183], v[238:241], v[2:5]
	s_barrier
	s_add_i32 s45, s45, 2
	s_add_u32 s37, s37, 0x8000
	s_addc_u32 s44, s44, 0
	s_add_u32 s0, s0, 0x100
	s_addc_u32 s1, s1, 0
	s_cmp_gt_u32 s45, 29
	s_cbranch_scc0 .LBB0_1934
	s_and_b64 vcc, exec, s[18:19]
	s_cbranch_vccz .LBB0_1937
	s_barrier

; #define PG8_WAIT_V(n) asm volatile("s_waitcnt vmcnt(" #n ")" ::: "memory")
; #define PG8_WAIT_L(n) asm volatile("s_waitcnt lgkmcnt(" #n ")" ::: "memory")
; #define PG8_BAR __builtin_amdgcn_s_barrier()
;     ...
;         for (int t = 0; t < nt; t += 2) {
;             const bool last = (t == nt - 2);
;             const char* a1 = cA + (size_t)(t + 1) * kstepA;
;             const char* a2 = last ? nA : cA + (size_t)(t + 2) * kstepA; const char* b2 = last ? nB : cB + (size_t)(t + 2) * kstepB;
;             const char* a3 = a2 + kstepA; const char* b3 = b2 + kstepB;
;             unsigned vs[2][2];
;             if constexpr (GATHER) {
;                 if (last && has_next) {
; #pragma unroll
;                     for (int hh = 0; hh < 2; ++hh)
; #pragma unroll
;                         for (int i = 0; i < 2; ++i) voffN[hh][i] = (unsigned)idxl[(ui + 1) * 256 + hh * HALF + sR[i]] * (unsigned)(K * 2) + (unsigned)sC[i] * 2u;
;                 }
; #pragma unroll
;                 for (int hh = 0; hh < 2; ++hh)
; #pragma unroll
;                     for (int i = 0; i < 2; ++i) vs[hh][i] = last ? voffN[hh][i] : voffA[hh][i];
;             } else {
; #pragma unroll
;                 for (int hh = 0; hh < 2; ++hh)
; #pragma unroll
;                     for (int i = 0; i < 2; ++i) vs[hh][i] = voffA[hh][i];
;             }
;             PG8_LDB(B0, 0, 0); PG8_LDB(B1, 0, 1); PG8_SCHED; PG8_LDA(At, 0, 0); PG8_STAGE(PG8_SA(1, 1), a1, voffA[1]);
;             PG8_WAIT_V(8); PG8_WAIT_L(0); PG8_BAR; if (do0) { PG8_MMA(0, 0, At, B0); PG8_MMA(0, 1, At, B1); } PG8_BAR; PG8_SCHED;
;             PG8_LDA(At, 0, 1); PG8_STAGE(PG8_SB(0, 0), b2, voffB); PG8_STAGE(PG8_SB(0, 1), b2 + hstep, voffB); PG8_STAGE(PG8_SA(0, 0), a2, vs[0]);
;             PG8_WAIT_V(8); PG8_WAIT_L(0); PG8_BAR; if (do1) { PG8_MMA(1, 0, At, B0); PG8_MMA(1, 1, At, B1); } PG8_BAR; PG8_SCHED;
;             PG8_LDB(B0, 1, 0); PG8_LDB(B1, 1, 1); PG8_SCHED; PG8_LDA(At, 1, 0); PG8_STAGE(PG8_SA(0, 1), a2, vs[1]);
;             PG8_WAIT_V(8); PG8_WAIT_L(0); PG8_BAR; if (do0) { PG8_MMA(0, 0, At, B0); PG8_MMA(0, 1, At, B1); } PG8_BAR; PG8_SCHED;
;             PG8_LDA(At, 1, 1); PG8_STAGE(PG8_SB(1, 0), b3, voffB); PG8_STAGE(PG8_SB(1, 1), b3 + hstep, voffB); PG8_STAGE(PG8_SA(1, 0), a3, vs[0]);
;             PG8_WAIT_V(8); PG8_WAIT_L(0); PG8_BAR; if (do1) { PG8_MMA(1, 0, At, B0); PG8_MMA(1, 1, At, B1); } PG8_BAR; PG8_SCHED;
.LBB0_2337:
	v_add_u32_e32 v136, s43, v159
	v_add_u32_e32 v145, s43, v160
	ds_read_b128 v[166:169], v136
	ds_read_b128 v[170:173], v145
	v_add_u32_e32 v136, s44, v159
	s_add_u32 s22, s90, s20
	v_add_u32_e32 v145, s44, v160
	ds_read_b128 v[174:177], v136
	ds_read_b128 v[178:181], v145
	v_add_u32_e32 v136, s45, v159
	s_addc_u32 s23, s91, s21
	v_add_u32_e32 v145, s45, v160
	ds_read_b128 v[182:185], v136
	ds_read_b128 v[186:189], v145
	v_add_u32_e32 v136, s46, v159
	s_add_u32 s24, s22, 0x4213700
	v_add_u32_e32 v145, s46, v160
	ds_read_b128 v[190:193], v136
	ds_read_b128 v[194:197], v145
	s_addc_u32 s25, s23, 0
	s_and_b64 s[22:23], s[2:3], exec
	s_cselect_b32 s22, s14, s13
	s_cselect_b32 s27, s83, s25
	s_cselect_b32 s26, s82, s24
	s_cselect_b32 s23, s15, s53
	s_add_u32 s24, s22, 0x4000
	s_addc_u32 s25, s23, 0
	v_cndmask_b32_e64 v136, v152, v146, s[2:3]
	v_cndmask_b32_e64 v232, v153, v147, s[2:3]
	v_cndmask_b32_e64 v145, v148, v164, s[2:3]
	v_cndmask_b32_e64 v149, v150, v165, s[2:3]
	v_lshl_add_u64 v[234:235], v[156:157], 0, s[20:21]
	s_add_i32 m0, s17, 0xc000
	ds_read_b128 v[200:203], v161
	ds_read_b128 v[204:207], v161 offset:2048
	ds_read_b128 v[208:211], v162
	ds_read_b128 v[212:215], v162 offset:2048
	ds_read_b128 v[216:219], v161 offset:4096
	ds_read_b128 v[220:223], v161 offset:6144
	ds_read_b128 v[224:227], v162 offset:4096
	ds_read_b128 v[228:231], v162 offset:6144
	global_load_lds_dwordx4 v[234:235], off
	v_lshl_add_u64 v[234:235], v[154:155], 0, s[20:21]
	s_add_i32 m0, s17, 0xe000
	s_nop 0
	global_load_lds_dwordx4 v[234:235], off
	s_waitcnt vmcnt(8)
	s_waitcnt lgkmcnt(0)
	s_barrier
	s_waitcnt lgkmcnt(0)
	v_mfma_f32_16x16x32_bf16 v[126:129], v[166:169], v[200:203], v[126:129]
	v_mfma_f32_16x16x32_bf16 v[122:125], v[174:177], v[200:203], v[122:125]
	v_mfma_f32_16x16x32_bf16 v[110:113], v[166:169], v[204:207], v[110:113]
	v_mfma_f32_16x16x32_bf16 v[106:109], v[174:177], v[204:207], v[106:109]
	v_mfma_f32_16x16x32_bf16 v[94:97], v[166:169], v[216:219], v[94:97]
	v_mfma_f32_16x16x32_bf16 v[90:93], v[174:177], v[216:219], v[90:93]
	v_mfma_f32_16x16x32_bf16 v[78:81], v[166:169], v[220:223], v[78:81]
	v_mfma_f32_16x16x32_bf16 v[74:77], v[174:177], v[220:223], v[74:77]
	v_mfma_f32_16x16x32_bf16 v[126:129], v[170:173], v[208:211], v[126:129]
	v_mfma_f32_16x16x32_bf16 v[122:125], v[178:181], v[208:211], v[122:125]
	v_mfma_f32_16x16x32_bf16 v[110:113], v[170:173], v[212:215], v[110:113]
	v_mfma_f32_16x16x32_bf16 v[106:109], v[178:181], v[212:215], v[106:109]
	v_mfma_f32_16x16x32_bf16 v[94:97], v[170:173], v[224:227], v[94:97]
	v_mfma_f32_16x16x32_bf16 v[90:93], v[178:181], v[224:227], v[90:93]
	v_mfma_f32_16x16x32_bf16 v[78:81], v[170:173], v[228:231], v[78:81]
	v_mfma_f32_16x16x32_bf16 v[74:77], v[178:181], v[228:231], v[74:77]
	v_mfma_f32_16x16x32_bf16 v[118:121], v[182:185], v[200:203], v[118:121]
	v_mfma_f32_16x16x32_bf16 v[114:117], v[190:193], v[200:203], v[114:117]
	v_mfma_f32_16x16x32_bf16 v[102:105], v[182:185], v[204:207], v[102:105]
	v_mfma_f32_16x16x32_bf16 v[98:101], v[190:193], v[204:207], v[98:101]
	v_mfma_f32_16x16x32_bf16 v[86:89], v[182:185], v[216:219], v[86:89]
	v_mfma_f32_16x16x32_bf16 v[82:85], v[190:193], v[216:219], v[82:85]
	v_mfma_f32_16x16x32_bf16 v[70:73], v[182:185], v[220:223], v[70:73]
	v_mfma_f32_16x16x32_bf16 v[66:69], v[190:193], v[220:223], v[66:69]
	v_mfma_f32_16x16x32_bf16 v[118:121], v[186:189], v[208:211], v[118:121]
	v_mfma_f32_16x16x32_bf16 v[114:117], v[194:197], v[208:211], v[114:117]
	v_mfma_f32_16x16x32_bf16 v[102:105], v[186:189], v[212:215], v[102:105]
	v_mfma_f32_16x16x32_bf16 v[98:101], v[194:197], v[212:215], v[98:101]
	v_mfma_f32_16x16x32_bf16 v[86:89], v[186:189], v[224:227], v[86:89]
	v_mfma_f32_16x16x32_bf16 v[82:85], v[194:197], v[224:227], v[82:85]
	v_mfma_f32_16x16x32_bf16 v[70:73], v[186:189], v[228:231], v[70:73]
	v_mfma_f32_16x16x32_bf16 v[66:69], v[194:197], v[228:231], v[66:69]
	s_barrier
	s_add_i32 s2, s43, s34
	v_lshl_add_u64 v[234:235], s[22:23], 0, v[132:133]
	s_mov_b32 m0, s2
	ds_read_b128 v[200:203], v161 offset:16384
	ds_read_b128 v[204:207], v161 offset:18432
	ds_read_b128 v[208:211], v162 offset:16384
	ds_read_b128 v[212:215], v162 offset:18432
	ds_read_b128 v[216:219], v161 offset:20480
	ds_read_b128 v[220:223], v161 offset:22528
	ds_read_b128 v[224:227], v162 offset:20480
	ds_read_b128 v[228:231], v162 offset:22528
	global_load_lds_dwordx4 v[234:235], off
	s_add_i32 m0, s2, 0x2000
	s_add_u32 s2, s22, 0x40000
	v_lshl_add_u64 v[234:235], s[22:23], 0, v[134:135]
	s_addc_u32 s3, s23, 0
	s_add_i32 s55, s45, s34
	global_load_lds_dwordx4 v[234:235], off
	v_lshl_add_u64 v[234:235], s[2:3], 0, v[132:133]
	s_mov_b32 m0, s55
	v_mov_b32_e32 v233, v137
	global_load_lds_dwordx4 v[234:235], off
	v_lshl_add_u64 v[234:235], s[2:3], 0, v[134:135]
	s_add_i32 m0, s55, 0x2000
	s_nop 0
	global_load_lds_dwordx4 v[234:235], off
	s_mov_b32 m0, s17
	v_lshl_add_u64 v[234:235], s[26:27], 0, v[136:137]
	global_load_lds_dwordx4 v136, s[26:27]
	s_mov_b32 m0, s35
	s_nop 0
	global_load_lds_dwordx4 v232, s[26:27]
	s_waitcnt vmcnt(8)
	s_waitcnt lgkmcnt(0)
	v_lshl_add_u64 v[232:233], s[26:27], 0, v[232:233]
	s_barrier
; #define PG8_STAGE(bufoff, gbase, voff) do { _Pragma("unroll") for (int _i = 0; _i < 2; ++_i) \
;         __builtin_amdgcn_global_load_lds((const unsigned*)((const char*)(gbase) + (voff)[_i]), (LAS unsigned*)(lds + (bufoff) + ldsw + _i * 8192), 16, 0, 0); } while (0)
; #define PG8_LDA(dst, b, h) do { _Pragma("unroll") for (int m = 0; m < 4; ++m) _Pragma("unroll") for (int k = 0; k < 2; ++k) dst[m][k] = *(const LAS bf16x8*)(lds + PG8_SA(b, h) + ((aoff ^ (k * 64)) + m * 2048)); } while (0)
; #define PG8_LDB(dst, b, h) do { _Pragma("unroll") for (int n = 0; n < 2; ++n) _Pragma("unroll") for (int k = 0; k < 2; ++k) dst[n][k] = *(const LAS bf16x8*)(lds + PG8_SB(b, h) + ((boff ^ (k * 64)) + n * 2048)); } while (0)
; #define PG8_MMA(ai, bj, At, Bt) do { __builtin_amdgcn_s_setprio(1); _Pragma("unroll") for (int m = 0; m < 4; ++m) _Pragma("unroll") for (int n = 0; n < 2; ++n) _Pragma("unroll") for (int k = 0; k < 2; ++k) \
;         acc[ai][bj][m][n] = __builtin_amdgcn_mfma_f32_16x16x32_bf16(Bt[n][k], At[m][k], acc[ai][bj][m][n], 0, 0, 0); __builtin_amdgcn_s_setprio(0); } while (0)
; #define PG8_WAIT_V(n) asm volatile("s_waitcnt vmcnt(" #n ")" ::: "memory")
; #define PG8_WAIT_L(n) asm volatile("s_waitcnt lgkmcnt(" #n ")" ::: "memory")
; #define PG8_BAR __builtin_amdgcn_s_barrier()
;     ...
;             PG8_LDB(B0, 0, 0); PG8_LDB(B1, 0, 1); PG8_SCHED; PG8_LDA(At, 0, 0); PG8_STAGE(PG8_SA(1, 1), a1, voffA[1]);
;             PG8_WAIT_V(8); PG8_WAIT_L(0); PG8_BAR; if (do0) { PG8_MMA(0, 0, At, B0); PG8_MMA(0, 1, At, B1); } PG8_BAR; PG8_SCHED;
;             PG8_LDA(At, 0, 1); PG8_STAGE(PG8_SB(0, 0), b2, voffB); PG8_STAGE(PG8_SB(0, 1), b2 + hstep, voffB); PG8_STAGE(PG8_SA(0, 0), a2, vs[0]);
;             PG8_WAIT_V(8); PG8_WAIT_L(0); PG8_BAR; if (do1) { PG8_MMA(1, 0, At, B0); PG8_MMA(1, 1, At, B1); } PG8_BAR; PG8_SCHED;
;             PG8_LDB(B0, 1, 0); PG8_LDB(B1, 1, 1); PG8_SCHED; PG8_LDA(At, 1, 0); PG8_STAGE(PG8_SA(0, 1), a2, vs[1]);
;             PG8_WAIT_V(8); PG8_WAIT_L(0); PG8_BAR; if (do0) { PG8_MMA(0, 0, At, B0); PG8_MMA(0, 1, At, B1); } PG8_BAR; PG8_SCHED;
;             PG8_LDA(At, 1, 1); PG8_STAGE(PG8_SB(1, 0), b3, voffB); PG8_STAGE(PG8_SB(1, 1), b3 + hstep, voffB); PG8_STAGE(PG8_SA(1, 0), a3, vs[0]);
;             PG8_WAIT_V(8); PG8_WAIT_L(0); PG8_BAR; if (do1) { PG8_MMA(1, 0, At, B0); PG8_MMA(1, 1, At, B1); } PG8_BAR; PG8_SCHED;
	s_waitcnt lgkmcnt(0)
	v_mfma_f32_16x16x32_bf16 v[62:65], v[166:169], v[200:203], v[62:65]
	v_mfma_f32_16x16x32_bf16 v[58:61], v[174:177], v[200:203], v[58:61]
	v_mfma_f32_16x16x32_bf16 v[46:49], v[166:169], v[204:207], v[46:49]
	v_mfma_f32_16x16x32_bf16 v[42:45], v[174:177], v[204:207], v[42:45]
	v_mfma_f32_16x16x32_bf16 v[30:33], v[166:169], v[216:219], v[30:33]
	v_mfma_f32_16x16x32_bf16 v[26:29], v[174:177], v[216:219], v[26:29]
	v_mfma_f32_16x16x32_bf16 v[14:17], v[166:169], v[220:223], v[14:17]
	v_mfma_f32_16x16x32_bf16 v[10:13], v[174:177], v[220:223], v[10:13]
	v_mfma_f32_16x16x32_bf16 v[62:65], v[170:173], v[208:211], v[62:65]
	v_mfma_f32_16x16x32_bf16 v[58:61], v[178:181], v[208:211], v[58:61]
	v_mfma_f32_16x16x32_bf16 v[46:49], v[170:173], v[212:215], v[46:49]
	v_mfma_f32_16x16x32_bf16 v[42:45], v[178:181], v[212:215], v[42:45]
	v_mfma_f32_16x16x32_bf16 v[30:33], v[170:173], v[224:227], v[30:33]
	v_mfma_f32_16x16x32_bf16 v[26:29], v[178:181], v[224:227], v[26:29]
	v_mfma_f32_16x16x32_bf16 v[14:17], v[170:173], v[228:231], v[14:17]
	v_mfma_f32_16x16x32_bf16 v[10:13], v[178:181], v[228:231], v[10:13]
	v_mfma_f32_16x16x32_bf16 v[54:57], v[182:185], v[200:203], v[54:57]
	v_mfma_f32_16x16x32_bf16 v[50:53], v[190:193], v[200:203], v[50:53]
	v_mfma_f32_16x16x32_bf16 v[38:41], v[182:185], v[204:207], v[38:41]
	v_mfma_f32_16x16x32_bf16 v[34:37], v[190:193], v[204:207], v[34:37]
	v_mfma_f32_16x16x32_bf16 v[22:25], v[182:185], v[216:219], v[22:25]
	v_mfma_f32_16x16x32_bf16 v[18:21], v[190:193], v[216:219], v[18:21]
	v_mfma_f32_16x16x32_bf16 v[6:9], v[182:185], v[220:223], v[6:9]
	v_mfma_f32_16x16x32_bf16 v[2:5], v[190:193], v[220:223], v[2:5]
	v_mfma_f32_16x16x32_bf16 v[54:57], v[186:189], v[208:211], v[54:57]
	v_mfma_f32_16x16x32_bf16 v[50:53], v[194:197], v[208:211], v[50:53]
	v_mfma_f32_16x16x32_bf16 v[38:41], v[186:189], v[212:215], v[38:41]
	v_mfma_f32_16x16x32_bf16 v[34:37], v[194:197], v[212:215], v[34:37]
	v_mfma_f32_16x16x32_bf16 v[22:25], v[186:189], v[224:227], v[22:25]
	v_mfma_f32_16x16x32_bf16 v[18:21], v[194:197], v[224:227], v[18:21]
	v_mfma_f32_16x16x32_bf16 v[6:9], v[186:189], v[228:231], v[6:9]
	v_mfma_f32_16x16x32_bf16 v[2:5], v[194:197], v[228:231], v[2:5]
	s_barrier
	s_add_i32 s2, 0, 0x18000
	v_add_u32_e32 v136, s2, v159
	v_add_u32_e32 v151, s2, v160
	ds_read_b128 v[166:169], v136
	ds_read_b128 v[170:173], v151
	v_add_u32_e32 v136, s47, v159
	s_add_i32 s55, 0, 0x1c000
	v_add_u32_e32 v151, s47, v160
	ds_read_b128 v[174:177], v136
	ds_read_b128 v[178:181], v151
	v_add_u32_e32 v136, s55, v159
	v_add_u32_e32 v151, s55, v160
	ds_read_b128 v[182:185], v136
	ds_read_b128 v[186:189], v151
	v_add_u32_e32 v136, s48, v159
	v_add_u32_e32 v151, s48, v160
	ds_read_b128 v[190:193], v136
	ds_read_b128 v[194:197], v151
	s_mov_b32 m0, s36
	ds_read_b128 v[200:203], v161 offset:32768
	ds_read_b128 v[204:207], v161 offset:34816
	ds_read_b128 v[208:211], v162 offset:32768
	ds_read_b128 v[212:215], v162 offset:34816
	ds_read_b128 v[216:219], v161 offset:36864
	ds_read_b128 v[220:223], v161 offset:38912
	ds_read_b128 v[224:227], v162 offset:36864
	ds_read_b128 v[228:231], v162 offset:38912
	global_load_lds_dwordx4 v145, s[26:27]
	s_mov_b32 m0, s37
	s_nop 0
	global_load_lds_dwordx4 v149, s[26:27]
	s_waitcnt vmcnt(8)
	s_waitcnt lgkmcnt(0)
	s_barrier
	s_waitcnt lgkmcnt(0)
	v_mfma_f32_16x16x32_bf16 v[126:129], v[166:169], v[200:203], v[126:129]
	v_mfma_f32_16x16x32_bf16 v[122:125], v[174:177], v[200:203], v[122:125]
	v_mfma_f32_16x16x32_bf16 v[110:113], v[166:169], v[204:207], v[110:113]
	v_mfma_f32_16x16x32_bf16 v[106:109], v[174:177], v[204:207], v[106:109]
	v_mfma_f32_16x16x32_bf16 v[94:97], v[166:169], v[216:219], v[94:97]
	v_mfma_f32_16x16x32_bf16 v[90:93], v[174:177], v[216:219], v[90:93]
	v_mfma_f32_16x16x32_bf16 v[78:81], v[166:169], v[220:223], v[78:81]
	v_mfma_f32_16x16x32_bf16 v[74:77], v[174:177], v[220:223], v[74:77]
	v_mfma_f32_16x16x32_bf16 v[126:129], v[170:173], v[208:211], v[126:129]
	v_mfma_f32_16x16x32_bf16 v[122:125], v[178:181], v[208:211], v[122:125]
	v_mfma_f32_16x16x32_bf16 v[110:113], v[170:173], v[212:215], v[110:113]
	v_mfma_f32_16x16x32_bf16 v[106:109], v[178:181], v[212:215], v[106:109]
	v_mfma_f32_16x16x32_bf16 v[94:97], v[170:173], v[224:227], v[94:97]
	v_mfma_f32_16x16x32_bf16 v[90:93], v[178:181], v[224:227], v[90:93]
	v_mfma_f32_16x16x32_bf16 v[78:81], v[170:173], v[228:231], v[78:81]
	v_mfma_f32_16x16x32_bf16 v[74:77], v[178:181], v[228:231], v[74:77]
	v_mfma_f32_16x16x32_bf16 v[118:121], v[182:185], v[200:203], v[118:121]
	v_mfma_f32_16x16x32_bf16 v[114:117], v[190:193], v[200:203], v[114:117]
	v_mfma_f32_16x16x32_bf16 v[102:105], v[182:185], v[204:207], v[102:105]
	v_mfma_f32_16x16x32_bf16 v[98:101], v[190:193], v[204:207], v[98:101]
	v_mfma_f32_16x16x32_bf16 v[86:89], v[182:185], v[216:219], v[86:89]
	v_mfma_f32_16x16x32_bf16 v[82:85], v[190:193], v[216:219], v[82:85]
	v_mfma_f32_16x16x32_bf16 v[70:73], v[182:185], v[220:223], v[70:73]
	v_mfma_f32_16x16x32_bf16 v[66:69], v[190:193], v[220:223], v[66:69]
	v_mfma_f32_16x16x32_bf16 v[118:121], v[186:189], v[208:211], v[118:121]
	v_mfma_f32_16x16x32_bf16 v[114:117], v[194:197], v[208:211], v[114:117]
	v_mfma_f32_16x16x32_bf16 v[102:105], v[186:189], v[212:215], v[102:105]
	v_mfma_f32_16x16x32_bf16 v[98:101], v[194:197], v[212:215], v[98:101]
	v_mfma_f32_16x16x32_bf16 v[86:89], v[186:189], v[224:227], v[86:89]
	v_mfma_f32_16x16x32_bf16 v[82:85], v[194:197], v[224:227], v[82:85]
	v_mfma_f32_16x16x32_bf16 v[70:73], v[186:189], v[228:231], v[70:73]
	v_mfma_f32_16x16x32_bf16 v[66:69], v[194:197], v[228:231], v[66:69]
	s_barrier
; #define PG8_STAGE(bufoff, gbase, voff) do { _Pragma("unroll") for (int _i = 0; _i < 2; ++_i) \
;         __builtin_amdgcn_global_load_lds((const unsigned*)((const char*)(gbase) + (voff)[_i]), (LAS unsigned*)(lds + (bufoff) + ldsw + _i * 8192), 16, 0, 0); } while (0)
; #define PG8_LDA(dst, b, h) do { _Pragma("unroll") for (int m = 0; m < 4; ++m) _Pragma("unroll") for (int k = 0; k < 2; ++k) dst[m][k] = *(const LAS bf16x8*)(lds + PG8_SA(b, h) + ((aoff ^ (k * 64)) + m * 2048)); } while (0)
; #define PG8_MMA(ai, bj, At, Bt) do { __builtin_amdgcn_s_setprio(1); _Pragma("unroll") for (int m = 0; m < 4; ++m) _Pragma("unroll") for (int n = 0; n < 2; ++n) _Pragma("unroll") for (int k = 0; k < 2; ++k) \
;         acc[ai][bj][m][n] = __builtin_amdgcn_mfma_f32_16x16x32_bf16(Bt[n][k], At[m][k], acc[ai][bj][m][n], 0, 0, 0); __builtin_amdgcn_s_setprio(0); } while (0)
; #define PG8_WAIT_V(n) asm volatile("s_waitcnt vmcnt(" #n ")" ::: "memory")
; #define PG8_WAIT_L(n) asm volatile("s_waitcnt lgkmcnt(" #n ")" ::: "memory")
; #define PG8_BAR __builtin_amdgcn_s_barrier()
; #define PG8_SCHED __builtin_amdgcn_sched_barrier(0)
;     ...
;             PG8_LDA(At, 1, 1); PG8_STAGE(PG8_SB(1, 0), b3, voffB); PG8_STAGE(PG8_SB(1, 1), b3 + hstep, voffB); PG8_STAGE(PG8_SA(1, 0), a3, vs[0]);
;             PG8_WAIT_V(8); PG8_WAIT_L(0); PG8_BAR; if (do1) { PG8_MMA(1, 0, At, B0); PG8_MMA(1, 1, At, B1); } PG8_BAR; PG8_SCHED;
;         }
	s_add_i32 s2, s2, s34
	v_lshl_add_u64 v[236:237], s[24:25], 0, v[132:133]
	s_mov_b32 m0, s2
	ds_read_b128 v[200:203], v161 offset:49152
	ds_read_b128 v[204:207], v161 offset:51200
	ds_read_b128 v[208:211], v162 offset:49152
	ds_read_b128 v[212:215], v162 offset:51200
	ds_read_b128 v[216:219], v161 offset:53248
	ds_read_b128 v[220:223], v161 offset:55296
	ds_read_b128 v[224:227], v162 offset:53248
	ds_read_b128 v[228:231], v162 offset:55296
	global_load_lds_dwordx4 v[236:237], off
	s_add_i32 m0, s2, 0x2000
	s_add_u32 s2, s22, 0x44000
	v_lshl_add_u64 v[236:237], s[24:25], 0, v[134:135]
	s_addc_u32 s3, s23, 0
	s_add_i32 s22, s55, s34
	global_load_lds_dwordx4 v[236:237], off
	v_lshl_add_u64 v[236:237], s[2:3], 0, v[132:133]
	s_mov_b32 m0, s22
	v_lshl_add_u64 v[234:235], v[234:235], 0, s[10:11]
	global_load_lds_dwordx4 v[236:237], off
	v_lshl_add_u64 v[236:237], s[2:3], 0, v[134:135]
	s_add_i32 m0, s22, 0x2000
	v_lshl_add_u64 v[232:233], v[232:233], 0, s[10:11]
	global_load_lds_dwordx4 v[236:237], off
	s_mov_b32 m0, s41
	s_nop 0
	global_load_lds_dwordx4 v[234:235], off
	s_mov_b32 m0, s42
	s_nop 0
	global_load_lds_dwordx4 v[232:233], off
	s_waitcnt vmcnt(8)
	s_waitcnt lgkmcnt(0)
	s_barrier
	s_waitcnt lgkmcnt(0)
	v_mfma_f32_16x16x32_bf16 v[62:65], v[166:169], v[200:203], v[62:65]
	v_mfma_f32_16x16x32_bf16 v[58:61], v[174:177], v[200:203], v[58:61]
	v_mfma_f32_16x16x32_bf16 v[46:49], v[166:169], v[204:207], v[46:49]
	v_mfma_f32_16x16x32_bf16 v[42:45], v[174:177], v[204:207], v[42:45]
	v_mfma_f32_16x16x32_bf16 v[30:33], v[166:169], v[216:219], v[30:33]
	v_mfma_f32_16x16x32_bf16 v[26:29], v[174:177], v[216:219], v[26:29]
	v_mfma_f32_16x16x32_bf16 v[14:17], v[166:169], v[220:223], v[14:17]
	v_mfma_f32_16x16x32_bf16 v[10:13], v[174:177], v[220:223], v[10:13]
	v_mfma_f32_16x16x32_bf16 v[62:65], v[170:173], v[208:211], v[62:65]
	v_mfma_f32_16x16x32_bf16 v[58:61], v[178:181], v[208:211], v[58:61]
	v_mfma_f32_16x16x32_bf16 v[46:49], v[170:173], v[212:215], v[46:49]
	v_mfma_f32_16x16x32_bf16 v[42:45], v[178:181], v[212:215], v[42:45]
	v_mfma_f32_16x16x32_bf16 v[30:33], v[170:173], v[224:227], v[30:33]
	v_mfma_f32_16x16x32_bf16 v[26:29], v[178:181], v[224:227], v[26:29]
	v_mfma_f32_16x16x32_bf16 v[14:17], v[170:173], v[228:231], v[14:17]
	v_mfma_f32_16x16x32_bf16 v[10:13], v[178:181], v[228:231], v[10:13]
	v_mfma_f32_16x16x32_bf16 v[54:57], v[182:185], v[200:203], v[54:57]
	v_mfma_f32_16x16x32_bf16 v[50:53], v[190:193], v[200:203], v[50:53]
	v_mfma_f32_16x16x32_bf16 v[38:41], v[182:185], v[204:207], v[38:41]
	v_mfma_f32_16x16x32_bf16 v[34:37], v[190:193], v[204:207], v[34:37]
	v_mfma_f32_16x16x32_bf16 v[22:25], v[182:185], v[216:219], v[22:25]
	v_mfma_f32_16x16x32_bf16 v[18:21], v[190:193], v[216:219], v[18:21]
	v_mfma_f32_16x16x32_bf16 v[6:9], v[182:185], v[220:223], v[6:9]
	v_mfma_f32_16x16x32_bf16 v[2:5], v[190:193], v[220:223], v[2:5]
	v_mfma_f32_16x16x32_bf16 v[54:57], v[186:189], v[208:211], v[54:57]
	v_mfma_f32_16x16x32_bf16 v[50:53], v[194:197], v[208:211], v[50:53]
	v_mfma_f32_16x16x32_bf16 v[38:41], v[186:189], v[212:215], v[38:41]
	v_mfma_f32_16x16x32_bf16 v[34:37], v[194:197], v[212:215], v[34:37]
	v_mfma_f32_16x16x32_bf16 v[22:25], v[186:189], v[224:227], v[22:25]
	v_mfma_f32_16x16x32_bf16 v[18:21], v[194:197], v[224:227], v[18:21]
	v_mfma_f32_16x16x32_bf16 v[6:9], v[186:189], v[228:231], v[6:9]
	v_mfma_f32_16x16x32_bf16 v[2:5], v[194:197], v[228:231], v[2:5]
	s_barrier
	s_add_i32 s54, s54, 2
	s_add_u32 s13, s13, 0x8000
	s_addc_u32 s53, s53, 0
	s_add_u32 s20, s20, 0x100
	s_addc_u32 s21, s21, 0
	s_cmp_gt_u32 s54, 13
	s_cbranch_scc1 .LBB0_2340

; #define PG8_WAIT_V(n) asm volatile("s_waitcnt vmcnt(" #n ")" ::: "memory")
; #define PG8_WAIT_L(n) asm volatile("s_waitcnt lgkmcnt(" #n ")" ::: "memory")
; #define PG8_BAR __builtin_amdgcn_s_barrier()
;     ...
;         for (int t = 0; t < nt; t += 2) {
;             const bool last = (t == nt - 2);
;             const char* a1 = cA + (size_t)(t + 1) * kstepA;
;             const char* a2 = last ? nA : cA + (size_t)(t + 2) * kstepA; const char* b2 = last ? nB : cB + (size_t)(t + 2) * kstepB;
;             const char* a3 = a2 + kstepA; const char* b3 = b2 + kstepB;
;             unsigned vs[2][2];
;             if constexpr (GATHER) {
;                 if (last && has_next) {
; #pragma unroll
;                     for (int hh = 0; hh < 2; ++hh)
; #pragma unroll
;                         for (int i = 0; i < 2; ++i) voffN[hh][i] = (unsigned)idxl[(ui + 1) * 256 + hh * HALF + sR[i]] * (unsigned)(K * 2) + (unsigned)sC[i] * 2u;
;                 }
; #pragma unroll
;                 for (int hh = 0; hh < 2; ++hh)
; #pragma unroll
;                     for (int i = 0; i < 2; ++i) vs[hh][i] = last ? voffN[hh][i] : voffA[hh][i];
;             } else {
; #pragma unroll
;                 for (int hh = 0; hh < 2; ++hh)
; #pragma unroll
;                     for (int i = 0; i < 2; ++i) vs[hh][i] = voffA[hh][i];
;             }
;             PG8_LDB(B0, 0, 0); PG8_LDB(B1, 0, 1); PG8_SCHED; PG8_LDA(At, 0, 0); PG8_STAGE(PG8_SA(1, 1), a1, voffA[1]);
;             PG8_WAIT_V(8); PG8_WAIT_L(0); PG8_BAR; if (do0) { PG8_MMA(0, 0, At, B0); PG8_MMA(0, 1, At, B1); } PG8_BAR; PG8_SCHED;
;             PG8_LDA(At, 0, 1); PG8_STAGE(PG8_SB(0, 0), b2, voffB); PG8_STAGE(PG8_SB(0, 1), b2 + hstep, voffB); PG8_STAGE(PG8_SA(0, 0), a2, vs[0]);
;             PG8_WAIT_V(8); PG8_WAIT_L(0); PG8_BAR; if (do1) { PG8_MMA(1, 0, At, B0); PG8_MMA(1, 1, At, B1); } PG8_BAR; PG8_SCHED;
;             PG8_LDB(B0, 1, 0); PG8_LDB(B1, 1, 1); PG8_SCHED; PG8_LDA(At, 1, 0); PG8_STAGE(PG8_SA(0, 1), a2, vs[1]);
;             PG8_WAIT_V(8); PG8_WAIT_L(0); PG8_BAR; if (do0) { PG8_MMA(0, 0, At, B0); PG8_MMA(0, 1, At, B1); } PG8_BAR; PG8_SCHED;
;             PG8_LDA(At, 1, 1); PG8_STAGE(PG8_SB(1, 0), b3, voffB); PG8_STAGE(PG8_SB(1, 1), b3 + hstep, voffB); PG8_STAGE(PG8_SA(1, 0), a3, vs[0]);
;             PG8_WAIT_V(8); PG8_WAIT_L(0); PG8_BAR; if (do1) { PG8_MMA(1, 0, At, B0); PG8_MMA(1, 1, At, B1); } PG8_BAR; PG8_SCHED;
.LBB0_2411:
	ds_read_b128 v[146:149], v153
	ds_read_b128 v[168:171], v154
	ds_read_b128 v[172:175], v155
	ds_read_b128 v[176:179], v156
	ds_read_b128 v[180:183], v157
	ds_read_b128 v[184:187], v158
	ds_read_b128 v[188:191], v159
	ds_read_b128 v[192:195], v160
	s_add_u32 s20, s18, 0x4000
	s_addc_u32 s21, s19, 0
	s_cmp_eq_u32 s56, 40
	s_cselect_b32 s26, s14, s20
	s_cselect_b32 s27, s15, s21
	s_cselect_b32 s22, s16, s54
	s_cselect_b32 s23, s17, s55
	s_add_u32 s20, s26, 0x4000
	s_addc_u32 s21, s27, 0
	v_lshl_add_u64 v[196:197], s[18:19], 0, v[142:143]
	s_add_i32 m0, s34, 0xc000
	ds_read_b128 v[200:203], v161
	ds_read_b128 v[204:207], v161 offset:2048
	ds_read_b128 v[208:211], v162
	ds_read_b128 v[212:215], v162 offset:2048
	ds_read_b128 v[216:219], v161 offset:4096
	ds_read_b128 v[220:223], v161 offset:6144
	ds_read_b128 v[224:227], v162 offset:4096
	ds_read_b128 v[228:231], v162 offset:6144
	global_load_lds_dwordx4 v[196:197], off
	v_lshl_add_u64 v[196:197], s[18:19], 0, v[144:145]
	s_add_i32 m0, s34, 0xe000
	s_add_u32 s24, s22, 0x4000
	global_load_lds_dwordx4 v[196:197], off
	s_waitcnt vmcnt(8)
	s_waitcnt lgkmcnt(0)
	s_addc_u32 s25, s23, 0
	s_barrier
	s_waitcnt lgkmcnt(0)
	v_mfma_f32_16x16x32_bf16 v[126:129], v[146:149], v[200:203], v[126:129]
	v_mfma_f32_16x16x32_bf16 v[122:125], v[172:175], v[200:203], v[122:125]
	v_mfma_f32_16x16x32_bf16 v[114:117], v[146:149], v[204:207], v[114:117]
	v_mfma_f32_16x16x32_bf16 v[106:109], v[172:175], v[204:207], v[106:109]
	v_mfma_f32_16x16x32_bf16 v[98:101], v[146:149], v[216:219], v[98:101]
	v_mfma_f32_16x16x32_bf16 v[90:93], v[172:175], v[216:219], v[90:93]
	v_mfma_f32_16x16x32_bf16 v[82:85], v[146:149], v[220:223], v[82:85]
	v_mfma_f32_16x16x32_bf16 v[74:77], v[172:175], v[220:223], v[74:77]
	v_mfma_f32_16x16x32_bf16 v[126:129], v[168:171], v[208:211], v[126:129]
	v_mfma_f32_16x16x32_bf16 v[122:125], v[176:179], v[208:211], v[122:125]
	v_mfma_f32_16x16x32_bf16 v[114:117], v[168:171], v[212:215], v[114:117]
	v_mfma_f32_16x16x32_bf16 v[106:109], v[176:179], v[212:215], v[106:109]
	v_mfma_f32_16x16x32_bf16 v[98:101], v[168:171], v[224:227], v[98:101]
	v_mfma_f32_16x16x32_bf16 v[90:93], v[176:179], v[224:227], v[90:93]
	v_mfma_f32_16x16x32_bf16 v[82:85], v[168:171], v[228:231], v[82:85]
	v_mfma_f32_16x16x32_bf16 v[74:77], v[176:179], v[228:231], v[74:77]
	v_mfma_f32_16x16x32_bf16 v[118:121], v[180:183], v[200:203], v[118:121]
	v_mfma_f32_16x16x32_bf16 v[110:113], v[188:191], v[200:203], v[110:113]
	v_mfma_f32_16x16x32_bf16 v[102:105], v[180:183], v[204:207], v[102:105]
	v_mfma_f32_16x16x32_bf16 v[94:97], v[188:191], v[204:207], v[94:97]
	v_mfma_f32_16x16x32_bf16 v[86:89], v[180:183], v[216:219], v[86:89]
	v_mfma_f32_16x16x32_bf16 v[78:81], v[188:191], v[216:219], v[78:81]
	v_mfma_f32_16x16x32_bf16 v[70:73], v[180:183], v[220:223], v[70:73]
	v_mfma_f32_16x16x32_bf16 v[66:69], v[188:191], v[220:223], v[66:69]
	v_mfma_f32_16x16x32_bf16 v[118:121], v[184:187], v[208:211], v[118:121]
	v_mfma_f32_16x16x32_bf16 v[110:113], v[192:195], v[208:211], v[110:113]
	v_mfma_f32_16x16x32_bf16 v[102:105], v[184:187], v[212:215], v[102:105]
	v_mfma_f32_16x16x32_bf16 v[94:97], v[192:195], v[212:215], v[94:97]
	v_mfma_f32_16x16x32_bf16 v[86:89], v[184:187], v[224:227], v[86:89]
	v_mfma_f32_16x16x32_bf16 v[78:81], v[192:195], v[224:227], v[78:81]
	v_mfma_f32_16x16x32_bf16 v[70:73], v[184:187], v[228:231], v[70:73]
	v_mfma_f32_16x16x32_bf16 v[66:69], v[192:195], v[228:231], v[66:69]
	s_barrier
	s_add_i32 s57, s42, s30
	v_lshl_add_u64 v[196:197], s[22:23], 0, v[132:133]
	s_mov_b32 m0, s57
	ds_read_b128 v[200:203], v161 offset:16384
	ds_read_b128 v[204:207], v161 offset:18432
	ds_read_b128 v[208:211], v162 offset:16384
	ds_read_b128 v[212:215], v162 offset:18432
	ds_read_b128 v[216:219], v161 offset:20480
	ds_read_b128 v[220:223], v161 offset:22528
	ds_read_b128 v[224:227], v162 offset:20480
	ds_read_b128 v[228:231], v162 offset:22528
	global_load_lds_dwordx4 v[196:197], off
	s_add_i32 m0, s57, 0x2000
	s_add_u32 s58, s22, 0xb0000
	v_lshl_add_u64 v[196:197], s[22:23], 0, v[130:131]
	s_addc_u32 s59, s23, 0
	s_add_i32 s57, s43, s30
	global_load_lds_dwordx4 v[196:197], off
	v_lshl_add_u64 v[196:197], s[58:59], 0, v[132:133]
	s_mov_b32 m0, s57
	s_nop 0
	global_load_lds_dwordx4 v[196:197], off
	v_lshl_add_u64 v[196:197], s[58:59], 0, v[130:131]
	s_add_i32 m0, s57, 0x2000
	s_nop 0
	global_load_lds_dwordx4 v[196:197], off
	v_lshl_add_u64 v[196:197], s[26:27], 0, v[134:135]
	s_mov_b32 m0, s34
	s_nop 0
	global_load_lds_dwordx4 v[196:197], off
	v_lshl_add_u64 v[196:197], s[26:27], 0, v[136:137]
	s_mov_b32 m0, s35
	s_nop 0
	global_load_lds_dwordx4 v[196:197], off
	s_waitcnt vmcnt(8)
	s_waitcnt lgkmcnt(0)
	s_barrier
; #define PG8_STAGE(bufoff, gbase, voff) do { _Pragma("unroll") for (int _i = 0; _i < 2; ++_i) \
;         __builtin_amdgcn_global_load_lds((const unsigned*)((const char*)(gbase) + (voff)[_i]), (LAS unsigned*)(lds + (bufoff) + ldsw + _i * 8192), 16, 0, 0); } while (0)
; #define PG8_LDA(dst, b, h) do { _Pragma("unroll") for (int m = 0; m < 4; ++m) _Pragma("unroll") for (int k = 0; k < 2; ++k) dst[m][k] = *(const LAS bf16x8*)(lds + PG8_SA(b, h) + ((aoff ^ (k * 64)) + m * 2048)); } while (0)
; #define PG8_LDB(dst, b, h) do { _Pragma("unroll") for (int n = 0; n < 2; ++n) _Pragma("unroll") for (int k = 0; k < 2; ++k) dst[n][k] = *(const LAS bf16x8*)(lds + PG8_SB(b, h) + ((boff ^ (k * 64)) + n * 2048)); } while (0)
; #define PG8_MMA(ai, bj, At, Bt) do { __builtin_amdgcn_s_setprio(1); _Pragma("unroll") for (int m = 0; m < 4; ++m) _Pragma("unroll") for (int n = 0; n < 2; ++n) _Pragma("unroll") for (int k = 0; k < 2; ++k) \
;         acc[ai][bj][m][n] = __builtin_amdgcn_mfma_f32_16x16x32_bf16(Bt[n][k], At[m][k], acc[ai][bj][m][n], 0, 0, 0); __builtin_amdgcn_s_setprio(0); } while (0)
; #define PG8_WAIT_V(n) asm volatile("s_waitcnt vmcnt(" #n ")" ::: "memory")
; #define PG8_WAIT_L(n) asm volatile("s_waitcnt lgkmcnt(" #n ")" ::: "memory")
; #define PG8_BAR __builtin_amdgcn_s_barrier()
;     ...
;             PG8_LDB(B0, 0, 0); PG8_LDB(B1, 0, 1); PG8_SCHED; PG8_LDA(At, 0, 0); PG8_STAGE(PG8_SA(1, 1), a1, voffA[1]);
;             PG8_WAIT_V(8); PG8_WAIT_L(0); PG8_BAR; if (do0) { PG8_MMA(0, 0, At, B0); PG8_MMA(0, 1, At, B1); } PG8_BAR; PG8_SCHED;
;             PG8_LDA(At, 0, 1); PG8_STAGE(PG8_SB(0, 0), b2, voffB); PG8_STAGE(PG8_SB(0, 1), b2 + hstep, voffB); PG8_STAGE(PG8_SA(0, 0), a2, vs[0]);
;             PG8_WAIT_V(8); PG8_WAIT_L(0); PG8_BAR; if (do1) { PG8_MMA(1, 0, At, B0); PG8_MMA(1, 1, At, B1); } PG8_BAR; PG8_SCHED;
;             PG8_LDB(B0, 1, 0); PG8_LDB(B1, 1, 1); PG8_SCHED; PG8_LDA(At, 1, 0); PG8_STAGE(PG8_SA(0, 1), a2, vs[1]);
;             PG8_WAIT_V(8); PG8_WAIT_L(0); PG8_BAR; if (do0) { PG8_MMA(0, 0, At, B0); PG8_MMA(0, 1, At, B1); } PG8_BAR; PG8_SCHED;
;             PG8_LDA(At, 1, 1); PG8_STAGE(PG8_SB(1, 0), b3, voffB); PG8_STAGE(PG8_SB(1, 1), b3 + hstep, voffB); PG8_STAGE(PG8_SA(1, 0), a3, vs[0]);
;             PG8_WAIT_V(8); PG8_WAIT_L(0); PG8_BAR; if (do1) { PG8_MMA(1, 0, At, B0); PG8_MMA(1, 1, At, B1); } PG8_BAR; PG8_SCHED;
	s_waitcnt lgkmcnt(0)
	v_mfma_f32_16x16x32_bf16 v[62:65], v[146:149], v[200:203], v[62:65]
	v_mfma_f32_16x16x32_bf16 v[58:61], v[172:175], v[200:203], v[58:61]
	v_mfma_f32_16x16x32_bf16 v[46:49], v[146:149], v[204:207], v[46:49]
	v_mfma_f32_16x16x32_bf16 v[42:45], v[172:175], v[204:207], v[42:45]
	v_mfma_f32_16x16x32_bf16 v[30:33], v[146:149], v[216:219], v[30:33]
	v_mfma_f32_16x16x32_bf16 v[26:29], v[172:175], v[216:219], v[26:29]
	v_mfma_f32_16x16x32_bf16 v[14:17], v[146:149], v[220:223], v[14:17]
	v_mfma_f32_16x16x32_bf16 v[10:13], v[172:175], v[220:223], v[10:13]
	v_mfma_f32_16x16x32_bf16 v[62:65], v[168:171], v[208:211], v[62:65]
	v_mfma_f32_16x16x32_bf16 v[58:61], v[176:179], v[208:211], v[58:61]
	v_mfma_f32_16x16x32_bf16 v[46:49], v[168:171], v[212:215], v[46:49]
	v_mfma_f32_16x16x32_bf16 v[42:45], v[176:179], v[212:215], v[42:45]
	v_mfma_f32_16x16x32_bf16 v[30:33], v[168:171], v[224:227], v[30:33]
	v_mfma_f32_16x16x32_bf16 v[26:29], v[176:179], v[224:227], v[26:29]
	v_mfma_f32_16x16x32_bf16 v[14:17], v[168:171], v[228:231], v[14:17]
	v_mfma_f32_16x16x32_bf16 v[10:13], v[176:179], v[228:231], v[10:13]
	v_mfma_f32_16x16x32_bf16 v[54:57], v[180:183], v[200:203], v[54:57]
	v_mfma_f32_16x16x32_bf16 v[50:53], v[188:191], v[200:203], v[50:53]
	v_mfma_f32_16x16x32_bf16 v[38:41], v[180:183], v[204:207], v[38:41]
	v_mfma_f32_16x16x32_bf16 v[34:37], v[188:191], v[204:207], v[34:37]
	v_mfma_f32_16x16x32_bf16 v[22:25], v[180:183], v[216:219], v[22:25]
	v_mfma_f32_16x16x32_bf16 v[18:21], v[188:191], v[216:219], v[18:21]
	v_mfma_f32_16x16x32_bf16 v[6:9], v[180:183], v[220:223], v[6:9]
	v_mfma_f32_16x16x32_bf16 v[2:5], v[188:191], v[220:223], v[2:5]
	v_mfma_f32_16x16x32_bf16 v[54:57], v[184:187], v[208:211], v[54:57]
	v_mfma_f32_16x16x32_bf16 v[50:53], v[192:195], v[208:211], v[50:53]
	v_mfma_f32_16x16x32_bf16 v[38:41], v[184:187], v[212:215], v[38:41]
	v_mfma_f32_16x16x32_bf16 v[34:37], v[192:195], v[212:215], v[34:37]
	v_mfma_f32_16x16x32_bf16 v[22:25], v[184:187], v[224:227], v[22:25]
	v_mfma_f32_16x16x32_bf16 v[18:21], v[192:195], v[224:227], v[18:21]
	v_mfma_f32_16x16x32_bf16 v[6:9], v[184:187], v[228:231], v[6:9]
	v_mfma_f32_16x16x32_bf16 v[2:5], v[192:195], v[228:231], v[2:5]
	s_barrier
	s_add_i32 s57, 0, 0x18000
	v_add_u32_e32 v146, s57, v150
	v_add_u32_e32 v167, s57, v151
	s_add_i32 s58, 0, 0x1c000
	ds_read_b128 v[146:149], v146
	ds_read_b128 v[168:171], v167
	ds_read_b128 v[172:175], v163
	ds_read_b128 v[176:179], v164
	v_add_u32_e32 v167, s58, v150
	v_add_u32_e32 v184, s58, v151
	ds_read_b128 v[180:183], v167
	ds_read_b128 v[184:187], v184
	ds_read_b128 v[188:191], v165
	ds_read_b128 v[192:195], v166
	s_mov_b32 m0, s36
	v_lshl_add_u64 v[196:197], s[26:27], 0, v[138:139]
	ds_read_b128 v[200:203], v161 offset:32768
	ds_read_b128 v[204:207], v161 offset:34816
	ds_read_b128 v[208:211], v162 offset:32768
	ds_read_b128 v[212:215], v162 offset:34816
	ds_read_b128 v[216:219], v161 offset:36864
	ds_read_b128 v[220:223], v161 offset:38912
	ds_read_b128 v[224:227], v162 offset:36864
	ds_read_b128 v[228:231], v162 offset:38912
	global_load_lds_dwordx4 v[196:197], off
	v_lshl_add_u64 v[196:197], s[26:27], 0, v[140:141]
	s_mov_b32 m0, s37
	s_nop 0
	global_load_lds_dwordx4 v[196:197], off
	s_waitcnt vmcnt(8)
	s_waitcnt lgkmcnt(0)
	s_barrier
	s_waitcnt lgkmcnt(0)
	v_mfma_f32_16x16x32_bf16 v[126:129], v[146:149], v[200:203], v[126:129]
	v_mfma_f32_16x16x32_bf16 v[122:125], v[172:175], v[200:203], v[122:125]
	v_mfma_f32_16x16x32_bf16 v[114:117], v[146:149], v[204:207], v[114:117]
	v_mfma_f32_16x16x32_bf16 v[106:109], v[172:175], v[204:207], v[106:109]
	v_mfma_f32_16x16x32_bf16 v[98:101], v[146:149], v[216:219], v[98:101]
	v_mfma_f32_16x16x32_bf16 v[90:93], v[172:175], v[216:219], v[90:93]
	v_mfma_f32_16x16x32_bf16 v[82:85], v[146:149], v[220:223], v[82:85]
	v_mfma_f32_16x16x32_bf16 v[74:77], v[172:175], v[220:223], v[74:77]
	v_mfma_f32_16x16x32_bf16 v[126:129], v[168:171], v[208:211], v[126:129]
	v_mfma_f32_16x16x32_bf16 v[122:125], v[176:179], v[208:211], v[122:125]
	v_mfma_f32_16x16x32_bf16 v[114:117], v[168:171], v[212:215], v[114:117]
	v_mfma_f32_16x16x32_bf16 v[106:109], v[176:179], v[212:215], v[106:109]
	v_mfma_f32_16x16x32_bf16 v[98:101], v[168:171], v[224:227], v[98:101]
	v_mfma_f32_16x16x32_bf16 v[90:93], v[176:179], v[224:227], v[90:93]
	v_mfma_f32_16x16x32_bf16 v[82:85], v[168:171], v[228:231], v[82:85]
	v_mfma_f32_16x16x32_bf16 v[74:77], v[176:179], v[228:231], v[74:77]
	v_mfma_f32_16x16x32_bf16 v[118:121], v[180:183], v[200:203], v[118:121]
	v_mfma_f32_16x16x32_bf16 v[110:113], v[188:191], v[200:203], v[110:113]
	v_mfma_f32_16x16x32_bf16 v[102:105], v[180:183], v[204:207], v[102:105]
	v_mfma_f32_16x16x32_bf16 v[94:97], v[188:191], v[204:207], v[94:97]
	v_mfma_f32_16x16x32_bf16 v[86:89], v[180:183], v[216:219], v[86:89]
	v_mfma_f32_16x16x32_bf16 v[78:81], v[188:191], v[216:219], v[78:81]
	v_mfma_f32_16x16x32_bf16 v[70:73], v[180:183], v[220:223], v[70:73]
	v_mfma_f32_16x16x32_bf16 v[66:69], v[188:191], v[220:223], v[66:69]
	v_mfma_f32_16x16x32_bf16 v[118:121], v[184:187], v[208:211], v[118:121]
	v_mfma_f32_16x16x32_bf16 v[110:113], v[192:195], v[208:211], v[110:113]
	v_mfma_f32_16x16x32_bf16 v[102:105], v[184:187], v[212:215], v[102:105]
	v_mfma_f32_16x16x32_bf16 v[94:97], v[192:195], v[212:215], v[94:97]
	v_mfma_f32_16x16x32_bf16 v[86:89], v[184:187], v[224:227], v[86:89]
	v_mfma_f32_16x16x32_bf16 v[78:81], v[192:195], v[224:227], v[78:81]
	v_mfma_f32_16x16x32_bf16 v[70:73], v[184:187], v[228:231], v[70:73]
	v_mfma_f32_16x16x32_bf16 v[66:69], v[192:195], v[228:231], v[66:69]
	s_barrier
; #define PG8_STAGE(bufoff, gbase, voff) do { _Pragma("unroll") for (int _i = 0; _i < 2; ++_i) \
;         __builtin_amdgcn_global_load_lds((const unsigned*)((const char*)(gbase) + (voff)[_i]), (LAS unsigned*)(lds + (bufoff) + ldsw + _i * 8192), 16, 0, 0); } while (0)
; #define PG8_LDA(dst, b, h) do { _Pragma("unroll") for (int m = 0; m < 4; ++m) _Pragma("unroll") for (int k = 0; k < 2; ++k) dst[m][k] = *(const LAS bf16x8*)(lds + PG8_SA(b, h) + ((aoff ^ (k * 64)) + m * 2048)); } while (0)
; #define PG8_MMA(ai, bj, At, Bt) do { __builtin_amdgcn_s_setprio(1); _Pragma("unroll") for (int m = 0; m < 4; ++m) _Pragma("unroll") for (int n = 0; n < 2; ++n) _Pragma("unroll") for (int k = 0; k < 2; ++k) \
;         acc[ai][bj][m][n] = __builtin_amdgcn_mfma_f32_16x16x32_bf16(Bt[n][k], At[m][k], acc[ai][bj][m][n], 0, 0, 0); __builtin_amdgcn_s_setprio(0); } while (0)
; #define PG8_WAIT_V(n) asm volatile("s_waitcnt vmcnt(" #n ")" ::: "memory")
; #define PG8_WAIT_L(n) asm volatile("s_waitcnt lgkmcnt(" #n ")" ::: "memory")
; #define PG8_BAR __builtin_amdgcn_s_barrier()
; #define PG8_SCHED __builtin_amdgcn_sched_barrier(0)
;     ...
;             PG8_LDA(At, 1, 1); PG8_STAGE(PG8_SB(1, 0), b3, voffB); PG8_STAGE(PG8_SB(1, 1), b3 + hstep, voffB); PG8_STAGE(PG8_SA(1, 0), a3, vs[0]);
;             PG8_WAIT_V(8); PG8_WAIT_L(0); PG8_BAR; if (do1) { PG8_MMA(1, 0, At, B0); PG8_MMA(1, 1, At, B1); } PG8_BAR; PG8_SCHED;
;         }
	s_add_i32 s26, s57, s30
	v_lshl_add_u64 v[196:197], s[24:25], 0, v[132:133]
	s_mov_b32 m0, s26
	ds_read_b128 v[200:203], v161 offset:49152
	ds_read_b128 v[204:207], v161 offset:51200
	ds_read_b128 v[208:211], v162 offset:49152
	ds_read_b128 v[212:215], v162 offset:51200
	ds_read_b128 v[216:219], v161 offset:53248
	ds_read_b128 v[220:223], v161 offset:55296
	ds_read_b128 v[224:227], v162 offset:53248
	ds_read_b128 v[228:231], v162 offset:55296
	global_load_lds_dwordx4 v[196:197], off
	s_add_i32 m0, s26, 0x2000
	s_add_u32 s22, s22, 0xb4000
	v_lshl_add_u64 v[196:197], s[24:25], 0, v[130:131]
	s_addc_u32 s23, s23, 0
	s_add_i32 s24, s58, s30
	global_load_lds_dwordx4 v[196:197], off
	v_lshl_add_u64 v[196:197], s[22:23], 0, v[132:133]
	s_mov_b32 m0, s24
	s_nop 0
	global_load_lds_dwordx4 v[196:197], off
	v_lshl_add_u64 v[196:197], s[22:23], 0, v[130:131]
	s_add_i32 m0, s24, 0x2000
	s_nop 0
	global_load_lds_dwordx4 v[196:197], off
	v_lshl_add_u64 v[196:197], s[20:21], 0, v[134:135]
	s_mov_b32 m0, s39
	s_nop 0
	global_load_lds_dwordx4 v[196:197], off
	v_lshl_add_u64 v[196:197], s[20:21], 0, v[136:137]
	s_mov_b32 m0, s40
	s_nop 0
	global_load_lds_dwordx4 v[196:197], off
	s_waitcnt vmcnt(8)
	s_waitcnt lgkmcnt(0)
	s_barrier
	s_waitcnt lgkmcnt(0)
	v_mfma_f32_16x16x32_bf16 v[62:65], v[146:149], v[200:203], v[62:65]
	v_mfma_f32_16x16x32_bf16 v[58:61], v[172:175], v[200:203], v[58:61]
	v_mfma_f32_16x16x32_bf16 v[46:49], v[146:149], v[204:207], v[46:49]
	v_mfma_f32_16x16x32_bf16 v[42:45], v[172:175], v[204:207], v[42:45]
	v_mfma_f32_16x16x32_bf16 v[30:33], v[146:149], v[216:219], v[30:33]
	v_mfma_f32_16x16x32_bf16 v[26:29], v[172:175], v[216:219], v[26:29]
	v_mfma_f32_16x16x32_bf16 v[14:17], v[146:149], v[220:223], v[14:17]
	v_mfma_f32_16x16x32_bf16 v[10:13], v[172:175], v[220:223], v[10:13]
	v_mfma_f32_16x16x32_bf16 v[62:65], v[168:171], v[208:211], v[62:65]
	v_mfma_f32_16x16x32_bf16 v[58:61], v[176:179], v[208:211], v[58:61]
	v_mfma_f32_16x16x32_bf16 v[46:49], v[168:171], v[212:215], v[46:49]
	v_mfma_f32_16x16x32_bf16 v[42:45], v[176:179], v[212:215], v[42:45]
	v_mfma_f32_16x16x32_bf16 v[30:33], v[168:171], v[224:227], v[30:33]
	v_mfma_f32_16x16x32_bf16 v[26:29], v[176:179], v[224:227], v[26:29]
	v_mfma_f32_16x16x32_bf16 v[14:17], v[168:171], v[228:231], v[14:17]
	v_mfma_f32_16x16x32_bf16 v[10:13], v[176:179], v[228:231], v[10:13]
	v_mfma_f32_16x16x32_bf16 v[54:57], v[180:183], v[200:203], v[54:57]
	v_mfma_f32_16x16x32_bf16 v[50:53], v[188:191], v[200:203], v[50:53]
	v_mfma_f32_16x16x32_bf16 v[38:41], v[180:183], v[204:207], v[38:41]
	v_mfma_f32_16x16x32_bf16 v[34:37], v[188:191], v[204:207], v[34:37]
	v_mfma_f32_16x16x32_bf16 v[22:25], v[180:183], v[216:219], v[22:25]
	v_mfma_f32_16x16x32_bf16 v[18:21], v[188:191], v[216:219], v[18:21]
	v_mfma_f32_16x16x32_bf16 v[6:9], v[180:183], v[220:223], v[6:9]
	v_mfma_f32_16x16x32_bf16 v[2:5], v[188:191], v[220:223], v[2:5]
	v_mfma_f32_16x16x32_bf16 v[54:57], v[184:187], v[208:211], v[54:57]
	v_mfma_f32_16x16x32_bf16 v[50:53], v[192:195], v[208:211], v[50:53]
	v_mfma_f32_16x16x32_bf16 v[38:41], v[184:187], v[212:215], v[38:41]
	v_mfma_f32_16x16x32_bf16 v[34:37], v[192:195], v[212:215], v[34:37]
	v_mfma_f32_16x16x32_bf16 v[22:25], v[184:187], v[224:227], v[22:25]
	v_mfma_f32_16x16x32_bf16 v[18:21], v[192:195], v[224:227], v[18:21]
	v_mfma_f32_16x16x32_bf16 v[6:9], v[184:187], v[228:231], v[6:9]
	v_mfma_f32_16x16x32_bf16 v[2:5], v[192:195], v[228:231], v[2:5]
	s_barrier
	s_add_i32 s56, s56, 2
	s_add_u32 s18, s18, 0x8000
	s_addc_u32 s19, s19, 0
	s_add_u32 s54, s54, 0x8000
	s_addc_u32 s55, s55, 0
	s_cmp_gt_u32 s56, 41
	s_cbranch_scc0 .LBB0_2411
	s_and_b64 vcc, exec, s[4:5]
	s_cbranch_vccz .LBB0_2414
	s_barrier
